# router phase: per-token finish vectorised across lanes via LDS scratch
# speedup vs baseline: 1.0090x; 1.0090x over previous
; #define LAS __attribute__((address_space(3)))
; __global__ void __launch_bounds__(NTHR, 2) fwd_kernel(Args args) {
;     ...
;         for (int c = wg; c < T / 64; c += G) {
;             if (tid < 8) lcnt[tid] = 0;
;             __syncthreads();
;             const int t0 = c * 64 + wave * 8;
;             float acc[8][8], ssq[8];
; #pragma unroll
;             for (int q = 0; q < 8; ++q) { ssq[q] = 0.f;
; #pragma unroll
;                 for (int e = 0; e < 8; ++e) acc[q][e] = 0.f; }
; #pragma unroll 2
;             for (int i = 0; i < 16; ++i) { const int k = 2 * lane + 128 * i; f32x2 rv[8]; unsigned xw[8];
; #pragma unroll
;                 for (int e = 0; e < 8; ++e) rv[e] = *(const LAS f32x2*)(Rg + e * DM + k);
; #pragma unroll
;                 for (int q = 0; q < 8; ++q) xw[q] = *(const unsigned*)(XB + (size_t)(t0 + q) * DM + k);
; #pragma unroll
;                 for (int q = 0; q < 8; ++q) { const float x0 = bflo(xw[q]), x1 = bfhi(xw[q]); ssq[q] += x0 * x0 + x1 * x1;
; #pragma unroll
;                     for (int e = 0; e < 8; ++e) acc[q][e] += x0 * rv[e].x + x1 * rv[e].y; } }
.Lr14_chunk:
	s_waitcnt vmcnt(0)
	v_cmp_gt_u32_e32 vcc, 8, v211
	s_and_saveexec_b64 s[2:3], vcc
	ds_write_b32 v229, v220
	s_mov_b64 exec, s[2:3]
	s_lshl_b32 s13, s12, 6
	s_add_i32 s13, s13, s33
	s_lshl_b32 s14, s13, 12
	s_add_u32 s40, s10, s14
	s_addc_u32 s41, s11, 0
	s_add_u32 s42, s40, 0x1000
	s_addc_u32 s43, s41, 0
	s_add_u32 s44, s42, 0x1000
	s_addc_u32 s45, s43, 0
	s_add_u32 s46, s44, 0x1000
	s_addc_u32 s47, s45, 0
	s_add_u32 s48, s46, 0x1000
	s_addc_u32 s49, s47, 0
	s_add_u32 s50, s48, 0x1000
	s_addc_u32 s51, s49, 0
	s_add_u32 s52, s50, 0x1000
	s_addc_u32 s53, s51, 0
	s_add_u32 s54, s52, 0x1000
	s_addc_u32 s55, s53, 0
	global_load_dwordx4 v[64:67], v208, s[40:41] offset:0
	global_load_dwordx4 v[68:71], v208, s[42:43] offset:0
	global_load_dwordx4 v[72:75], v208, s[44:45] offset:0
	global_load_dwordx4 v[76:79], v208, s[46:47] offset:0
	global_load_dwordx4 v[80:83], v208, s[48:49] offset:0
	global_load_dwordx4 v[84:87], v208, s[50:51] offset:0
	global_load_dwordx4 v[88:91], v208, s[52:53] offset:0
	global_load_dwordx4 v[92:95], v208, s[54:55] offset:0
	global_load_dwordx4 v[96:99], v208, s[40:41] offset:1024
	global_load_dwordx4 v[100:103], v208, s[42:43] offset:1024
	global_load_dwordx4 v[104:107], v208, s[44:45] offset:1024
	global_load_dwordx4 v[108:111], v208, s[46:47] offset:1024
	global_load_dwordx4 v[112:115], v208, s[48:49] offset:1024
	global_load_dwordx4 v[116:119], v208, s[50:51] offset:1024
	global_load_dwordx4 v[120:123], v208, s[52:53] offset:1024
	global_load_dwordx4 v[124:127], v208, s[54:55] offset:1024
	v_mov_b64_e32 v[0:1], 0
	v_mov_b64_e32 v[2:3], 0
	v_mov_b64_e32 v[4:5], 0
	v_mov_b64_e32 v[6:7], 0
	v_mov_b64_e32 v[8:9], 0
	v_mov_b64_e32 v[10:11], 0
	v_mov_b64_e32 v[12:13], 0
	v_mov_b64_e32 v[14:15], 0
	v_mov_b64_e32 v[16:17], 0
	v_mov_b64_e32 v[18:19], 0
	v_mov_b64_e32 v[20:21], 0
	v_mov_b64_e32 v[22:23], 0
	v_mov_b64_e32 v[24:25], 0
	v_mov_b64_e32 v[26:27], 0
	v_mov_b64_e32 v[28:29], 0
	v_mov_b64_e32 v[30:31], 0
	v_mov_b64_e32 v[32:33], 0
	v_mov_b64_e32 v[34:35], 0
	v_mov_b64_e32 v[36:37], 0
	v_mov_b64_e32 v[38:39], 0
	v_mov_b64_e32 v[40:41], 0
	v_mov_b64_e32 v[42:43], 0
	v_mov_b64_e32 v[44:45], 0
	v_mov_b64_e32 v[46:47], 0
	v_mov_b64_e32 v[48:49], 0
	v_mov_b64_e32 v[50:51], 0
	v_mov_b64_e32 v[52:53], 0
	v_mov_b64_e32 v[54:55], 0
	v_mov_b64_e32 v[56:57], 0
	v_mov_b64_e32 v[58:59], 0
	v_mov_b64_e32 v[60:61], 0
	v_mov_b64_e32 v[62:63], 0
	v_mov_b64_e32 v[192:193], 0
	v_mov_b64_e32 v[194:195], 0
	v_mov_b64_e32 v[196:197], 0
	v_mov_b64_e32 v[198:199], 0
	v_mov_b64_e32 v[200:201], 0
	v_mov_b64_e32 v[202:203], 0
	v_mov_b64_e32 v[204:205], 0
	v_mov_b64_e32 v[206:207], 0
	s_waitcnt lgkmcnt(0)
	s_barrier
	ds_read_b128 v[128:131], v208 offset:0
	ds_read_b128 v[132:135], v208 offset:1024
	ds_read_b128 v[136:139], v208 offset:2048
	ds_read_b128 v[140:143], v208 offset:3072
	ds_read_b128 v[144:147], v208 offset:4096
	ds_read_b128 v[148:151], v208 offset:5120
	ds_read_b128 v[152:155], v208 offset:6144
	ds_read_b128 v[156:159], v208 offset:7168
	ds_read_b128 v[160:163], v208 offset:8192
	ds_read_b128 v[164:167], v208 offset:9216
	ds_read_b128 v[168:171], v208 offset:10240
	ds_read_b128 v[172:175], v208 offset:11264
	ds_read_b128 v[176:179], v208 offset:12288
	ds_read_b128 v[180:183], v208 offset:13312
	ds_read_b128 v[184:187], v208 offset:14336
	ds_read_b128 v[188:191], v208 offset:15360
	s_waitcnt vmcnt(8)
	s_waitcnt lgkmcnt(0)
	v_lshlrev_b32_e32 v232, 16, v64
	v_and_b32_e32 v233, s15, v64
	v_lshlrev_b32_e32 v234, 16, v65
	v_and_b32_e32 v235, s15, v65
	v_lshlrev_b32_e32 v236, 16, v66
	v_and_b32_e32 v237, s15, v66
	v_lshlrev_b32_e32 v238, 16, v67
	v_and_b32_e32 v239, s15, v67
	v_pk_fma_f32 v[192:193], v[232:233], v[232:233], v[192:193]
	v_pk_fma_f32 v[192:193], v[234:235], v[234:235], v[192:193]
	v_pk_fma_f32 v[192:193], v[236:237], v[236:237], v[192:193]
	v_pk_fma_f32 v[192:193], v[238:239], v[238:239], v[192:193]
	v_pk_fma_f32 v[0:1], v[232:233], v[128:129], v[0:1] op_sel_hi:[0,1,1]
	v_pk_fma_f32 v[2:3], v[232:233], v[130:131], v[2:3] op_sel_hi:[0,1,1]
	v_pk_fma_f32 v[4:5], v[232:233], v[132:133], v[4:5] op_sel_hi:[0,1,1]
	v_pk_fma_f32 v[6:7], v[232:233], v[134:135], v[6:7] op_sel_hi:[0,1,1]
	v_pk_fma_f32 v[0:1], v[232:233], v[136:137], v[0:1] op_sel:[1,0,0] op_sel_hi:[1,1,1]
	v_pk_fma_f32 v[2:3], v[232:233], v[138:139], v[2:3] op_sel:[1,0,0] op_sel_hi:[1,1,1]
	v_pk_fma_f32 v[4:5], v[232:233], v[140:141], v[4:5] op_sel:[1,0,0] op_sel_hi:[1,1,1]
	v_pk_fma_f32 v[6:7], v[232:233], v[142:143], v[6:7] op_sel:[1,0,0] op_sel_hi:[1,1,1]
	v_pk_fma_f32 v[0:1], v[234:235], v[144:145], v[0:1] op_sel_hi:[0,1,1]
	v_pk_fma_f32 v[2:3], v[234:235], v[146:147], v[2:3] op_sel_hi:[0,1,1]
	v_pk_fma_f32 v[4:5], v[234:235], v[148:149], v[4:5] op_sel_hi:[0,1,1]
	v_pk_fma_f32 v[6:7], v[234:235], v[150:151], v[6:7] op_sel_hi:[0,1,1]
	v_pk_fma_f32 v[0:1], v[234:235], v[152:153], v[0:1] op_sel:[1,0,0] op_sel_hi:[1,1,1]
	v_pk_fma_f32 v[2:3], v[234:235], v[154:155], v[2:3] op_sel:[1,0,0] op_sel_hi:[1,1,1]
	v_pk_fma_f32 v[4:5], v[234:235], v[156:157], v[4:5] op_sel:[1,0,0] op_sel_hi:[1,1,1]
	v_pk_fma_f32 v[6:7], v[234:235], v[158:159], v[6:7] op_sel:[1,0,0] op_sel_hi:[1,1,1]
	v_pk_fma_f32 v[0:1], v[236:237], v[160:161], v[0:1] op_sel_hi:[0,1,1]
	v_pk_fma_f32 v[2:3], v[236:237], v[162:163], v[2:3] op_sel_hi:[0,1,1]
	v_pk_fma_f32 v[4:5], v[236:237], v[164:165], v[4:5] op_sel_hi:[0,1,1]
	v_pk_fma_f32 v[6:7], v[236:237], v[166:167], v[6:7] op_sel_hi:[0,1,1]
	v_pk_fma_f32 v[0:1], v[236:237], v[168:169], v[0:1] op_sel:[1,0,0] op_sel_hi:[1,1,1]
	v_pk_fma_f32 v[2:3], v[236:237], v[170:171], v[2:3] op_sel:[1,0,0] op_sel_hi:[1,1,1]
; #define LAS __attribute__((address_space(3)))
; __global__ void __launch_bounds__(NTHR, 2) fwd_kernel(Args args) {
;     ...
;             for (int i = 0; i < 16; ++i) { const int k = 2 * lane + 128 * i; f32x2 rv[8]; unsigned xw[8];
; #pragma unroll
;                 for (int e = 0; e < 8; ++e) rv[e] = *(const LAS f32x2*)(Rg + e * DM + k);
; #pragma unroll
;                 for (int q = 0; q < 8; ++q) xw[q] = *(const unsigned*)(XB + (size_t)(t0 + q) * DM + k);
; #pragma unroll
;                 for (int q = 0; q < 8; ++q) { const float x0 = bflo(xw[q]), x1 = bfhi(xw[q]); ssq[q] += x0 * x0 + x1 * x1;
; #pragma unroll
;                     for (int e = 0; e < 8; ++e) acc[q][e] += x0 * rv[e].x + x1 * rv[e].y; } }
	v_pk_fma_f32 v[4:5], v[236:237], v[172:173], v[4:5] op_sel:[1,0,0] op_sel_hi:[1,1,1]
	v_pk_fma_f32 v[6:7], v[236:237], v[174:175], v[6:7] op_sel:[1,0,0] op_sel_hi:[1,1,1]
	v_pk_fma_f32 v[0:1], v[238:239], v[176:177], v[0:1] op_sel_hi:[0,1,1]
	v_pk_fma_f32 v[2:3], v[238:239], v[178:179], v[2:3] op_sel_hi:[0,1,1]
	v_pk_fma_f32 v[4:5], v[238:239], v[180:181], v[4:5] op_sel_hi:[0,1,1]
	v_pk_fma_f32 v[6:7], v[238:239], v[182:183], v[6:7] op_sel_hi:[0,1,1]
	v_pk_fma_f32 v[0:1], v[238:239], v[184:185], v[0:1] op_sel:[1,0,0] op_sel_hi:[1,1,1]
	v_pk_fma_f32 v[2:3], v[238:239], v[186:187], v[2:3] op_sel:[1,0,0] op_sel_hi:[1,1,1]
	v_pk_fma_f32 v[4:5], v[238:239], v[188:189], v[4:5] op_sel:[1,0,0] op_sel_hi:[1,1,1]
	v_pk_fma_f32 v[6:7], v[238:239], v[190:191], v[6:7] op_sel:[1,0,0] op_sel_hi:[1,1,1]
	v_lshlrev_b32_e32 v232, 16, v68
	v_and_b32_e32 v233, s15, v68
	v_lshlrev_b32_e32 v234, 16, v69
	v_and_b32_e32 v235, s15, v69
	v_lshlrev_b32_e32 v236, 16, v70
	v_and_b32_e32 v237, s15, v70
	v_lshlrev_b32_e32 v238, 16, v71
	v_and_b32_e32 v239, s15, v71
	v_pk_fma_f32 v[194:195], v[232:233], v[232:233], v[194:195]
	v_pk_fma_f32 v[194:195], v[234:235], v[234:235], v[194:195]
	v_pk_fma_f32 v[194:195], v[236:237], v[236:237], v[194:195]
	v_pk_fma_f32 v[194:195], v[238:239], v[238:239], v[194:195]
	v_pk_fma_f32 v[8:9], v[232:233], v[128:129], v[8:9] op_sel_hi:[0,1,1]
	v_pk_fma_f32 v[10:11], v[232:233], v[130:131], v[10:11] op_sel_hi:[0,1,1]
	v_pk_fma_f32 v[12:13], v[232:233], v[132:133], v[12:13] op_sel_hi:[0,1,1]
	v_pk_fma_f32 v[14:15], v[232:233], v[134:135], v[14:15] op_sel_hi:[0,1,1]
	v_pk_fma_f32 v[8:9], v[232:233], v[136:137], v[8:9] op_sel:[1,0,0] op_sel_hi:[1,1,1]
	v_pk_fma_f32 v[10:11], v[232:233], v[138:139], v[10:11] op_sel:[1,0,0] op_sel_hi:[1,1,1]
	v_pk_fma_f32 v[12:13], v[232:233], v[140:141], v[12:13] op_sel:[1,0,0] op_sel_hi:[1,1,1]
	v_pk_fma_f32 v[14:15], v[232:233], v[142:143], v[14:15] op_sel:[1,0,0] op_sel_hi:[1,1,1]
	v_pk_fma_f32 v[8:9], v[234:235], v[144:145], v[8:9] op_sel_hi:[0,1,1]
	v_pk_fma_f32 v[10:11], v[234:235], v[146:147], v[10:11] op_sel_hi:[0,1,1]
	v_pk_fma_f32 v[12:13], v[234:235], v[148:149], v[12:13] op_sel_hi:[0,1,1]
	v_pk_fma_f32 v[14:15], v[234:235], v[150:151], v[14:15] op_sel_hi:[0,1,1]
	v_pk_fma_f32 v[8:9], v[234:235], v[152:153], v[8:9] op_sel:[1,0,0] op_sel_hi:[1,1,1]
	v_pk_fma_f32 v[10:11], v[234:235], v[154:155], v[10:11] op_sel:[1,0,0] op_sel_hi:[1,1,1]
	v_pk_fma_f32 v[12:13], v[234:235], v[156:157], v[12:13] op_sel:[1,0,0] op_sel_hi:[1,1,1]
	v_pk_fma_f32 v[14:15], v[234:235], v[158:159], v[14:15] op_sel:[1,0,0] op_sel_hi:[1,1,1]
	v_pk_fma_f32 v[8:9], v[236:237], v[160:161], v[8:9] op_sel_hi:[0,1,1]
	v_pk_fma_f32 v[10:11], v[236:237], v[162:163], v[10:11] op_sel_hi:[0,1,1]
	v_pk_fma_f32 v[12:13], v[236:237], v[164:165], v[12:13] op_sel_hi:[0,1,1]
	v_pk_fma_f32 v[14:15], v[236:237], v[166:167], v[14:15] op_sel_hi:[0,1,1]
	v_pk_fma_f32 v[8:9], v[236:237], v[168:169], v[8:9] op_sel:[1,0,0] op_sel_hi:[1,1,1]
	v_pk_fma_f32 v[10:11], v[236:237], v[170:171], v[10:11] op_sel:[1,0,0] op_sel_hi:[1,1,1]
	v_pk_fma_f32 v[12:13], v[236:237], v[172:173], v[12:13] op_sel:[1,0,0] op_sel_hi:[1,1,1]
	v_pk_fma_f32 v[14:15], v[236:237], v[174:175], v[14:15] op_sel:[1,0,0] op_sel_hi:[1,1,1]
	v_pk_fma_f32 v[8:9], v[238:239], v[176:177], v[8:9] op_sel_hi:[0,1,1]
	v_pk_fma_f32 v[10:11], v[238:239], v[178:179], v[10:11] op_sel_hi:[0,1,1]
	v_pk_fma_f32 v[12:13], v[238:239], v[180:181], v[12:13] op_sel_hi:[0,1,1]
	v_pk_fma_f32 v[14:15], v[238:239], v[182:183], v[14:15] op_sel_hi:[0,1,1]
	v_pk_fma_f32 v[8:9], v[238:239], v[184:185], v[8:9] op_sel:[1,0,0] op_sel_hi:[1,1,1]
	v_pk_fma_f32 v[10:11], v[238:239], v[186:187], v[10:11] op_sel:[1,0,0] op_sel_hi:[1,1,1]
	v_pk_fma_f32 v[12:13], v[238:239], v[188:189], v[12:13] op_sel:[1,0,0] op_sel_hi:[1,1,1]
	v_pk_fma_f32 v[14:15], v[238:239], v[190:191], v[14:15] op_sel:[1,0,0] op_sel_hi:[1,1,1]
	v_lshlrev_b32_e32 v232, 16, v72
	v_and_b32_e32 v233, s15, v72
	v_lshlrev_b32_e32 v234, 16, v73
	v_and_b32_e32 v235, s15, v73
	v_lshlrev_b32_e32 v236, 16, v74
	v_and_b32_e32 v237, s15, v74
	v_lshlrev_b32_e32 v238, 16, v75
	v_and_b32_e32 v239, s15, v75
	v_pk_fma_f32 v[196:197], v[232:233], v[232:233], v[196:197]
	v_pk_fma_f32 v[196:197], v[234:235], v[234:235], v[196:197]
	v_pk_fma_f32 v[196:197], v[236:237], v[236:237], v[196:197]
	v_pk_fma_f32 v[196:197], v[238:239], v[238:239], v[196:197]
	v_pk_fma_f32 v[16:17], v[232:233], v[128:129], v[16:17] op_sel_hi:[0,1,1]
	v_pk_fma_f32 v[18:19], v[232:233], v[130:131], v[18:19] op_sel_hi:[0,1,1]
	v_pk_fma_f32 v[20:21], v[232:233], v[132:133], v[20:21] op_sel_hi:[0,1,1]
	v_pk_fma_f32 v[22:23], v[232:233], v[134:135], v[22:23] op_sel_hi:[0,1,1]
	v_pk_fma_f32 v[16:17], v[232:233], v[136:137], v[16:17] op_sel:[1,0,0] op_sel_hi:[1,1,1]
	v_pk_fma_f32 v[18:19], v[232:233], v[138:139], v[18:19] op_sel:[1,0,0] op_sel_hi:[1,1,1]
	v_pk_fma_f32 v[20:21], v[232:233], v[140:141], v[20:21] op_sel:[1,0,0] op_sel_hi:[1,1,1]
	v_pk_fma_f32 v[22:23], v[232:233], v[142:143], v[22:23] op_sel:[1,0,0] op_sel_hi:[1,1,1]
	v_pk_fma_f32 v[16:17], v[234:235], v[144:145], v[16:17] op_sel_hi:[0,1,1]
	v_pk_fma_f32 v[18:19], v[234:235], v[146:147], v[18:19] op_sel_hi:[0,1,1]
	v_pk_fma_f32 v[20:21], v[234:235], v[148:149], v[20:21] op_sel_hi:[0,1,1]
	v_pk_fma_f32 v[22:23], v[234:235], v[150:151], v[22:23] op_sel_hi:[0,1,1]
	v_pk_fma_f32 v[16:17], v[234:235], v[152:153], v[16:17] op_sel:[1,0,0] op_sel_hi:[1,1,1]
	v_pk_fma_f32 v[18:19], v[234:235], v[154:155], v[18:19] op_sel:[1,0,0] op_sel_hi:[1,1,1]
	v_pk_fma_f32 v[20:21], v[234:235], v[156:157], v[20:21] op_sel:[1,0,0] op_sel_hi:[1,1,1]
; #define LAS __attribute__((address_space(3)))
; __global__ void __launch_bounds__(NTHR, 2) fwd_kernel(Args args) {
;     ...
;             for (int i = 0; i < 16; ++i) { const int k = 2 * lane + 128 * i; f32x2 rv[8]; unsigned xw[8];
; #pragma unroll
;                 for (int e = 0; e < 8; ++e) rv[e] = *(const LAS f32x2*)(Rg + e * DM + k);
; #pragma unroll
;                 for (int q = 0; q < 8; ++q) xw[q] = *(const unsigned*)(XB + (size_t)(t0 + q) * DM + k);
; #pragma unroll
;                 for (int q = 0; q < 8; ++q) { const float x0 = bflo(xw[q]), x1 = bfhi(xw[q]); ssq[q] += x0 * x0 + x1 * x1;
; #pragma unroll
;                     for (int e = 0; e < 8; ++e) acc[q][e] += x0 * rv[e].x + x1 * rv[e].y; } }
	v_pk_fma_f32 v[22:23], v[234:235], v[158:159], v[22:23] op_sel:[1,0,0] op_sel_hi:[1,1,1]
	v_pk_fma_f32 v[16:17], v[236:237], v[160:161], v[16:17] op_sel_hi:[0,1,1]
	v_pk_fma_f32 v[18:19], v[236:237], v[162:163], v[18:19] op_sel_hi:[0,1,1]
	v_pk_fma_f32 v[20:21], v[236:237], v[164:165], v[20:21] op_sel_hi:[0,1,1]
	v_pk_fma_f32 v[22:23], v[236:237], v[166:167], v[22:23] op_sel_hi:[0,1,1]
	v_pk_fma_f32 v[16:17], v[236:237], v[168:169], v[16:17] op_sel:[1,0,0] op_sel_hi:[1,1,1]
	v_pk_fma_f32 v[18:19], v[236:237], v[170:171], v[18:19] op_sel:[1,0,0] op_sel_hi:[1,1,1]
	v_pk_fma_f32 v[20:21], v[236:237], v[172:173], v[20:21] op_sel:[1,0,0] op_sel_hi:[1,1,1]
	v_pk_fma_f32 v[22:23], v[236:237], v[174:175], v[22:23] op_sel:[1,0,0] op_sel_hi:[1,1,1]
	v_pk_fma_f32 v[16:17], v[238:239], v[176:177], v[16:17] op_sel_hi:[0,1,1]
	v_pk_fma_f32 v[18:19], v[238:239], v[178:179], v[18:19] op_sel_hi:[0,1,1]
	v_pk_fma_f32 v[20:21], v[238:239], v[180:181], v[20:21] op_sel_hi:[0,1,1]
	v_pk_fma_f32 v[22:23], v[238:239], v[182:183], v[22:23] op_sel_hi:[0,1,1]
	v_pk_fma_f32 v[16:17], v[238:239], v[184:185], v[16:17] op_sel:[1,0,0] op_sel_hi:[1,1,1]
	v_pk_fma_f32 v[18:19], v[238:239], v[186:187], v[18:19] op_sel:[1,0,0] op_sel_hi:[1,1,1]
	v_pk_fma_f32 v[20:21], v[238:239], v[188:189], v[20:21] op_sel:[1,0,0] op_sel_hi:[1,1,1]
	v_pk_fma_f32 v[22:23], v[238:239], v[190:191], v[22:23] op_sel:[1,0,0] op_sel_hi:[1,1,1]
	v_lshlrev_b32_e32 v232, 16, v76
	v_and_b32_e32 v233, s15, v76
	v_lshlrev_b32_e32 v234, 16, v77
	v_and_b32_e32 v235, s15, v77
	v_lshlrev_b32_e32 v236, 16, v78
	v_and_b32_e32 v237, s15, v78
	v_lshlrev_b32_e32 v238, 16, v79
	v_and_b32_e32 v239, s15, v79
	v_pk_fma_f32 v[198:199], v[232:233], v[232:233], v[198:199]
	v_pk_fma_f32 v[198:199], v[234:235], v[234:235], v[198:199]
	v_pk_fma_f32 v[198:199], v[236:237], v[236:237], v[198:199]
	v_pk_fma_f32 v[198:199], v[238:239], v[238:239], v[198:199]
	v_pk_fma_f32 v[24:25], v[232:233], v[128:129], v[24:25] op_sel_hi:[0,1,1]
	v_pk_fma_f32 v[26:27], v[232:233], v[130:131], v[26:27] op_sel_hi:[0,1,1]
	v_pk_fma_f32 v[28:29], v[232:233], v[132:133], v[28:29] op_sel_hi:[0,1,1]
	v_pk_fma_f32 v[30:31], v[232:233], v[134:135], v[30:31] op_sel_hi:[0,1,1]
	v_pk_fma_f32 v[24:25], v[232:233], v[136:137], v[24:25] op_sel:[1,0,0] op_sel_hi:[1,1,1]
	v_pk_fma_f32 v[26:27], v[232:233], v[138:139], v[26:27] op_sel:[1,0,0] op_sel_hi:[1,1,1]
	v_pk_fma_f32 v[28:29], v[232:233], v[140:141], v[28:29] op_sel:[1,0,0] op_sel_hi:[1,1,1]
	v_pk_fma_f32 v[30:31], v[232:233], v[142:143], v[30:31] op_sel:[1,0,0] op_sel_hi:[1,1,1]
	v_pk_fma_f32 v[24:25], v[234:235], v[144:145], v[24:25] op_sel_hi:[0,1,1]
	v_pk_fma_f32 v[26:27], v[234:235], v[146:147], v[26:27] op_sel_hi:[0,1,1]
	v_pk_fma_f32 v[28:29], v[234:235], v[148:149], v[28:29] op_sel_hi:[0,1,1]
	v_pk_fma_f32 v[30:31], v[234:235], v[150:151], v[30:31] op_sel_hi:[0,1,1]
	v_pk_fma_f32 v[24:25], v[234:235], v[152:153], v[24:25] op_sel:[1,0,0] op_sel_hi:[1,1,1]
	v_pk_fma_f32 v[26:27], v[234:235], v[154:155], v[26:27] op_sel:[1,0,0] op_sel_hi:[1,1,1]
	v_pk_fma_f32 v[28:29], v[234:235], v[156:157], v[28:29] op_sel:[1,0,0] op_sel_hi:[1,1,1]
	v_pk_fma_f32 v[30:31], v[234:235], v[158:159], v[30:31] op_sel:[1,0,0] op_sel_hi:[1,1,1]
	v_pk_fma_f32 v[24:25], v[236:237], v[160:161], v[24:25] op_sel_hi:[0,1,1]
	v_pk_fma_f32 v[26:27], v[236:237], v[162:163], v[26:27] op_sel_hi:[0,1,1]
	v_pk_fma_f32 v[28:29], v[236:237], v[164:165], v[28:29] op_sel_hi:[0,1,1]
	v_pk_fma_f32 v[30:31], v[236:237], v[166:167], v[30:31] op_sel_hi:[0,1,1]
	v_pk_fma_f32 v[24:25], v[236:237], v[168:169], v[24:25] op_sel:[1,0,0] op_sel_hi:[1,1,1]
	v_pk_fma_f32 v[26:27], v[236:237], v[170:171], v[26:27] op_sel:[1,0,0] op_sel_hi:[1,1,1]
	v_pk_fma_f32 v[28:29], v[236:237], v[172:173], v[28:29] op_sel:[1,0,0] op_sel_hi:[1,1,1]
	v_pk_fma_f32 v[30:31], v[236:237], v[174:175], v[30:31] op_sel:[1,0,0] op_sel_hi:[1,1,1]
	v_pk_fma_f32 v[24:25], v[238:239], v[176:177], v[24:25] op_sel_hi:[0,1,1]
	v_pk_fma_f32 v[26:27], v[238:239], v[178:179], v[26:27] op_sel_hi:[0,1,1]
	v_pk_fma_f32 v[28:29], v[238:239], v[180:181], v[28:29] op_sel_hi:[0,1,1]
	v_pk_fma_f32 v[30:31], v[238:239], v[182:183], v[30:31] op_sel_hi:[0,1,1]
	v_pk_fma_f32 v[24:25], v[238:239], v[184:185], v[24:25] op_sel:[1,0,0] op_sel_hi:[1,1,1]
	v_pk_fma_f32 v[26:27], v[238:239], v[186:187], v[26:27] op_sel:[1,0,0] op_sel_hi:[1,1,1]
	v_pk_fma_f32 v[28:29], v[238:239], v[188:189], v[28:29] op_sel:[1,0,0] op_sel_hi:[1,1,1]
	v_pk_fma_f32 v[30:31], v[238:239], v[190:191], v[30:31] op_sel:[1,0,0] op_sel_hi:[1,1,1]
	v_lshlrev_b32_e32 v232, 16, v80
	v_and_b32_e32 v233, s15, v80
	v_lshlrev_b32_e32 v234, 16, v81
	v_and_b32_e32 v235, s15, v81
	v_lshlrev_b32_e32 v236, 16, v82
	v_and_b32_e32 v237, s15, v82
	v_lshlrev_b32_e32 v238, 16, v83
	v_and_b32_e32 v239, s15, v83
	v_pk_fma_f32 v[200:201], v[232:233], v[232:233], v[200:201]
	v_pk_fma_f32 v[200:201], v[234:235], v[234:235], v[200:201]
	v_pk_fma_f32 v[200:201], v[236:237], v[236:237], v[200:201]
	v_pk_fma_f32 v[200:201], v[238:239], v[238:239], v[200:201]
	v_pk_fma_f32 v[32:33], v[232:233], v[128:129], v[32:33] op_sel_hi:[0,1,1]
	v_pk_fma_f32 v[34:35], v[232:233], v[130:131], v[34:35] op_sel_hi:[0,1,1]
	v_pk_fma_f32 v[36:37], v[232:233], v[132:133], v[36:37] op_sel_hi:[0,1,1]
	v_pk_fma_f32 v[38:39], v[232:233], v[134:135], v[38:39] op_sel_hi:[0,1,1]
	v_pk_fma_f32 v[32:33], v[232:233], v[136:137], v[32:33] op_sel:[1,0,0] op_sel_hi:[1,1,1]
	v_pk_fma_f32 v[34:35], v[232:233], v[138:139], v[34:35] op_sel:[1,0,0] op_sel_hi:[1,1,1]
	v_pk_fma_f32 v[36:37], v[232:233], v[140:141], v[36:37] op_sel:[1,0,0] op_sel_hi:[1,1,1]
; #define LAS __attribute__((address_space(3)))
; __global__ void __launch_bounds__(NTHR, 2) fwd_kernel(Args args) {
;     ...
;             for (int i = 0; i < 16; ++i) { const int k = 2 * lane + 128 * i; f32x2 rv[8]; unsigned xw[8];
; #pragma unroll
;                 for (int e = 0; e < 8; ++e) rv[e] = *(const LAS f32x2*)(Rg + e * DM + k);
; #pragma unroll
;                 for (int q = 0; q < 8; ++q) xw[q] = *(const unsigned*)(XB + (size_t)(t0 + q) * DM + k);
; #pragma unroll
;                 for (int q = 0; q < 8; ++q) { const float x0 = bflo(xw[q]), x1 = bfhi(xw[q]); ssq[q] += x0 * x0 + x1 * x1;
; #pragma unroll
;                     for (int e = 0; e < 8; ++e) acc[q][e] += x0 * rv[e].x + x1 * rv[e].y; } }
	v_pk_fma_f32 v[38:39], v[232:233], v[142:143], v[38:39] op_sel:[1,0,0] op_sel_hi:[1,1,1]
	v_pk_fma_f32 v[32:33], v[234:235], v[144:145], v[32:33] op_sel_hi:[0,1,1]
	v_pk_fma_f32 v[34:35], v[234:235], v[146:147], v[34:35] op_sel_hi:[0,1,1]
	v_pk_fma_f32 v[36:37], v[234:235], v[148:149], v[36:37] op_sel_hi:[0,1,1]
	v_pk_fma_f32 v[38:39], v[234:235], v[150:151], v[38:39] op_sel_hi:[0,1,1]
	v_pk_fma_f32 v[32:33], v[234:235], v[152:153], v[32:33] op_sel:[1,0,0] op_sel_hi:[1,1,1]
	v_pk_fma_f32 v[34:35], v[234:235], v[154:155], v[34:35] op_sel:[1,0,0] op_sel_hi:[1,1,1]
	v_pk_fma_f32 v[36:37], v[234:235], v[156:157], v[36:37] op_sel:[1,0,0] op_sel_hi:[1,1,1]
	v_pk_fma_f32 v[38:39], v[234:235], v[158:159], v[38:39] op_sel:[1,0,0] op_sel_hi:[1,1,1]
	v_pk_fma_f32 v[32:33], v[236:237], v[160:161], v[32:33] op_sel_hi:[0,1,1]
	v_pk_fma_f32 v[34:35], v[236:237], v[162:163], v[34:35] op_sel_hi:[0,1,1]
	v_pk_fma_f32 v[36:37], v[236:237], v[164:165], v[36:37] op_sel_hi:[0,1,1]
	v_pk_fma_f32 v[38:39], v[236:237], v[166:167], v[38:39] op_sel_hi:[0,1,1]
	v_pk_fma_f32 v[32:33], v[236:237], v[168:169], v[32:33] op_sel:[1,0,0] op_sel_hi:[1,1,1]
	v_pk_fma_f32 v[34:35], v[236:237], v[170:171], v[34:35] op_sel:[1,0,0] op_sel_hi:[1,1,1]
	v_pk_fma_f32 v[36:37], v[236:237], v[172:173], v[36:37] op_sel:[1,0,0] op_sel_hi:[1,1,1]
	v_pk_fma_f32 v[38:39], v[236:237], v[174:175], v[38:39] op_sel:[1,0,0] op_sel_hi:[1,1,1]
	v_pk_fma_f32 v[32:33], v[238:239], v[176:177], v[32:33] op_sel_hi:[0,1,1]
	v_pk_fma_f32 v[34:35], v[238:239], v[178:179], v[34:35] op_sel_hi:[0,1,1]
	v_pk_fma_f32 v[36:37], v[238:239], v[180:181], v[36:37] op_sel_hi:[0,1,1]
	v_pk_fma_f32 v[38:39], v[238:239], v[182:183], v[38:39] op_sel_hi:[0,1,1]
	v_pk_fma_f32 v[32:33], v[238:239], v[184:185], v[32:33] op_sel:[1,0,0] op_sel_hi:[1,1,1]
	v_pk_fma_f32 v[34:35], v[238:239], v[186:187], v[34:35] op_sel:[1,0,0] op_sel_hi:[1,1,1]
	v_pk_fma_f32 v[36:37], v[238:239], v[188:189], v[36:37] op_sel:[1,0,0] op_sel_hi:[1,1,1]
	v_pk_fma_f32 v[38:39], v[238:239], v[190:191], v[38:39] op_sel:[1,0,0] op_sel_hi:[1,1,1]
	v_lshlrev_b32_e32 v232, 16, v84
	v_and_b32_e32 v233, s15, v84
	v_lshlrev_b32_e32 v234, 16, v85
	v_and_b32_e32 v235, s15, v85
	v_lshlrev_b32_e32 v236, 16, v86
	v_and_b32_e32 v237, s15, v86
	v_lshlrev_b32_e32 v238, 16, v87
	v_and_b32_e32 v239, s15, v87
	v_pk_fma_f32 v[202:203], v[232:233], v[232:233], v[202:203]
	v_pk_fma_f32 v[202:203], v[234:235], v[234:235], v[202:203]
	v_pk_fma_f32 v[202:203], v[236:237], v[236:237], v[202:203]
	v_pk_fma_f32 v[202:203], v[238:239], v[238:239], v[202:203]
	v_pk_fma_f32 v[40:41], v[232:233], v[128:129], v[40:41] op_sel_hi:[0,1,1]
	v_pk_fma_f32 v[42:43], v[232:233], v[130:131], v[42:43] op_sel_hi:[0,1,1]
	v_pk_fma_f32 v[44:45], v[232:233], v[132:133], v[44:45] op_sel_hi:[0,1,1]
	v_pk_fma_f32 v[46:47], v[232:233], v[134:135], v[46:47] op_sel_hi:[0,1,1]
	v_pk_fma_f32 v[40:41], v[232:233], v[136:137], v[40:41] op_sel:[1,0,0] op_sel_hi:[1,1,1]
	v_pk_fma_f32 v[42:43], v[232:233], v[138:139], v[42:43] op_sel:[1,0,0] op_sel_hi:[1,1,1]
	v_pk_fma_f32 v[44:45], v[232:233], v[140:141], v[44:45] op_sel:[1,0,0] op_sel_hi:[1,1,1]
	v_pk_fma_f32 v[46:47], v[232:233], v[142:143], v[46:47] op_sel:[1,0,0] op_sel_hi:[1,1,1]
	v_pk_fma_f32 v[40:41], v[234:235], v[144:145], v[40:41] op_sel_hi:[0,1,1]
	v_pk_fma_f32 v[42:43], v[234:235], v[146:147], v[42:43] op_sel_hi:[0,1,1]
	v_pk_fma_f32 v[44:45], v[234:235], v[148:149], v[44:45] op_sel_hi:[0,1,1]
	v_pk_fma_f32 v[46:47], v[234:235], v[150:151], v[46:47] op_sel_hi:[0,1,1]
	v_pk_fma_f32 v[40:41], v[234:235], v[152:153], v[40:41] op_sel:[1,0,0] op_sel_hi:[1,1,1]
	v_pk_fma_f32 v[42:43], v[234:235], v[154:155], v[42:43] op_sel:[1,0,0] op_sel_hi:[1,1,1]
	v_pk_fma_f32 v[44:45], v[234:235], v[156:157], v[44:45] op_sel:[1,0,0] op_sel_hi:[1,1,1]
	v_pk_fma_f32 v[46:47], v[234:235], v[158:159], v[46:47] op_sel:[1,0,0] op_sel_hi:[1,1,1]
	v_pk_fma_f32 v[40:41], v[236:237], v[160:161], v[40:41] op_sel_hi:[0,1,1]
	v_pk_fma_f32 v[42:43], v[236:237], v[162:163], v[42:43] op_sel_hi:[0,1,1]
	v_pk_fma_f32 v[44:45], v[236:237], v[164:165], v[44:45] op_sel_hi:[0,1,1]
	v_pk_fma_f32 v[46:47], v[236:237], v[166:167], v[46:47] op_sel_hi:[0,1,1]
	v_pk_fma_f32 v[40:41], v[236:237], v[168:169], v[40:41] op_sel:[1,0,0] op_sel_hi:[1,1,1]
	v_pk_fma_f32 v[42:43], v[236:237], v[170:171], v[42:43] op_sel:[1,0,0] op_sel_hi:[1,1,1]
	v_pk_fma_f32 v[44:45], v[236:237], v[172:173], v[44:45] op_sel:[1,0,0] op_sel_hi:[1,1,1]
	v_pk_fma_f32 v[46:47], v[236:237], v[174:175], v[46:47] op_sel:[1,0,0] op_sel_hi:[1,1,1]
	v_pk_fma_f32 v[40:41], v[238:239], v[176:177], v[40:41] op_sel_hi:[0,1,1]
	v_pk_fma_f32 v[42:43], v[238:239], v[178:179], v[42:43] op_sel_hi:[0,1,1]
	v_pk_fma_f32 v[44:45], v[238:239], v[180:181], v[44:45] op_sel_hi:[0,1,1]
	v_pk_fma_f32 v[46:47], v[238:239], v[182:183], v[46:47] op_sel_hi:[0,1,1]
	v_pk_fma_f32 v[40:41], v[238:239], v[184:185], v[40:41] op_sel:[1,0,0] op_sel_hi:[1,1,1]
	v_pk_fma_f32 v[42:43], v[238:239], v[186:187], v[42:43] op_sel:[1,0,0] op_sel_hi:[1,1,1]
	v_pk_fma_f32 v[44:45], v[238:239], v[188:189], v[44:45] op_sel:[1,0,0] op_sel_hi:[1,1,1]
	v_pk_fma_f32 v[46:47], v[238:239], v[190:191], v[46:47] op_sel:[1,0,0] op_sel_hi:[1,1,1]
	v_lshlrev_b32_e32 v232, 16, v88
	v_and_b32_e32 v233, s15, v88
	v_lshlrev_b32_e32 v234, 16, v89
	v_and_b32_e32 v235, s15, v89
	v_lshlrev_b32_e32 v236, 16, v90
	v_and_b32_e32 v237, s15, v90
	v_lshlrev_b32_e32 v238, 16, v91
	v_and_b32_e32 v239, s15, v91
	v_pk_fma_f32 v[204:205], v[232:233], v[232:233], v[204:205]
	v_pk_fma_f32 v[204:205], v[234:235], v[234:235], v[204:205]
	v_pk_fma_f32 v[204:205], v[236:237], v[236:237], v[204:205]
; #define LAS __attribute__((address_space(3)))
; __global__ void __launch_bounds__(NTHR, 2) fwd_kernel(Args args) {
;     ...
;             for (int i = 0; i < 16; ++i) { const int k = 2 * lane + 128 * i; f32x2 rv[8]; unsigned xw[8];
; #pragma unroll
;                 for (int e = 0; e < 8; ++e) rv[e] = *(const LAS f32x2*)(Rg + e * DM + k);
; #pragma unroll
;                 for (int q = 0; q < 8; ++q) xw[q] = *(const unsigned*)(XB + (size_t)(t0 + q) * DM + k);
; #pragma unroll
;                 for (int q = 0; q < 8; ++q) { const float x0 = bflo(xw[q]), x1 = bfhi(xw[q]); ssq[q] += x0 * x0 + x1 * x1;
; #pragma unroll
;                     for (int e = 0; e < 8; ++e) acc[q][e] += x0 * rv[e].x + x1 * rv[e].y; } }
	v_pk_fma_f32 v[204:205], v[238:239], v[238:239], v[204:205]
	v_pk_fma_f32 v[48:49], v[232:233], v[128:129], v[48:49] op_sel_hi:[0,1,1]
	v_pk_fma_f32 v[50:51], v[232:233], v[130:131], v[50:51] op_sel_hi:[0,1,1]
	v_pk_fma_f32 v[52:53], v[232:233], v[132:133], v[52:53] op_sel_hi:[0,1,1]
	v_pk_fma_f32 v[54:55], v[232:233], v[134:135], v[54:55] op_sel_hi:[0,1,1]
	v_pk_fma_f32 v[48:49], v[232:233], v[136:137], v[48:49] op_sel:[1,0,0] op_sel_hi:[1,1,1]
	v_pk_fma_f32 v[50:51], v[232:233], v[138:139], v[50:51] op_sel:[1,0,0] op_sel_hi:[1,1,1]
	v_pk_fma_f32 v[52:53], v[232:233], v[140:141], v[52:53] op_sel:[1,0,0] op_sel_hi:[1,1,1]
	v_pk_fma_f32 v[54:55], v[232:233], v[142:143], v[54:55] op_sel:[1,0,0] op_sel_hi:[1,1,1]
	v_pk_fma_f32 v[48:49], v[234:235], v[144:145], v[48:49] op_sel_hi:[0,1,1]
	v_pk_fma_f32 v[50:51], v[234:235], v[146:147], v[50:51] op_sel_hi:[0,1,1]
	v_pk_fma_f32 v[52:53], v[234:235], v[148:149], v[52:53] op_sel_hi:[0,1,1]
	v_pk_fma_f32 v[54:55], v[234:235], v[150:151], v[54:55] op_sel_hi:[0,1,1]
	v_pk_fma_f32 v[48:49], v[234:235], v[152:153], v[48:49] op_sel:[1,0,0] op_sel_hi:[1,1,1]
	v_pk_fma_f32 v[50:51], v[234:235], v[154:155], v[50:51] op_sel:[1,0,0] op_sel_hi:[1,1,1]
	v_pk_fma_f32 v[52:53], v[234:235], v[156:157], v[52:53] op_sel:[1,0,0] op_sel_hi:[1,1,1]
	v_pk_fma_f32 v[54:55], v[234:235], v[158:159], v[54:55] op_sel:[1,0,0] op_sel_hi:[1,1,1]
	v_pk_fma_f32 v[48:49], v[236:237], v[160:161], v[48:49] op_sel_hi:[0,1,1]
	v_pk_fma_f32 v[50:51], v[236:237], v[162:163], v[50:51] op_sel_hi:[0,1,1]
	v_pk_fma_f32 v[52:53], v[236:237], v[164:165], v[52:53] op_sel_hi:[0,1,1]
	v_pk_fma_f32 v[54:55], v[236:237], v[166:167], v[54:55] op_sel_hi:[0,1,1]
	v_pk_fma_f32 v[48:49], v[236:237], v[168:169], v[48:49] op_sel:[1,0,0] op_sel_hi:[1,1,1]
	v_pk_fma_f32 v[50:51], v[236:237], v[170:171], v[50:51] op_sel:[1,0,0] op_sel_hi:[1,1,1]
	v_pk_fma_f32 v[52:53], v[236:237], v[172:173], v[52:53] op_sel:[1,0,0] op_sel_hi:[1,1,1]
	v_pk_fma_f32 v[54:55], v[236:237], v[174:175], v[54:55] op_sel:[1,0,0] op_sel_hi:[1,1,1]
	v_pk_fma_f32 v[48:49], v[238:239], v[176:177], v[48:49] op_sel_hi:[0,1,1]
	v_pk_fma_f32 v[50:51], v[238:239], v[178:179], v[50:51] op_sel_hi:[0,1,1]
	v_pk_fma_f32 v[52:53], v[238:239], v[180:181], v[52:53] op_sel_hi:[0,1,1]
	v_pk_fma_f32 v[54:55], v[238:239], v[182:183], v[54:55] op_sel_hi:[0,1,1]
	v_pk_fma_f32 v[48:49], v[238:239], v[184:185], v[48:49] op_sel:[1,0,0] op_sel_hi:[1,1,1]
	v_pk_fma_f32 v[50:51], v[238:239], v[186:187], v[50:51] op_sel:[1,0,0] op_sel_hi:[1,1,1]
	v_pk_fma_f32 v[52:53], v[238:239], v[188:189], v[52:53] op_sel:[1,0,0] op_sel_hi:[1,1,1]
	v_pk_fma_f32 v[54:55], v[238:239], v[190:191], v[54:55] op_sel:[1,0,0] op_sel_hi:[1,1,1]
	v_lshlrev_b32_e32 v232, 16, v92
	v_and_b32_e32 v233, s15, v92
	v_lshlrev_b32_e32 v234, 16, v93
	v_and_b32_e32 v235, s15, v93
	v_lshlrev_b32_e32 v236, 16, v94
	v_and_b32_e32 v237, s15, v94
	v_lshlrev_b32_e32 v238, 16, v95
	v_and_b32_e32 v239, s15, v95
	v_pk_fma_f32 v[206:207], v[232:233], v[232:233], v[206:207]
	v_pk_fma_f32 v[206:207], v[234:235], v[234:235], v[206:207]
	v_pk_fma_f32 v[206:207], v[236:237], v[236:237], v[206:207]
	v_pk_fma_f32 v[206:207], v[238:239], v[238:239], v[206:207]
	v_pk_fma_f32 v[56:57], v[232:233], v[128:129], v[56:57] op_sel_hi:[0,1,1]
	v_pk_fma_f32 v[58:59], v[232:233], v[130:131], v[58:59] op_sel_hi:[0,1,1]
	v_pk_fma_f32 v[60:61], v[232:233], v[132:133], v[60:61] op_sel_hi:[0,1,1]
	v_pk_fma_f32 v[62:63], v[232:233], v[134:135], v[62:63] op_sel_hi:[0,1,1]
	v_pk_fma_f32 v[56:57], v[232:233], v[136:137], v[56:57] op_sel:[1,0,0] op_sel_hi:[1,1,1]
	v_pk_fma_f32 v[58:59], v[232:233], v[138:139], v[58:59] op_sel:[1,0,0] op_sel_hi:[1,1,1]
	v_pk_fma_f32 v[60:61], v[232:233], v[140:141], v[60:61] op_sel:[1,0,0] op_sel_hi:[1,1,1]
	v_pk_fma_f32 v[62:63], v[232:233], v[142:143], v[62:63] op_sel:[1,0,0] op_sel_hi:[1,1,1]
	v_pk_fma_f32 v[56:57], v[234:235], v[144:145], v[56:57] op_sel_hi:[0,1,1]
	v_pk_fma_f32 v[58:59], v[234:235], v[146:147], v[58:59] op_sel_hi:[0,1,1]
	v_pk_fma_f32 v[60:61], v[234:235], v[148:149], v[60:61] op_sel_hi:[0,1,1]
	v_pk_fma_f32 v[62:63], v[234:235], v[150:151], v[62:63] op_sel_hi:[0,1,1]
	v_pk_fma_f32 v[56:57], v[234:235], v[152:153], v[56:57] op_sel:[1,0,0] op_sel_hi:[1,1,1]
	v_pk_fma_f32 v[58:59], v[234:235], v[154:155], v[58:59] op_sel:[1,0,0] op_sel_hi:[1,1,1]
	v_pk_fma_f32 v[60:61], v[234:235], v[156:157], v[60:61] op_sel:[1,0,0] op_sel_hi:[1,1,1]
	v_pk_fma_f32 v[62:63], v[234:235], v[158:159], v[62:63] op_sel:[1,0,0] op_sel_hi:[1,1,1]
	v_pk_fma_f32 v[56:57], v[236:237], v[160:161], v[56:57] op_sel_hi:[0,1,1]
	v_pk_fma_f32 v[58:59], v[236:237], v[162:163], v[58:59] op_sel_hi:[0,1,1]
	v_pk_fma_f32 v[60:61], v[236:237], v[164:165], v[60:61] op_sel_hi:[0,1,1]
	v_pk_fma_f32 v[62:63], v[236:237], v[166:167], v[62:63] op_sel_hi:[0,1,1]
	v_pk_fma_f32 v[56:57], v[236:237], v[168:169], v[56:57] op_sel:[1,0,0] op_sel_hi:[1,1,1]
	v_pk_fma_f32 v[58:59], v[236:237], v[170:171], v[58:59] op_sel:[1,0,0] op_sel_hi:[1,1,1]
	v_pk_fma_f32 v[60:61], v[236:237], v[172:173], v[60:61] op_sel:[1,0,0] op_sel_hi:[1,1,1]
	v_pk_fma_f32 v[62:63], v[236:237], v[174:175], v[62:63] op_sel:[1,0,0] op_sel_hi:[1,1,1]
	v_pk_fma_f32 v[56:57], v[238:239], v[176:177], v[56:57] op_sel_hi:[0,1,1]
	v_pk_fma_f32 v[58:59], v[238:239], v[178:179], v[58:59] op_sel_hi:[0,1,1]
	v_pk_fma_f32 v[60:61], v[238:239], v[180:181], v[60:61] op_sel_hi:[0,1,1]
	v_pk_fma_f32 v[62:63], v[238:239], v[182:183], v[62:63] op_sel_hi:[0,1,1]
	v_pk_fma_f32 v[56:57], v[238:239], v[184:185], v[56:57] op_sel:[1,0,0] op_sel_hi:[1,1,1]
	v_pk_fma_f32 v[58:59], v[238:239], v[186:187], v[58:59] op_sel:[1,0,0] op_sel_hi:[1,1,1]
	v_pk_fma_f32 v[60:61], v[238:239], v[188:189], v[60:61] op_sel:[1,0,0] op_sel_hi:[1,1,1]
	v_pk_fma_f32 v[62:63], v[238:239], v[190:191], v[62:63] op_sel:[1,0,0] op_sel_hi:[1,1,1]
	global_load_dwordx4 v[64:67], v208, s[40:41] offset:2048
	global_load_dwordx4 v[68:71], v208, s[42:43] offset:2048
	global_load_dwordx4 v[72:75], v208, s[44:45] offset:2048
	global_load_dwordx4 v[76:79], v208, s[46:47] offset:2048
	global_load_dwordx4 v[80:83], v208, s[48:49] offset:2048
	global_load_dwordx4 v[84:87], v208, s[50:51] offset:2048
	global_load_dwordx4 v[88:91], v208, s[52:53] offset:2048
	global_load_dwordx4 v[92:95], v208, s[54:55] offset:2048
	ds_read_b128 v[128:131], v208 offset:16384
	ds_read_b128 v[132:135], v208 offset:17408
	ds_read_b128 v[136:139], v208 offset:18432
	ds_read_b128 v[140:143], v208 offset:19456
	ds_read_b128 v[144:147], v208 offset:20480
	ds_read_b128 v[148:151], v208 offset:21504
	ds_read_b128 v[152:155], v208 offset:22528
	ds_read_b128 v[156:159], v208 offset:23552
	ds_read_b128 v[160:163], v208 offset:24576
	ds_read_b128 v[164:167], v208 offset:25600
	ds_read_b128 v[168:171], v208 offset:26624
	ds_read_b128 v[172:175], v208 offset:27648
	ds_read_b128 v[176:179], v208 offset:28672
	ds_read_b128 v[180:183], v208 offset:29696
	ds_read_b128 v[184:187], v208 offset:30720
	ds_read_b128 v[188:191], v208 offset:31744
	s_waitcnt vmcnt(8)
; #define LAS __attribute__((address_space(3)))
; __global__ void __launch_bounds__(NTHR, 2) fwd_kernel(Args args) {
;     ...
;             for (int i = 0; i < 16; ++i) { const int k = 2 * lane + 128 * i; f32x2 rv[8]; unsigned xw[8];
; #pragma unroll
;                 for (int e = 0; e < 8; ++e) rv[e] = *(const LAS f32x2*)(Rg + e * DM + k);
; #pragma unroll
;                 for (int q = 0; q < 8; ++q) xw[q] = *(const unsigned*)(XB + (size_t)(t0 + q) * DM + k);
; #pragma unroll
;                 for (int q = 0; q < 8; ++q) { const float x0 = bflo(xw[q]), x1 = bfhi(xw[q]); ssq[q] += x0 * x0 + x1 * x1;
; #pragma unroll
;                     for (int e = 0; e < 8; ++e) acc[q][e] += x0 * rv[e].x + x1 * rv[e].y; } }
	s_waitcnt lgkmcnt(0)
	v_lshlrev_b32_e32 v232, 16, v96
	v_and_b32_e32 v233, s15, v96
	v_lshlrev_b32_e32 v234, 16, v97
	v_and_b32_e32 v235, s15, v97
	v_lshlrev_b32_e32 v236, 16, v98
	v_and_b32_e32 v237, s15, v98
	v_lshlrev_b32_e32 v238, 16, v99
	v_and_b32_e32 v239, s15, v99
	v_pk_fma_f32 v[192:193], v[232:233], v[232:233], v[192:193]
	v_pk_fma_f32 v[192:193], v[234:235], v[234:235], v[192:193]
	v_pk_fma_f32 v[192:193], v[236:237], v[236:237], v[192:193]
	v_pk_fma_f32 v[192:193], v[238:239], v[238:239], v[192:193]
	v_pk_fma_f32 v[0:1], v[232:233], v[128:129], v[0:1] op_sel_hi:[0,1,1]
	v_pk_fma_f32 v[2:3], v[232:233], v[130:131], v[2:3] op_sel_hi:[0,1,1]
	v_pk_fma_f32 v[4:5], v[232:233], v[132:133], v[4:5] op_sel_hi:[0,1,1]
	v_pk_fma_f32 v[6:7], v[232:233], v[134:135], v[6:7] op_sel_hi:[0,1,1]
	v_pk_fma_f32 v[0:1], v[232:233], v[136:137], v[0:1] op_sel:[1,0,0] op_sel_hi:[1,1,1]
	v_pk_fma_f32 v[2:3], v[232:233], v[138:139], v[2:3] op_sel:[1,0,0] op_sel_hi:[1,1,1]
	v_pk_fma_f32 v[4:5], v[232:233], v[140:141], v[4:5] op_sel:[1,0,0] op_sel_hi:[1,1,1]
	v_pk_fma_f32 v[6:7], v[232:233], v[142:143], v[6:7] op_sel:[1,0,0] op_sel_hi:[1,1,1]
	v_pk_fma_f32 v[0:1], v[234:235], v[144:145], v[0:1] op_sel_hi:[0,1,1]
	v_pk_fma_f32 v[2:3], v[234:235], v[146:147], v[2:3] op_sel_hi:[0,1,1]
	v_pk_fma_f32 v[4:5], v[234:235], v[148:149], v[4:5] op_sel_hi:[0,1,1]
	v_pk_fma_f32 v[6:7], v[234:235], v[150:151], v[6:7] op_sel_hi:[0,1,1]
	v_pk_fma_f32 v[0:1], v[234:235], v[152:153], v[0:1] op_sel:[1,0,0] op_sel_hi:[1,1,1]
	v_pk_fma_f32 v[2:3], v[234:235], v[154:155], v[2:3] op_sel:[1,0,0] op_sel_hi:[1,1,1]
	v_pk_fma_f32 v[4:5], v[234:235], v[156:157], v[4:5] op_sel:[1,0,0] op_sel_hi:[1,1,1]
	v_pk_fma_f32 v[6:7], v[234:235], v[158:159], v[6:7] op_sel:[1,0,0] op_sel_hi:[1,1,1]
	v_pk_fma_f32 v[0:1], v[236:237], v[160:161], v[0:1] op_sel_hi:[0,1,1]
	v_pk_fma_f32 v[2:3], v[236:237], v[162:163], v[2:3] op_sel_hi:[0,1,1]
	v_pk_fma_f32 v[4:5], v[236:237], v[164:165], v[4:5] op_sel_hi:[0,1,1]
	v_pk_fma_f32 v[6:7], v[236:237], v[166:167], v[6:7] op_sel_hi:[0,1,1]
	v_pk_fma_f32 v[0:1], v[236:237], v[168:169], v[0:1] op_sel:[1,0,0] op_sel_hi:[1,1,1]
	v_pk_fma_f32 v[2:3], v[236:237], v[170:171], v[2:3] op_sel:[1,0,0] op_sel_hi:[1,1,1]
	v_pk_fma_f32 v[4:5], v[236:237], v[172:173], v[4:5] op_sel:[1,0,0] op_sel_hi:[1,1,1]
	v_pk_fma_f32 v[6:7], v[236:237], v[174:175], v[6:7] op_sel:[1,0,0] op_sel_hi:[1,1,1]
	v_pk_fma_f32 v[0:1], v[238:239], v[176:177], v[0:1] op_sel_hi:[0,1,1]
	v_pk_fma_f32 v[2:3], v[238:239], v[178:179], v[2:3] op_sel_hi:[0,1,1]
	v_pk_fma_f32 v[4:5], v[238:239], v[180:181], v[4:5] op_sel_hi:[0,1,1]
	v_pk_fma_f32 v[6:7], v[238:239], v[182:183], v[6:7] op_sel_hi:[0,1,1]
	v_pk_fma_f32 v[0:1], v[238:239], v[184:185], v[0:1] op_sel:[1,0,0] op_sel_hi:[1,1,1]
	v_pk_fma_f32 v[2:3], v[238:239], v[186:187], v[2:3] op_sel:[1,0,0] op_sel_hi:[1,1,1]
	v_pk_fma_f32 v[4:5], v[238:239], v[188:189], v[4:5] op_sel:[1,0,0] op_sel_hi:[1,1,1]
	v_pk_fma_f32 v[6:7], v[238:239], v[190:191], v[6:7] op_sel:[1,0,0] op_sel_hi:[1,1,1]
	v_lshlrev_b32_e32 v232, 16, v100
	v_and_b32_e32 v233, s15, v100
	v_lshlrev_b32_e32 v234, 16, v101
	v_and_b32_e32 v235, s15, v101
	v_lshlrev_b32_e32 v236, 16, v102
	v_and_b32_e32 v237, s15, v102
	v_lshlrev_b32_e32 v238, 16, v103
	v_and_b32_e32 v239, s15, v103
	v_pk_fma_f32 v[194:195], v[232:233], v[232:233], v[194:195]
	v_pk_fma_f32 v[194:195], v[234:235], v[234:235], v[194:195]
	v_pk_fma_f32 v[194:195], v[236:237], v[236:237], v[194:195]
	v_pk_fma_f32 v[194:195], v[238:239], v[238:239], v[194:195]
	v_pk_fma_f32 v[8:9], v[232:233], v[128:129], v[8:9] op_sel_hi:[0,1,1]
	v_pk_fma_f32 v[10:11], v[232:233], v[130:131], v[10:11] op_sel_hi:[0,1,1]
	v_pk_fma_f32 v[12:13], v[232:233], v[132:133], v[12:13] op_sel_hi:[0,1,1]
	v_pk_fma_f32 v[14:15], v[232:233], v[134:135], v[14:15] op_sel_hi:[0,1,1]
	v_pk_fma_f32 v[8:9], v[232:233], v[136:137], v[8:9] op_sel:[1,0,0] op_sel_hi:[1,1,1]
	v_pk_fma_f32 v[10:11], v[232:233], v[138:139], v[10:11] op_sel:[1,0,0] op_sel_hi:[1,1,1]
	v_pk_fma_f32 v[12:13], v[232:233], v[140:141], v[12:13] op_sel:[1,0,0] op_sel_hi:[1,1,1]
	v_pk_fma_f32 v[14:15], v[232:233], v[142:143], v[14:15] op_sel:[1,0,0] op_sel_hi:[1,1,1]
	v_pk_fma_f32 v[8:9], v[234:235], v[144:145], v[8:9] op_sel_hi:[0,1,1]
	v_pk_fma_f32 v[10:11], v[234:235], v[146:147], v[10:11] op_sel_hi:[0,1,1]
	v_pk_fma_f32 v[12:13], v[234:235], v[148:149], v[12:13] op_sel_hi:[0,1,1]
	v_pk_fma_f32 v[14:15], v[234:235], v[150:151], v[14:15] op_sel_hi:[0,1,1]
	v_pk_fma_f32 v[8:9], v[234:235], v[152:153], v[8:9] op_sel:[1,0,0] op_sel_hi:[1,1,1]
	v_pk_fma_f32 v[10:11], v[234:235], v[154:155], v[10:11] op_sel:[1,0,0] op_sel_hi:[1,1,1]
	v_pk_fma_f32 v[12:13], v[234:235], v[156:157], v[12:13] op_sel:[1,0,0] op_sel_hi:[1,1,1]
	v_pk_fma_f32 v[14:15], v[234:235], v[158:159], v[14:15] op_sel:[1,0,0] op_sel_hi:[1,1,1]
	v_pk_fma_f32 v[8:9], v[236:237], v[160:161], v[8:9] op_sel_hi:[0,1,1]
	v_pk_fma_f32 v[10:11], v[236:237], v[162:163], v[10:11] op_sel_hi:[0,1,1]
	v_pk_fma_f32 v[12:13], v[236:237], v[164:165], v[12:13] op_sel_hi:[0,1,1]
	v_pk_fma_f32 v[14:15], v[236:237], v[166:167], v[14:15] op_sel_hi:[0,1,1]
	v_pk_fma_f32 v[8:9], v[236:237], v[168:169], v[8:9] op_sel:[1,0,0] op_sel_hi:[1,1,1]
	v_pk_fma_f32 v[10:11], v[236:237], v[170:171], v[10:11] op_sel:[1,0,0] op_sel_hi:[1,1,1]
	v_pk_fma_f32 v[12:13], v[236:237], v[172:173], v[12:13] op_sel:[1,0,0] op_sel_hi:[1,1,1]
	v_pk_fma_f32 v[14:15], v[236:237], v[174:175], v[14:15] op_sel:[1,0,0] op_sel_hi:[1,1,1]
	v_pk_fma_f32 v[8:9], v[238:239], v[176:177], v[8:9] op_sel_hi:[0,1,1]
	v_pk_fma_f32 v[10:11], v[238:239], v[178:179], v[10:11] op_sel_hi:[0,1,1]
; #define LAS __attribute__((address_space(3)))
; __global__ void __launch_bounds__(NTHR, 2) fwd_kernel(Args args) {
;     ...
;             for (int i = 0; i < 16; ++i) { const int k = 2 * lane + 128 * i; f32x2 rv[8]; unsigned xw[8];
; #pragma unroll
;                 for (int e = 0; e < 8; ++e) rv[e] = *(const LAS f32x2*)(Rg + e * DM + k);
; #pragma unroll
;                 for (int q = 0; q < 8; ++q) xw[q] = *(const unsigned*)(XB + (size_t)(t0 + q) * DM + k);
; #pragma unroll
;                 for (int q = 0; q < 8; ++q) { const float x0 = bflo(xw[q]), x1 = bfhi(xw[q]); ssq[q] += x0 * x0 + x1 * x1;
; #pragma unroll
;                     for (int e = 0; e < 8; ++e) acc[q][e] += x0 * rv[e].x + x1 * rv[e].y; } }
	v_pk_fma_f32 v[12:13], v[238:239], v[180:181], v[12:13] op_sel_hi:[0,1,1]
	v_pk_fma_f32 v[14:15], v[238:239], v[182:183], v[14:15] op_sel_hi:[0,1,1]
	v_pk_fma_f32 v[8:9], v[238:239], v[184:185], v[8:9] op_sel:[1,0,0] op_sel_hi:[1,1,1]
	v_pk_fma_f32 v[10:11], v[238:239], v[186:187], v[10:11] op_sel:[1,0,0] op_sel_hi:[1,1,1]
	v_pk_fma_f32 v[12:13], v[238:239], v[188:189], v[12:13] op_sel:[1,0,0] op_sel_hi:[1,1,1]
	v_pk_fma_f32 v[14:15], v[238:239], v[190:191], v[14:15] op_sel:[1,0,0] op_sel_hi:[1,1,1]
	v_lshlrev_b32_e32 v232, 16, v104
	v_and_b32_e32 v233, s15, v104
	v_lshlrev_b32_e32 v234, 16, v105
	v_and_b32_e32 v235, s15, v105
	v_lshlrev_b32_e32 v236, 16, v106
	v_and_b32_e32 v237, s15, v106
	v_lshlrev_b32_e32 v238, 16, v107
	v_and_b32_e32 v239, s15, v107
	v_pk_fma_f32 v[196:197], v[232:233], v[232:233], v[196:197]
	v_pk_fma_f32 v[196:197], v[234:235], v[234:235], v[196:197]
	v_pk_fma_f32 v[196:197], v[236:237], v[236:237], v[196:197]
	v_pk_fma_f32 v[196:197], v[238:239], v[238:239], v[196:197]
	v_pk_fma_f32 v[16:17], v[232:233], v[128:129], v[16:17] op_sel_hi:[0,1,1]
	v_pk_fma_f32 v[18:19], v[232:233], v[130:131], v[18:19] op_sel_hi:[0,1,1]
	v_pk_fma_f32 v[20:21], v[232:233], v[132:133], v[20:21] op_sel_hi:[0,1,1]
	v_pk_fma_f32 v[22:23], v[232:233], v[134:135], v[22:23] op_sel_hi:[0,1,1]
	v_pk_fma_f32 v[16:17], v[232:233], v[136:137], v[16:17] op_sel:[1,0,0] op_sel_hi:[1,1,1]
	v_pk_fma_f32 v[18:19], v[232:233], v[138:139], v[18:19] op_sel:[1,0,0] op_sel_hi:[1,1,1]
	v_pk_fma_f32 v[20:21], v[232:233], v[140:141], v[20:21] op_sel:[1,0,0] op_sel_hi:[1,1,1]
	v_pk_fma_f32 v[22:23], v[232:233], v[142:143], v[22:23] op_sel:[1,0,0] op_sel_hi:[1,1,1]
	v_pk_fma_f32 v[16:17], v[234:235], v[144:145], v[16:17] op_sel_hi:[0,1,1]
	v_pk_fma_f32 v[18:19], v[234:235], v[146:147], v[18:19] op_sel_hi:[0,1,1]
	v_pk_fma_f32 v[20:21], v[234:235], v[148:149], v[20:21] op_sel_hi:[0,1,1]
	v_pk_fma_f32 v[22:23], v[234:235], v[150:151], v[22:23] op_sel_hi:[0,1,1]
	v_pk_fma_f32 v[16:17], v[234:235], v[152:153], v[16:17] op_sel:[1,0,0] op_sel_hi:[1,1,1]
	v_pk_fma_f32 v[18:19], v[234:235], v[154:155], v[18:19] op_sel:[1,0,0] op_sel_hi:[1,1,1]
	v_pk_fma_f32 v[20:21], v[234:235], v[156:157], v[20:21] op_sel:[1,0,0] op_sel_hi:[1,1,1]
	v_pk_fma_f32 v[22:23], v[234:235], v[158:159], v[22:23] op_sel:[1,0,0] op_sel_hi:[1,1,1]
	v_pk_fma_f32 v[16:17], v[236:237], v[160:161], v[16:17] op_sel_hi:[0,1,1]
	v_pk_fma_f32 v[18:19], v[236:237], v[162:163], v[18:19] op_sel_hi:[0,1,1]
	v_pk_fma_f32 v[20:21], v[236:237], v[164:165], v[20:21] op_sel_hi:[0,1,1]
	v_pk_fma_f32 v[22:23], v[236:237], v[166:167], v[22:23] op_sel_hi:[0,1,1]
	v_pk_fma_f32 v[16:17], v[236:237], v[168:169], v[16:17] op_sel:[1,0,0] op_sel_hi:[1,1,1]
	v_pk_fma_f32 v[18:19], v[236:237], v[170:171], v[18:19] op_sel:[1,0,0] op_sel_hi:[1,1,1]
	v_pk_fma_f32 v[20:21], v[236:237], v[172:173], v[20:21] op_sel:[1,0,0] op_sel_hi:[1,1,1]
	v_pk_fma_f32 v[22:23], v[236:237], v[174:175], v[22:23] op_sel:[1,0,0] op_sel_hi:[1,1,1]
	v_pk_fma_f32 v[16:17], v[238:239], v[176:177], v[16:17] op_sel_hi:[0,1,1]
	v_pk_fma_f32 v[18:19], v[238:239], v[178:179], v[18:19] op_sel_hi:[0,1,1]
	v_pk_fma_f32 v[20:21], v[238:239], v[180:181], v[20:21] op_sel_hi:[0,1,1]
	v_pk_fma_f32 v[22:23], v[238:239], v[182:183], v[22:23] op_sel_hi:[0,1,1]
	v_pk_fma_f32 v[16:17], v[238:239], v[184:185], v[16:17] op_sel:[1,0,0] op_sel_hi:[1,1,1]
	v_pk_fma_f32 v[18:19], v[238:239], v[186:187], v[18:19] op_sel:[1,0,0] op_sel_hi:[1,1,1]
	v_pk_fma_f32 v[20:21], v[238:239], v[188:189], v[20:21] op_sel:[1,0,0] op_sel_hi:[1,1,1]
	v_pk_fma_f32 v[22:23], v[238:239], v[190:191], v[22:23] op_sel:[1,0,0] op_sel_hi:[1,1,1]
	v_lshlrev_b32_e32 v232, 16, v108
	v_and_b32_e32 v233, s15, v108
	v_lshlrev_b32_e32 v234, 16, v109
	v_and_b32_e32 v235, s15, v109
	v_lshlrev_b32_e32 v236, 16, v110
	v_and_b32_e32 v237, s15, v110
	v_lshlrev_b32_e32 v238, 16, v111
	v_and_b32_e32 v239, s15, v111
	v_pk_fma_f32 v[198:199], v[232:233], v[232:233], v[198:199]
	v_pk_fma_f32 v[198:199], v[234:235], v[234:235], v[198:199]
	v_pk_fma_f32 v[198:199], v[236:237], v[236:237], v[198:199]
	v_pk_fma_f32 v[198:199], v[238:239], v[238:239], v[198:199]
	v_pk_fma_f32 v[24:25], v[232:233], v[128:129], v[24:25] op_sel_hi:[0,1,1]
	v_pk_fma_f32 v[26:27], v[232:233], v[130:131], v[26:27] op_sel_hi:[0,1,1]
	v_pk_fma_f32 v[28:29], v[232:233], v[132:133], v[28:29] op_sel_hi:[0,1,1]
	v_pk_fma_f32 v[30:31], v[232:233], v[134:135], v[30:31] op_sel_hi:[0,1,1]
	v_pk_fma_f32 v[24:25], v[232:233], v[136:137], v[24:25] op_sel:[1,0,0] op_sel_hi:[1,1,1]
	v_pk_fma_f32 v[26:27], v[232:233], v[138:139], v[26:27] op_sel:[1,0,0] op_sel_hi:[1,1,1]
	v_pk_fma_f32 v[28:29], v[232:233], v[140:141], v[28:29] op_sel:[1,0,0] op_sel_hi:[1,1,1]
	v_pk_fma_f32 v[30:31], v[232:233], v[142:143], v[30:31] op_sel:[1,0,0] op_sel_hi:[1,1,1]
	v_pk_fma_f32 v[24:25], v[234:235], v[144:145], v[24:25] op_sel_hi:[0,1,1]
	v_pk_fma_f32 v[26:27], v[234:235], v[146:147], v[26:27] op_sel_hi:[0,1,1]
	v_pk_fma_f32 v[28:29], v[234:235], v[148:149], v[28:29] op_sel_hi:[0,1,1]
	v_pk_fma_f32 v[30:31], v[234:235], v[150:151], v[30:31] op_sel_hi:[0,1,1]
	v_pk_fma_f32 v[24:25], v[234:235], v[152:153], v[24:25] op_sel:[1,0,0] op_sel_hi:[1,1,1]
	v_pk_fma_f32 v[26:27], v[234:235], v[154:155], v[26:27] op_sel:[1,0,0] op_sel_hi:[1,1,1]
	v_pk_fma_f32 v[28:29], v[234:235], v[156:157], v[28:29] op_sel:[1,0,0] op_sel_hi:[1,1,1]
	v_pk_fma_f32 v[30:31], v[234:235], v[158:159], v[30:31] op_sel:[1,0,0] op_sel_hi:[1,1,1]
	v_pk_fma_f32 v[24:25], v[236:237], v[160:161], v[24:25] op_sel_hi:[0,1,1]
	v_pk_fma_f32 v[26:27], v[236:237], v[162:163], v[26:27] op_sel_hi:[0,1,1]
; #define LAS __attribute__((address_space(3)))
; __global__ void __launch_bounds__(NTHR, 2) fwd_kernel(Args args) {
;     ...
;             for (int i = 0; i < 16; ++i) { const int k = 2 * lane + 128 * i; f32x2 rv[8]; unsigned xw[8];
; #pragma unroll
;                 for (int e = 0; e < 8; ++e) rv[e] = *(const LAS f32x2*)(Rg + e * DM + k);
; #pragma unroll
;                 for (int q = 0; q < 8; ++q) xw[q] = *(const unsigned*)(XB + (size_t)(t0 + q) * DM + k);
; #pragma unroll
;                 for (int q = 0; q < 8; ++q) { const float x0 = bflo(xw[q]), x1 = bfhi(xw[q]); ssq[q] += x0 * x0 + x1 * x1;
; #pragma unroll
;                     for (int e = 0; e < 8; ++e) acc[q][e] += x0 * rv[e].x + x1 * rv[e].y; } }
	v_pk_fma_f32 v[28:29], v[236:237], v[164:165], v[28:29] op_sel_hi:[0,1,1]
	v_pk_fma_f32 v[30:31], v[236:237], v[166:167], v[30:31] op_sel_hi:[0,1,1]
	v_pk_fma_f32 v[24:25], v[236:237], v[168:169], v[24:25] op_sel:[1,0,0] op_sel_hi:[1,1,1]
	v_pk_fma_f32 v[26:27], v[236:237], v[170:171], v[26:27] op_sel:[1,0,0] op_sel_hi:[1,1,1]
	v_pk_fma_f32 v[28:29], v[236:237], v[172:173], v[28:29] op_sel:[1,0,0] op_sel_hi:[1,1,1]
	v_pk_fma_f32 v[30:31], v[236:237], v[174:175], v[30:31] op_sel:[1,0,0] op_sel_hi:[1,1,1]
	v_pk_fma_f32 v[24:25], v[238:239], v[176:177], v[24:25] op_sel_hi:[0,1,1]
	v_pk_fma_f32 v[26:27], v[238:239], v[178:179], v[26:27] op_sel_hi:[0,1,1]
	v_pk_fma_f32 v[28:29], v[238:239], v[180:181], v[28:29] op_sel_hi:[0,1,1]
	v_pk_fma_f32 v[30:31], v[238:239], v[182:183], v[30:31] op_sel_hi:[0,1,1]
	v_pk_fma_f32 v[24:25], v[238:239], v[184:185], v[24:25] op_sel:[1,0,0] op_sel_hi:[1,1,1]
	v_pk_fma_f32 v[26:27], v[238:239], v[186:187], v[26:27] op_sel:[1,0,0] op_sel_hi:[1,1,1]
	v_pk_fma_f32 v[28:29], v[238:239], v[188:189], v[28:29] op_sel:[1,0,0] op_sel_hi:[1,1,1]
	v_pk_fma_f32 v[30:31], v[238:239], v[190:191], v[30:31] op_sel:[1,0,0] op_sel_hi:[1,1,1]
	v_lshlrev_b32_e32 v232, 16, v112
	v_and_b32_e32 v233, s15, v112
	v_lshlrev_b32_e32 v234, 16, v113
	v_and_b32_e32 v235, s15, v113
	v_lshlrev_b32_e32 v236, 16, v114
	v_and_b32_e32 v237, s15, v114
	v_lshlrev_b32_e32 v238, 16, v115
	v_and_b32_e32 v239, s15, v115
	v_pk_fma_f32 v[200:201], v[232:233], v[232:233], v[200:201]
	v_pk_fma_f32 v[200:201], v[234:235], v[234:235], v[200:201]
	v_pk_fma_f32 v[200:201], v[236:237], v[236:237], v[200:201]
	v_pk_fma_f32 v[200:201], v[238:239], v[238:239], v[200:201]
	v_pk_fma_f32 v[32:33], v[232:233], v[128:129], v[32:33] op_sel_hi:[0,1,1]
	v_pk_fma_f32 v[34:35], v[232:233], v[130:131], v[34:35] op_sel_hi:[0,1,1]
	v_pk_fma_f32 v[36:37], v[232:233], v[132:133], v[36:37] op_sel_hi:[0,1,1]
	v_pk_fma_f32 v[38:39], v[232:233], v[134:135], v[38:39] op_sel_hi:[0,1,1]
	v_pk_fma_f32 v[32:33], v[232:233], v[136:137], v[32:33] op_sel:[1,0,0] op_sel_hi:[1,1,1]
	v_pk_fma_f32 v[34:35], v[232:233], v[138:139], v[34:35] op_sel:[1,0,0] op_sel_hi:[1,1,1]
	v_pk_fma_f32 v[36:37], v[232:233], v[140:141], v[36:37] op_sel:[1,0,0] op_sel_hi:[1,1,1]
	v_pk_fma_f32 v[38:39], v[232:233], v[142:143], v[38:39] op_sel:[1,0,0] op_sel_hi:[1,1,1]
	v_pk_fma_f32 v[32:33], v[234:235], v[144:145], v[32:33] op_sel_hi:[0,1,1]
	v_pk_fma_f32 v[34:35], v[234:235], v[146:147], v[34:35] op_sel_hi:[0,1,1]
	v_pk_fma_f32 v[36:37], v[234:235], v[148:149], v[36:37] op_sel_hi:[0,1,1]
	v_pk_fma_f32 v[38:39], v[234:235], v[150:151], v[38:39] op_sel_hi:[0,1,1]
	v_pk_fma_f32 v[32:33], v[234:235], v[152:153], v[32:33] op_sel:[1,0,0] op_sel_hi:[1,1,1]
	v_pk_fma_f32 v[34:35], v[234:235], v[154:155], v[34:35] op_sel:[1,0,0] op_sel_hi:[1,1,1]
	v_pk_fma_f32 v[36:37], v[234:235], v[156:157], v[36:37] op_sel:[1,0,0] op_sel_hi:[1,1,1]
	v_pk_fma_f32 v[38:39], v[234:235], v[158:159], v[38:39] op_sel:[1,0,0] op_sel_hi:[1,1,1]
	v_pk_fma_f32 v[32:33], v[236:237], v[160:161], v[32:33] op_sel_hi:[0,1,1]
	v_pk_fma_f32 v[34:35], v[236:237], v[162:163], v[34:35] op_sel_hi:[0,1,1]
	v_pk_fma_f32 v[36:37], v[236:237], v[164:165], v[36:37] op_sel_hi:[0,1,1]
	v_pk_fma_f32 v[38:39], v[236:237], v[166:167], v[38:39] op_sel_hi:[0,1,1]
	v_pk_fma_f32 v[32:33], v[236:237], v[168:169], v[32:33] op_sel:[1,0,0] op_sel_hi:[1,1,1]
	v_pk_fma_f32 v[34:35], v[236:237], v[170:171], v[34:35] op_sel:[1,0,0] op_sel_hi:[1,1,1]
	v_pk_fma_f32 v[36:37], v[236:237], v[172:173], v[36:37] op_sel:[1,0,0] op_sel_hi:[1,1,1]
	v_pk_fma_f32 v[38:39], v[236:237], v[174:175], v[38:39] op_sel:[1,0,0] op_sel_hi:[1,1,1]
	v_pk_fma_f32 v[32:33], v[238:239], v[176:177], v[32:33] op_sel_hi:[0,1,1]
	v_pk_fma_f32 v[34:35], v[238:239], v[178:179], v[34:35] op_sel_hi:[0,1,1]
	v_pk_fma_f32 v[36:37], v[238:239], v[180:181], v[36:37] op_sel_hi:[0,1,1]
	v_pk_fma_f32 v[38:39], v[238:239], v[182:183], v[38:39] op_sel_hi:[0,1,1]
	v_pk_fma_f32 v[32:33], v[238:239], v[184:185], v[32:33] op_sel:[1,0,0] op_sel_hi:[1,1,1]
	v_pk_fma_f32 v[34:35], v[238:239], v[186:187], v[34:35] op_sel:[1,0,0] op_sel_hi:[1,1,1]
	v_pk_fma_f32 v[36:37], v[238:239], v[188:189], v[36:37] op_sel:[1,0,0] op_sel_hi:[1,1,1]
	v_pk_fma_f32 v[38:39], v[238:239], v[190:191], v[38:39] op_sel:[1,0,0] op_sel_hi:[1,1,1]
	v_lshlrev_b32_e32 v232, 16, v116
	v_and_b32_e32 v233, s15, v116
	v_lshlrev_b32_e32 v234, 16, v117
	v_and_b32_e32 v235, s15, v117
	v_lshlrev_b32_e32 v236, 16, v118
	v_and_b32_e32 v237, s15, v118
	v_lshlrev_b32_e32 v238, 16, v119
	v_and_b32_e32 v239, s15, v119
	v_pk_fma_f32 v[202:203], v[232:233], v[232:233], v[202:203]
	v_pk_fma_f32 v[202:203], v[234:235], v[234:235], v[202:203]
	v_pk_fma_f32 v[202:203], v[236:237], v[236:237], v[202:203]
	v_pk_fma_f32 v[202:203], v[238:239], v[238:239], v[202:203]
	v_pk_fma_f32 v[40:41], v[232:233], v[128:129], v[40:41] op_sel_hi:[0,1,1]
	v_pk_fma_f32 v[42:43], v[232:233], v[130:131], v[42:43] op_sel_hi:[0,1,1]
	v_pk_fma_f32 v[44:45], v[232:233], v[132:133], v[44:45] op_sel_hi:[0,1,1]
	v_pk_fma_f32 v[46:47], v[232:233], v[134:135], v[46:47] op_sel_hi:[0,1,1]
	v_pk_fma_f32 v[40:41], v[232:233], v[136:137], v[40:41] op_sel:[1,0,0] op_sel_hi:[1,1,1]
	v_pk_fma_f32 v[42:43], v[232:233], v[138:139], v[42:43] op_sel:[1,0,0] op_sel_hi:[1,1,1]
	v_pk_fma_f32 v[44:45], v[232:233], v[140:141], v[44:45] op_sel:[1,0,0] op_sel_hi:[1,1,1]
	v_pk_fma_f32 v[46:47], v[232:233], v[142:143], v[46:47] op_sel:[1,0,0] op_sel_hi:[1,1,1]
	v_pk_fma_f32 v[40:41], v[234:235], v[144:145], v[40:41] op_sel_hi:[0,1,1]
	v_pk_fma_f32 v[42:43], v[234:235], v[146:147], v[42:43] op_sel_hi:[0,1,1]
; #define LAS __attribute__((address_space(3)))
; __global__ void __launch_bounds__(NTHR, 2) fwd_kernel(Args args) {
;     ...
;             for (int i = 0; i < 16; ++i) { const int k = 2 * lane + 128 * i; f32x2 rv[8]; unsigned xw[8];
; #pragma unroll
;                 for (int e = 0; e < 8; ++e) rv[e] = *(const LAS f32x2*)(Rg + e * DM + k);
; #pragma unroll
;                 for (int q = 0; q < 8; ++q) xw[q] = *(const unsigned*)(XB + (size_t)(t0 + q) * DM + k);
; #pragma unroll
;                 for (int q = 0; q < 8; ++q) { const float x0 = bflo(xw[q]), x1 = bfhi(xw[q]); ssq[q] += x0 * x0 + x1 * x1;
; #pragma unroll
;                     for (int e = 0; e < 8; ++e) acc[q][e] += x0 * rv[e].x + x1 * rv[e].y; } }
	v_pk_fma_f32 v[44:45], v[234:235], v[148:149], v[44:45] op_sel_hi:[0,1,1]
	v_pk_fma_f32 v[46:47], v[234:235], v[150:151], v[46:47] op_sel_hi:[0,1,1]
	v_pk_fma_f32 v[40:41], v[234:235], v[152:153], v[40:41] op_sel:[1,0,0] op_sel_hi:[1,1,1]
	v_pk_fma_f32 v[42:43], v[234:235], v[154:155], v[42:43] op_sel:[1,0,0] op_sel_hi:[1,1,1]
	v_pk_fma_f32 v[44:45], v[234:235], v[156:157], v[44:45] op_sel:[1,0,0] op_sel_hi:[1,1,1]
	v_pk_fma_f32 v[46:47], v[234:235], v[158:159], v[46:47] op_sel:[1,0,0] op_sel_hi:[1,1,1]
	v_pk_fma_f32 v[40:41], v[236:237], v[160:161], v[40:41] op_sel_hi:[0,1,1]
	v_pk_fma_f32 v[42:43], v[236:237], v[162:163], v[42:43] op_sel_hi:[0,1,1]
	v_pk_fma_f32 v[44:45], v[236:237], v[164:165], v[44:45] op_sel_hi:[0,1,1]
	v_pk_fma_f32 v[46:47], v[236:237], v[166:167], v[46:47] op_sel_hi:[0,1,1]
	v_pk_fma_f32 v[40:41], v[236:237], v[168:169], v[40:41] op_sel:[1,0,0] op_sel_hi:[1,1,1]
	v_pk_fma_f32 v[42:43], v[236:237], v[170:171], v[42:43] op_sel:[1,0,0] op_sel_hi:[1,1,1]
	v_pk_fma_f32 v[44:45], v[236:237], v[172:173], v[44:45] op_sel:[1,0,0] op_sel_hi:[1,1,1]
	v_pk_fma_f32 v[46:47], v[236:237], v[174:175], v[46:47] op_sel:[1,0,0] op_sel_hi:[1,1,1]
	v_pk_fma_f32 v[40:41], v[238:239], v[176:177], v[40:41] op_sel_hi:[0,1,1]
	v_pk_fma_f32 v[42:43], v[238:239], v[178:179], v[42:43] op_sel_hi:[0,1,1]
	v_pk_fma_f32 v[44:45], v[238:239], v[180:181], v[44:45] op_sel_hi:[0,1,1]
	v_pk_fma_f32 v[46:47], v[238:239], v[182:183], v[46:47] op_sel_hi:[0,1,1]
	v_pk_fma_f32 v[40:41], v[238:239], v[184:185], v[40:41] op_sel:[1,0,0] op_sel_hi:[1,1,1]
	v_pk_fma_f32 v[42:43], v[238:239], v[186:187], v[42:43] op_sel:[1,0,0] op_sel_hi:[1,1,1]
	v_pk_fma_f32 v[44:45], v[238:239], v[188:189], v[44:45] op_sel:[1,0,0] op_sel_hi:[1,1,1]
	v_pk_fma_f32 v[46:47], v[238:239], v[190:191], v[46:47] op_sel:[1,0,0] op_sel_hi:[1,1,1]
	v_lshlrev_b32_e32 v232, 16, v120
	v_and_b32_e32 v233, s15, v120
	v_lshlrev_b32_e32 v234, 16, v121
	v_and_b32_e32 v235, s15, v121
	v_lshlrev_b32_e32 v236, 16, v122
	v_and_b32_e32 v237, s15, v122
	v_lshlrev_b32_e32 v238, 16, v123
	v_and_b32_e32 v239, s15, v123
	v_pk_fma_f32 v[204:205], v[232:233], v[232:233], v[204:205]
	v_pk_fma_f32 v[204:205], v[234:235], v[234:235], v[204:205]
	v_pk_fma_f32 v[204:205], v[236:237], v[236:237], v[204:205]
	v_pk_fma_f32 v[204:205], v[238:239], v[238:239], v[204:205]
	v_pk_fma_f32 v[48:49], v[232:233], v[128:129], v[48:49] op_sel_hi:[0,1,1]
	v_pk_fma_f32 v[50:51], v[232:233], v[130:131], v[50:51] op_sel_hi:[0,1,1]
	v_pk_fma_f32 v[52:53], v[232:233], v[132:133], v[52:53] op_sel_hi:[0,1,1]
	v_pk_fma_f32 v[54:55], v[232:233], v[134:135], v[54:55] op_sel_hi:[0,1,1]
	v_pk_fma_f32 v[48:49], v[232:233], v[136:137], v[48:49] op_sel:[1,0,0] op_sel_hi:[1,1,1]
	v_pk_fma_f32 v[50:51], v[232:233], v[138:139], v[50:51] op_sel:[1,0,0] op_sel_hi:[1,1,1]
	v_pk_fma_f32 v[52:53], v[232:233], v[140:141], v[52:53] op_sel:[1,0,0] op_sel_hi:[1,1,1]
	v_pk_fma_f32 v[54:55], v[232:233], v[142:143], v[54:55] op_sel:[1,0,0] op_sel_hi:[1,1,1]
	v_pk_fma_f32 v[48:49], v[234:235], v[144:145], v[48:49] op_sel_hi:[0,1,1]
	v_pk_fma_f32 v[50:51], v[234:235], v[146:147], v[50:51] op_sel_hi:[0,1,1]
	v_pk_fma_f32 v[52:53], v[234:235], v[148:149], v[52:53] op_sel_hi:[0,1,1]
	v_pk_fma_f32 v[54:55], v[234:235], v[150:151], v[54:55] op_sel_hi:[0,1,1]
	v_pk_fma_f32 v[48:49], v[234:235], v[152:153], v[48:49] op_sel:[1,0,0] op_sel_hi:[1,1,1]
	v_pk_fma_f32 v[50:51], v[234:235], v[154:155], v[50:51] op_sel:[1,0,0] op_sel_hi:[1,1,1]
	v_pk_fma_f32 v[52:53], v[234:235], v[156:157], v[52:53] op_sel:[1,0,0] op_sel_hi:[1,1,1]
	v_pk_fma_f32 v[54:55], v[234:235], v[158:159], v[54:55] op_sel:[1,0,0] op_sel_hi:[1,1,1]
	v_pk_fma_f32 v[48:49], v[236:237], v[160:161], v[48:49] op_sel_hi:[0,1,1]
	v_pk_fma_f32 v[50:51], v[236:237], v[162:163], v[50:51] op_sel_hi:[0,1,1]
	v_pk_fma_f32 v[52:53], v[236:237], v[164:165], v[52:53] op_sel_hi:[0,1,1]
	v_pk_fma_f32 v[54:55], v[236:237], v[166:167], v[54:55] op_sel_hi:[0,1,1]
	v_pk_fma_f32 v[48:49], v[236:237], v[168:169], v[48:49] op_sel:[1,0,0] op_sel_hi:[1,1,1]
	v_pk_fma_f32 v[50:51], v[236:237], v[170:171], v[50:51] op_sel:[1,0,0] op_sel_hi:[1,1,1]
	v_pk_fma_f32 v[52:53], v[236:237], v[172:173], v[52:53] op_sel:[1,0,0] op_sel_hi:[1,1,1]
	v_pk_fma_f32 v[54:55], v[236:237], v[174:175], v[54:55] op_sel:[1,0,0] op_sel_hi:[1,1,1]
	v_pk_fma_f32 v[48:49], v[238:239], v[176:177], v[48:49] op_sel_hi:[0,1,1]
	v_pk_fma_f32 v[50:51], v[238:239], v[178:179], v[50:51] op_sel_hi:[0,1,1]
	v_pk_fma_f32 v[52:53], v[238:239], v[180:181], v[52:53] op_sel_hi:[0,1,1]
	v_pk_fma_f32 v[54:55], v[238:239], v[182:183], v[54:55] op_sel_hi:[0,1,1]
	v_pk_fma_f32 v[48:49], v[238:239], v[184:185], v[48:49] op_sel:[1,0,0] op_sel_hi:[1,1,1]
	v_pk_fma_f32 v[50:51], v[238:239], v[186:187], v[50:51] op_sel:[1,0,0] op_sel_hi:[1,1,1]
	v_pk_fma_f32 v[52:53], v[238:239], v[188:189], v[52:53] op_sel:[1,0,0] op_sel_hi:[1,1,1]
	v_pk_fma_f32 v[54:55], v[238:239], v[190:191], v[54:55] op_sel:[1,0,0] op_sel_hi:[1,1,1]
	v_lshlrev_b32_e32 v232, 16, v124
	v_and_b32_e32 v233, s15, v124
	v_lshlrev_b32_e32 v234, 16, v125
	v_and_b32_e32 v235, s15, v125
	v_lshlrev_b32_e32 v236, 16, v126
	v_and_b32_e32 v237, s15, v126
	v_lshlrev_b32_e32 v238, 16, v127
	v_and_b32_e32 v239, s15, v127
	v_pk_fma_f32 v[206:207], v[232:233], v[232:233], v[206:207]
	v_pk_fma_f32 v[206:207], v[234:235], v[234:235], v[206:207]
	v_pk_fma_f32 v[206:207], v[236:237], v[236:237], v[206:207]
	v_pk_fma_f32 v[206:207], v[238:239], v[238:239], v[206:207]
	v_pk_fma_f32 v[56:57], v[232:233], v[128:129], v[56:57] op_sel_hi:[0,1,1]
	v_pk_fma_f32 v[58:59], v[232:233], v[130:131], v[58:59] op_sel_hi:[0,1,1]
; #define LAS __attribute__((address_space(3)))
; __global__ void __launch_bounds__(NTHR, 2) fwd_kernel(Args args) {
;     ...
;             for (int i = 0; i < 16; ++i) { const int k = 2 * lane + 128 * i; f32x2 rv[8]; unsigned xw[8];
; #pragma unroll
;                 for (int e = 0; e < 8; ++e) rv[e] = *(const LAS f32x2*)(Rg + e * DM + k);
; #pragma unroll
;                 for (int q = 0; q < 8; ++q) xw[q] = *(const unsigned*)(XB + (size_t)(t0 + q) * DM + k);
; #pragma unroll
;                 for (int q = 0; q < 8; ++q) { const float x0 = bflo(xw[q]), x1 = bfhi(xw[q]); ssq[q] += x0 * x0 + x1 * x1;
; #pragma unroll
;                     for (int e = 0; e < 8; ++e) acc[q][e] += x0 * rv[e].x + x1 * rv[e].y; } }
	v_pk_fma_f32 v[60:61], v[232:233], v[132:133], v[60:61] op_sel_hi:[0,1,1]
	v_pk_fma_f32 v[62:63], v[232:233], v[134:135], v[62:63] op_sel_hi:[0,1,1]
	v_pk_fma_f32 v[56:57], v[232:233], v[136:137], v[56:57] op_sel:[1,0,0] op_sel_hi:[1,1,1]
	v_pk_fma_f32 v[58:59], v[232:233], v[138:139], v[58:59] op_sel:[1,0,0] op_sel_hi:[1,1,1]
	v_pk_fma_f32 v[60:61], v[232:233], v[140:141], v[60:61] op_sel:[1,0,0] op_sel_hi:[1,1,1]
	v_pk_fma_f32 v[62:63], v[232:233], v[142:143], v[62:63] op_sel:[1,0,0] op_sel_hi:[1,1,1]
	v_pk_fma_f32 v[56:57], v[234:235], v[144:145], v[56:57] op_sel_hi:[0,1,1]
	v_pk_fma_f32 v[58:59], v[234:235], v[146:147], v[58:59] op_sel_hi:[0,1,1]
	v_pk_fma_f32 v[60:61], v[234:235], v[148:149], v[60:61] op_sel_hi:[0,1,1]
	v_pk_fma_f32 v[62:63], v[234:235], v[150:151], v[62:63] op_sel_hi:[0,1,1]
	v_pk_fma_f32 v[56:57], v[234:235], v[152:153], v[56:57] op_sel:[1,0,0] op_sel_hi:[1,1,1]
	v_pk_fma_f32 v[58:59], v[234:235], v[154:155], v[58:59] op_sel:[1,0,0] op_sel_hi:[1,1,1]
	v_pk_fma_f32 v[60:61], v[234:235], v[156:157], v[60:61] op_sel:[1,0,0] op_sel_hi:[1,1,1]
	v_pk_fma_f32 v[62:63], v[234:235], v[158:159], v[62:63] op_sel:[1,0,0] op_sel_hi:[1,1,1]
	v_pk_fma_f32 v[56:57], v[236:237], v[160:161], v[56:57] op_sel_hi:[0,1,1]
	v_pk_fma_f32 v[58:59], v[236:237], v[162:163], v[58:59] op_sel_hi:[0,1,1]
	v_pk_fma_f32 v[60:61], v[236:237], v[164:165], v[60:61] op_sel_hi:[0,1,1]
	v_pk_fma_f32 v[62:63], v[236:237], v[166:167], v[62:63] op_sel_hi:[0,1,1]
	v_pk_fma_f32 v[56:57], v[236:237], v[168:169], v[56:57] op_sel:[1,0,0] op_sel_hi:[1,1,1]
	v_pk_fma_f32 v[58:59], v[236:237], v[170:171], v[58:59] op_sel:[1,0,0] op_sel_hi:[1,1,1]
	v_pk_fma_f32 v[60:61], v[236:237], v[172:173], v[60:61] op_sel:[1,0,0] op_sel_hi:[1,1,1]
	v_pk_fma_f32 v[62:63], v[236:237], v[174:175], v[62:63] op_sel:[1,0,0] op_sel_hi:[1,1,1]
	v_pk_fma_f32 v[56:57], v[238:239], v[176:177], v[56:57] op_sel_hi:[0,1,1]
	v_pk_fma_f32 v[58:59], v[238:239], v[178:179], v[58:59] op_sel_hi:[0,1,1]
	v_pk_fma_f32 v[60:61], v[238:239], v[180:181], v[60:61] op_sel_hi:[0,1,1]
	v_pk_fma_f32 v[62:63], v[238:239], v[182:183], v[62:63] op_sel_hi:[0,1,1]
	v_pk_fma_f32 v[56:57], v[238:239], v[184:185], v[56:57] op_sel:[1,0,0] op_sel_hi:[1,1,1]
	v_pk_fma_f32 v[58:59], v[238:239], v[186:187], v[58:59] op_sel:[1,0,0] op_sel_hi:[1,1,1]
	v_pk_fma_f32 v[60:61], v[238:239], v[188:189], v[60:61] op_sel:[1,0,0] op_sel_hi:[1,1,1]
	v_pk_fma_f32 v[62:63], v[238:239], v[190:191], v[62:63] op_sel:[1,0,0] op_sel_hi:[1,1,1]
	global_load_dwordx4 v[96:99], v208, s[40:41] offset:3072
	global_load_dwordx4 v[100:103], v208, s[42:43] offset:3072
	global_load_dwordx4 v[104:107], v208, s[44:45] offset:3072
	global_load_dwordx4 v[108:111], v208, s[46:47] offset:3072
	global_load_dwordx4 v[112:115], v208, s[48:49] offset:3072
	global_load_dwordx4 v[116:119], v208, s[50:51] offset:3072
	global_load_dwordx4 v[120:123], v208, s[52:53] offset:3072
	global_load_dwordx4 v[124:127], v208, s[54:55] offset:3072
	ds_read_b128 v[128:131], v208 offset:32768
	ds_read_b128 v[132:135], v208 offset:33792
	ds_read_b128 v[136:139], v208 offset:34816
	ds_read_b128 v[140:143], v208 offset:35840
	ds_read_b128 v[144:147], v208 offset:36864
	ds_read_b128 v[148:151], v208 offset:37888
	ds_read_b128 v[152:155], v208 offset:38912
	ds_read_b128 v[156:159], v208 offset:39936
	ds_read_b128 v[160:163], v208 offset:40960
	ds_read_b128 v[164:167], v208 offset:41984
	ds_read_b128 v[168:171], v208 offset:43008
	ds_read_b128 v[172:175], v208 offset:44032
	ds_read_b128 v[176:179], v208 offset:45056
	ds_read_b128 v[180:183], v208 offset:46080
	ds_read_b128 v[184:187], v208 offset:47104
	ds_read_b128 v[188:191], v208 offset:48128
	s_waitcnt vmcnt(8)
	s_waitcnt lgkmcnt(0)
	v_lshlrev_b32_e32 v232, 16, v64
	v_and_b32_e32 v233, s15, v64
	v_lshlrev_b32_e32 v234, 16, v65
	v_and_b32_e32 v235, s15, v65
	v_lshlrev_b32_e32 v236, 16, v66
	v_and_b32_e32 v237, s15, v66
	v_lshlrev_b32_e32 v238, 16, v67
	v_and_b32_e32 v239, s15, v67
	v_pk_fma_f32 v[192:193], v[232:233], v[232:233], v[192:193]
	v_pk_fma_f32 v[192:193], v[234:235], v[234:235], v[192:193]
	v_pk_fma_f32 v[192:193], v[236:237], v[236:237], v[192:193]
	v_pk_fma_f32 v[192:193], v[238:239], v[238:239], v[192:193]
	v_pk_fma_f32 v[0:1], v[232:233], v[128:129], v[0:1] op_sel_hi:[0,1,1]
	v_pk_fma_f32 v[2:3], v[232:233], v[130:131], v[2:3] op_sel_hi:[0,1,1]
	v_pk_fma_f32 v[4:5], v[232:233], v[132:133], v[4:5] op_sel_hi:[0,1,1]
	v_pk_fma_f32 v[6:7], v[232:233], v[134:135], v[6:7] op_sel_hi:[0,1,1]
	v_pk_fma_f32 v[0:1], v[232:233], v[136:137], v[0:1] op_sel:[1,0,0] op_sel_hi:[1,1,1]
	v_pk_fma_f32 v[2:3], v[232:233], v[138:139], v[2:3] op_sel:[1,0,0] op_sel_hi:[1,1,1]
	v_pk_fma_f32 v[4:5], v[232:233], v[140:141], v[4:5] op_sel:[1,0,0] op_sel_hi:[1,1,1]
	v_pk_fma_f32 v[6:7], v[232:233], v[142:143], v[6:7] op_sel:[1,0,0] op_sel_hi:[1,1,1]
	v_pk_fma_f32 v[0:1], v[234:235], v[144:145], v[0:1] op_sel_hi:[0,1,1]
	v_pk_fma_f32 v[2:3], v[234:235], v[146:147], v[2:3] op_sel_hi:[0,1,1]
	v_pk_fma_f32 v[4:5], v[234:235], v[148:149], v[4:5] op_sel_hi:[0,1,1]
	v_pk_fma_f32 v[6:7], v[234:235], v[150:151], v[6:7] op_sel_hi:[0,1,1]
	v_pk_fma_f32 v[0:1], v[234:235], v[152:153], v[0:1] op_sel:[1,0,0] op_sel_hi:[1,1,1]
	v_pk_fma_f32 v[2:3], v[234:235], v[154:155], v[2:3] op_sel:[1,0,0] op_sel_hi:[1,1,1]
	v_pk_fma_f32 v[4:5], v[234:235], v[156:157], v[4:5] op_sel:[1,0,0] op_sel_hi:[1,1,1]
	v_pk_fma_f32 v[6:7], v[234:235], v[158:159], v[6:7] op_sel:[1,0,0] op_sel_hi:[1,1,1]
	v_pk_fma_f32 v[0:1], v[236:237], v[160:161], v[0:1] op_sel_hi:[0,1,1]
	v_pk_fma_f32 v[2:3], v[236:237], v[162:163], v[2:3] op_sel_hi:[0,1,1]
; #define LAS __attribute__((address_space(3)))
; __global__ void __launch_bounds__(NTHR, 2) fwd_kernel(Args args) {
;     ...
;             for (int i = 0; i < 16; ++i) { const int k = 2 * lane + 128 * i; f32x2 rv[8]; unsigned xw[8];
; #pragma unroll
;                 for (int e = 0; e < 8; ++e) rv[e] = *(const LAS f32x2*)(Rg + e * DM + k);
; #pragma unroll
;                 for (int q = 0; q < 8; ++q) xw[q] = *(const unsigned*)(XB + (size_t)(t0 + q) * DM + k);
; #pragma unroll
;                 for (int q = 0; q < 8; ++q) { const float x0 = bflo(xw[q]), x1 = bfhi(xw[q]); ssq[q] += x0 * x0 + x1 * x1;
; #pragma unroll
;                     for (int e = 0; e < 8; ++e) acc[q][e] += x0 * rv[e].x + x1 * rv[e].y; } }
	v_pk_fma_f32 v[4:5], v[236:237], v[164:165], v[4:5] op_sel_hi:[0,1,1]
	v_pk_fma_f32 v[6:7], v[236:237], v[166:167], v[6:7] op_sel_hi:[0,1,1]
	v_pk_fma_f32 v[0:1], v[236:237], v[168:169], v[0:1] op_sel:[1,0,0] op_sel_hi:[1,1,1]
	v_pk_fma_f32 v[2:3], v[236:237], v[170:171], v[2:3] op_sel:[1,0,0] op_sel_hi:[1,1,1]
	v_pk_fma_f32 v[4:5], v[236:237], v[172:173], v[4:5] op_sel:[1,0,0] op_sel_hi:[1,1,1]
	v_pk_fma_f32 v[6:7], v[236:237], v[174:175], v[6:7] op_sel:[1,0,0] op_sel_hi:[1,1,1]
	v_pk_fma_f32 v[0:1], v[238:239], v[176:177], v[0:1] op_sel_hi:[0,1,1]
	v_pk_fma_f32 v[2:3], v[238:239], v[178:179], v[2:3] op_sel_hi:[0,1,1]
	v_pk_fma_f32 v[4:5], v[238:239], v[180:181], v[4:5] op_sel_hi:[0,1,1]
	v_pk_fma_f32 v[6:7], v[238:239], v[182:183], v[6:7] op_sel_hi:[0,1,1]
	v_pk_fma_f32 v[0:1], v[238:239], v[184:185], v[0:1] op_sel:[1,0,0] op_sel_hi:[1,1,1]
	v_pk_fma_f32 v[2:3], v[238:239], v[186:187], v[2:3] op_sel:[1,0,0] op_sel_hi:[1,1,1]
	v_pk_fma_f32 v[4:5], v[238:239], v[188:189], v[4:5] op_sel:[1,0,0] op_sel_hi:[1,1,1]
	v_pk_fma_f32 v[6:7], v[238:239], v[190:191], v[6:7] op_sel:[1,0,0] op_sel_hi:[1,1,1]
	v_lshlrev_b32_e32 v232, 16, v68
	v_and_b32_e32 v233, s15, v68
	v_lshlrev_b32_e32 v234, 16, v69
	v_and_b32_e32 v235, s15, v69
	v_lshlrev_b32_e32 v236, 16, v70
	v_and_b32_e32 v237, s15, v70
	v_lshlrev_b32_e32 v238, 16, v71
	v_and_b32_e32 v239, s15, v71
	v_pk_fma_f32 v[194:195], v[232:233], v[232:233], v[194:195]
	v_pk_fma_f32 v[194:195], v[234:235], v[234:235], v[194:195]
	v_pk_fma_f32 v[194:195], v[236:237], v[236:237], v[194:195]
	v_pk_fma_f32 v[194:195], v[238:239], v[238:239], v[194:195]
	v_pk_fma_f32 v[8:9], v[232:233], v[128:129], v[8:9] op_sel_hi:[0,1,1]
	v_pk_fma_f32 v[10:11], v[232:233], v[130:131], v[10:11] op_sel_hi:[0,1,1]
	v_pk_fma_f32 v[12:13], v[232:233], v[132:133], v[12:13] op_sel_hi:[0,1,1]
	v_pk_fma_f32 v[14:15], v[232:233], v[134:135], v[14:15] op_sel_hi:[0,1,1]
	v_pk_fma_f32 v[8:9], v[232:233], v[136:137], v[8:9] op_sel:[1,0,0] op_sel_hi:[1,1,1]
	v_pk_fma_f32 v[10:11], v[232:233], v[138:139], v[10:11] op_sel:[1,0,0] op_sel_hi:[1,1,1]
	v_pk_fma_f32 v[12:13], v[232:233], v[140:141], v[12:13] op_sel:[1,0,0] op_sel_hi:[1,1,1]
	v_pk_fma_f32 v[14:15], v[232:233], v[142:143], v[14:15] op_sel:[1,0,0] op_sel_hi:[1,1,1]
	v_pk_fma_f32 v[8:9], v[234:235], v[144:145], v[8:9] op_sel_hi:[0,1,1]
	v_pk_fma_f32 v[10:11], v[234:235], v[146:147], v[10:11] op_sel_hi:[0,1,1]
	v_pk_fma_f32 v[12:13], v[234:235], v[148:149], v[12:13] op_sel_hi:[0,1,1]
	v_pk_fma_f32 v[14:15], v[234:235], v[150:151], v[14:15] op_sel_hi:[0,1,1]
	v_pk_fma_f32 v[8:9], v[234:235], v[152:153], v[8:9] op_sel:[1,0,0] op_sel_hi:[1,1,1]
	v_pk_fma_f32 v[10:11], v[234:235], v[154:155], v[10:11] op_sel:[1,0,0] op_sel_hi:[1,1,1]
	v_pk_fma_f32 v[12:13], v[234:235], v[156:157], v[12:13] op_sel:[1,0,0] op_sel_hi:[1,1,1]
	v_pk_fma_f32 v[14:15], v[234:235], v[158:159], v[14:15] op_sel:[1,0,0] op_sel_hi:[1,1,1]
	v_pk_fma_f32 v[8:9], v[236:237], v[160:161], v[8:9] op_sel_hi:[0,1,1]
	v_pk_fma_f32 v[10:11], v[236:237], v[162:163], v[10:11] op_sel_hi:[0,1,1]
	v_pk_fma_f32 v[12:13], v[236:237], v[164:165], v[12:13] op_sel_hi:[0,1,1]
	v_pk_fma_f32 v[14:15], v[236:237], v[166:167], v[14:15] op_sel_hi:[0,1,1]
	v_pk_fma_f32 v[8:9], v[236:237], v[168:169], v[8:9] op_sel:[1,0,0] op_sel_hi:[1,1,1]
	v_pk_fma_f32 v[10:11], v[236:237], v[170:171], v[10:11] op_sel:[1,0,0] op_sel_hi:[1,1,1]
	v_pk_fma_f32 v[12:13], v[236:237], v[172:173], v[12:13] op_sel:[1,0,0] op_sel_hi:[1,1,1]
	v_pk_fma_f32 v[14:15], v[236:237], v[174:175], v[14:15] op_sel:[1,0,0] op_sel_hi:[1,1,1]
	v_pk_fma_f32 v[8:9], v[238:239], v[176:177], v[8:9] op_sel_hi:[0,1,1]
	v_pk_fma_f32 v[10:11], v[238:239], v[178:179], v[10:11] op_sel_hi:[0,1,1]
	v_pk_fma_f32 v[12:13], v[238:239], v[180:181], v[12:13] op_sel_hi:[0,1,1]
	v_pk_fma_f32 v[14:15], v[238:239], v[182:183], v[14:15] op_sel_hi:[0,1,1]
	v_pk_fma_f32 v[8:9], v[238:239], v[184:185], v[8:9] op_sel:[1,0,0] op_sel_hi:[1,1,1]
	v_pk_fma_f32 v[10:11], v[238:239], v[186:187], v[10:11] op_sel:[1,0,0] op_sel_hi:[1,1,1]
	v_pk_fma_f32 v[12:13], v[238:239], v[188:189], v[12:13] op_sel:[1,0,0] op_sel_hi:[1,1,1]
	v_pk_fma_f32 v[14:15], v[238:239], v[190:191], v[14:15] op_sel:[1,0,0] op_sel_hi:[1,1,1]
	v_lshlrev_b32_e32 v232, 16, v72
	v_and_b32_e32 v233, s15, v72
	v_lshlrev_b32_e32 v234, 16, v73
	v_and_b32_e32 v235, s15, v73
	v_lshlrev_b32_e32 v236, 16, v74
	v_and_b32_e32 v237, s15, v74
	v_lshlrev_b32_e32 v238, 16, v75
	v_and_b32_e32 v239, s15, v75
	v_pk_fma_f32 v[196:197], v[232:233], v[232:233], v[196:197]
	v_pk_fma_f32 v[196:197], v[234:235], v[234:235], v[196:197]
	v_pk_fma_f32 v[196:197], v[236:237], v[236:237], v[196:197]
	v_pk_fma_f32 v[196:197], v[238:239], v[238:239], v[196:197]
	v_pk_fma_f32 v[16:17], v[232:233], v[128:129], v[16:17] op_sel_hi:[0,1,1]
	v_pk_fma_f32 v[18:19], v[232:233], v[130:131], v[18:19] op_sel_hi:[0,1,1]
	v_pk_fma_f32 v[20:21], v[232:233], v[132:133], v[20:21] op_sel_hi:[0,1,1]
	v_pk_fma_f32 v[22:23], v[232:233], v[134:135], v[22:23] op_sel_hi:[0,1,1]
	v_pk_fma_f32 v[16:17], v[232:233], v[136:137], v[16:17] op_sel:[1,0,0] op_sel_hi:[1,1,1]
	v_pk_fma_f32 v[18:19], v[232:233], v[138:139], v[18:19] op_sel:[1,0,0] op_sel_hi:[1,1,1]
	v_pk_fma_f32 v[20:21], v[232:233], v[140:141], v[20:21] op_sel:[1,0,0] op_sel_hi:[1,1,1]
	v_pk_fma_f32 v[22:23], v[232:233], v[142:143], v[22:23] op_sel:[1,0,0] op_sel_hi:[1,1,1]
	v_pk_fma_f32 v[16:17], v[234:235], v[144:145], v[16:17] op_sel_hi:[0,1,1]
	v_pk_fma_f32 v[18:19], v[234:235], v[146:147], v[18:19] op_sel_hi:[0,1,1]
	v_pk_fma_f32 v[20:21], v[234:235], v[148:149], v[20:21] op_sel_hi:[0,1,1]
	v_pk_fma_f32 v[22:23], v[234:235], v[150:151], v[22:23] op_sel_hi:[0,1,1]
; #define LAS __attribute__((address_space(3)))
; __global__ void __launch_bounds__(NTHR, 2) fwd_kernel(Args args) {
;     ...
;             for (int i = 0; i < 16; ++i) { const int k = 2 * lane + 128 * i; f32x2 rv[8]; unsigned xw[8];
; #pragma unroll
;                 for (int e = 0; e < 8; ++e) rv[e] = *(const LAS f32x2*)(Rg + e * DM + k);
; #pragma unroll
;                 for (int q = 0; q < 8; ++q) xw[q] = *(const unsigned*)(XB + (size_t)(t0 + q) * DM + k);
; #pragma unroll
;                 for (int q = 0; q < 8; ++q) { const float x0 = bflo(xw[q]), x1 = bfhi(xw[q]); ssq[q] += x0 * x0 + x1 * x1;
; #pragma unroll
;                     for (int e = 0; e < 8; ++e) acc[q][e] += x0 * rv[e].x + x1 * rv[e].y; } }
	v_pk_fma_f32 v[16:17], v[234:235], v[152:153], v[16:17] op_sel:[1,0,0] op_sel_hi:[1,1,1]
	v_pk_fma_f32 v[18:19], v[234:235], v[154:155], v[18:19] op_sel:[1,0,0] op_sel_hi:[1,1,1]
	v_pk_fma_f32 v[20:21], v[234:235], v[156:157], v[20:21] op_sel:[1,0,0] op_sel_hi:[1,1,1]
	v_pk_fma_f32 v[22:23], v[234:235], v[158:159], v[22:23] op_sel:[1,0,0] op_sel_hi:[1,1,1]
	v_pk_fma_f32 v[16:17], v[236:237], v[160:161], v[16:17] op_sel_hi:[0,1,1]
	v_pk_fma_f32 v[18:19], v[236:237], v[162:163], v[18:19] op_sel_hi:[0,1,1]
	v_pk_fma_f32 v[20:21], v[236:237], v[164:165], v[20:21] op_sel_hi:[0,1,1]
	v_pk_fma_f32 v[22:23], v[236:237], v[166:167], v[22:23] op_sel_hi:[0,1,1]
	v_pk_fma_f32 v[16:17], v[236:237], v[168:169], v[16:17] op_sel:[1,0,0] op_sel_hi:[1,1,1]
	v_pk_fma_f32 v[18:19], v[236:237], v[170:171], v[18:19] op_sel:[1,0,0] op_sel_hi:[1,1,1]
	v_pk_fma_f32 v[20:21], v[236:237], v[172:173], v[20:21] op_sel:[1,0,0] op_sel_hi:[1,1,1]
	v_pk_fma_f32 v[22:23], v[236:237], v[174:175], v[22:23] op_sel:[1,0,0] op_sel_hi:[1,1,1]
	v_pk_fma_f32 v[16:17], v[238:239], v[176:177], v[16:17] op_sel_hi:[0,1,1]
	v_pk_fma_f32 v[18:19], v[238:239], v[178:179], v[18:19] op_sel_hi:[0,1,1]
	v_pk_fma_f32 v[20:21], v[238:239], v[180:181], v[20:21] op_sel_hi:[0,1,1]
	v_pk_fma_f32 v[22:23], v[238:239], v[182:183], v[22:23] op_sel_hi:[0,1,1]
	v_pk_fma_f32 v[16:17], v[238:239], v[184:185], v[16:17] op_sel:[1,0,0] op_sel_hi:[1,1,1]
	v_pk_fma_f32 v[18:19], v[238:239], v[186:187], v[18:19] op_sel:[1,0,0] op_sel_hi:[1,1,1]
	v_pk_fma_f32 v[20:21], v[238:239], v[188:189], v[20:21] op_sel:[1,0,0] op_sel_hi:[1,1,1]
	v_pk_fma_f32 v[22:23], v[238:239], v[190:191], v[22:23] op_sel:[1,0,0] op_sel_hi:[1,1,1]
	v_lshlrev_b32_e32 v232, 16, v76
	v_and_b32_e32 v233, s15, v76
	v_lshlrev_b32_e32 v234, 16, v77
	v_and_b32_e32 v235, s15, v77
	v_lshlrev_b32_e32 v236, 16, v78
	v_and_b32_e32 v237, s15, v78
	v_lshlrev_b32_e32 v238, 16, v79
	v_and_b32_e32 v239, s15, v79
	v_pk_fma_f32 v[198:199], v[232:233], v[232:233], v[198:199]
	v_pk_fma_f32 v[198:199], v[234:235], v[234:235], v[198:199]
	v_pk_fma_f32 v[198:199], v[236:237], v[236:237], v[198:199]
	v_pk_fma_f32 v[198:199], v[238:239], v[238:239], v[198:199]
	v_pk_fma_f32 v[24:25], v[232:233], v[128:129], v[24:25] op_sel_hi:[0,1,1]
	v_pk_fma_f32 v[26:27], v[232:233], v[130:131], v[26:27] op_sel_hi:[0,1,1]
	v_pk_fma_f32 v[28:29], v[232:233], v[132:133], v[28:29] op_sel_hi:[0,1,1]
	v_pk_fma_f32 v[30:31], v[232:233], v[134:135], v[30:31] op_sel_hi:[0,1,1]
	v_pk_fma_f32 v[24:25], v[232:233], v[136:137], v[24:25] op_sel:[1,0,0] op_sel_hi:[1,1,1]
	v_pk_fma_f32 v[26:27], v[232:233], v[138:139], v[26:27] op_sel:[1,0,0] op_sel_hi:[1,1,1]
	v_pk_fma_f32 v[28:29], v[232:233], v[140:141], v[28:29] op_sel:[1,0,0] op_sel_hi:[1,1,1]
	v_pk_fma_f32 v[30:31], v[232:233], v[142:143], v[30:31] op_sel:[1,0,0] op_sel_hi:[1,1,1]
	v_pk_fma_f32 v[24:25], v[234:235], v[144:145], v[24:25] op_sel_hi:[0,1,1]
	v_pk_fma_f32 v[26:27], v[234:235], v[146:147], v[26:27] op_sel_hi:[0,1,1]
	v_pk_fma_f32 v[28:29], v[234:235], v[148:149], v[28:29] op_sel_hi:[0,1,1]
	v_pk_fma_f32 v[30:31], v[234:235], v[150:151], v[30:31] op_sel_hi:[0,1,1]
	v_pk_fma_f32 v[24:25], v[234:235], v[152:153], v[24:25] op_sel:[1,0,0] op_sel_hi:[1,1,1]
	v_pk_fma_f32 v[26:27], v[234:235], v[154:155], v[26:27] op_sel:[1,0,0] op_sel_hi:[1,1,1]
	v_pk_fma_f32 v[28:29], v[234:235], v[156:157], v[28:29] op_sel:[1,0,0] op_sel_hi:[1,1,1]
	v_pk_fma_f32 v[30:31], v[234:235], v[158:159], v[30:31] op_sel:[1,0,0] op_sel_hi:[1,1,1]
	v_pk_fma_f32 v[24:25], v[236:237], v[160:161], v[24:25] op_sel_hi:[0,1,1]
	v_pk_fma_f32 v[26:27], v[236:237], v[162:163], v[26:27] op_sel_hi:[0,1,1]
	v_pk_fma_f32 v[28:29], v[236:237], v[164:165], v[28:29] op_sel_hi:[0,1,1]
	v_pk_fma_f32 v[30:31], v[236:237], v[166:167], v[30:31] op_sel_hi:[0,1,1]
	v_pk_fma_f32 v[24:25], v[236:237], v[168:169], v[24:25] op_sel:[1,0,0] op_sel_hi:[1,1,1]
	v_pk_fma_f32 v[26:27], v[236:237], v[170:171], v[26:27] op_sel:[1,0,0] op_sel_hi:[1,1,1]
	v_pk_fma_f32 v[28:29], v[236:237], v[172:173], v[28:29] op_sel:[1,0,0] op_sel_hi:[1,1,1]
	v_pk_fma_f32 v[30:31], v[236:237], v[174:175], v[30:31] op_sel:[1,0,0] op_sel_hi:[1,1,1]
	v_pk_fma_f32 v[24:25], v[238:239], v[176:177], v[24:25] op_sel_hi:[0,1,1]
	v_pk_fma_f32 v[26:27], v[238:239], v[178:179], v[26:27] op_sel_hi:[0,1,1]
	v_pk_fma_f32 v[28:29], v[238:239], v[180:181], v[28:29] op_sel_hi:[0,1,1]
	v_pk_fma_f32 v[30:31], v[238:239], v[182:183], v[30:31] op_sel_hi:[0,1,1]
	v_pk_fma_f32 v[24:25], v[238:239], v[184:185], v[24:25] op_sel:[1,0,0] op_sel_hi:[1,1,1]
	v_pk_fma_f32 v[26:27], v[238:239], v[186:187], v[26:27] op_sel:[1,0,0] op_sel_hi:[1,1,1]
	v_pk_fma_f32 v[28:29], v[238:239], v[188:189], v[28:29] op_sel:[1,0,0] op_sel_hi:[1,1,1]
	v_pk_fma_f32 v[30:31], v[238:239], v[190:191], v[30:31] op_sel:[1,0,0] op_sel_hi:[1,1,1]
	v_lshlrev_b32_e32 v232, 16, v80
	v_and_b32_e32 v233, s15, v80
	v_lshlrev_b32_e32 v234, 16, v81
	v_and_b32_e32 v235, s15, v81
	v_lshlrev_b32_e32 v236, 16, v82
	v_and_b32_e32 v237, s15, v82
	v_lshlrev_b32_e32 v238, 16, v83
	v_and_b32_e32 v239, s15, v83
	v_pk_fma_f32 v[200:201], v[232:233], v[232:233], v[200:201]
	v_pk_fma_f32 v[200:201], v[234:235], v[234:235], v[200:201]
	v_pk_fma_f32 v[200:201], v[236:237], v[236:237], v[200:201]
	v_pk_fma_f32 v[200:201], v[238:239], v[238:239], v[200:201]
	v_pk_fma_f32 v[32:33], v[232:233], v[128:129], v[32:33] op_sel_hi:[0,1,1]
	v_pk_fma_f32 v[34:35], v[232:233], v[130:131], v[34:35] op_sel_hi:[0,1,1]
	v_pk_fma_f32 v[36:37], v[232:233], v[132:133], v[36:37] op_sel_hi:[0,1,1]
	v_pk_fma_f32 v[38:39], v[232:233], v[134:135], v[38:39] op_sel_hi:[0,1,1]
; #define LAS __attribute__((address_space(3)))
; __global__ void __launch_bounds__(NTHR, 2) fwd_kernel(Args args) {
;     ...
;             for (int i = 0; i < 16; ++i) { const int k = 2 * lane + 128 * i; f32x2 rv[8]; unsigned xw[8];
; #pragma unroll
;                 for (int e = 0; e < 8; ++e) rv[e] = *(const LAS f32x2*)(Rg + e * DM + k);
; #pragma unroll
;                 for (int q = 0; q < 8; ++q) xw[q] = *(const unsigned*)(XB + (size_t)(t0 + q) * DM + k);
; #pragma unroll
;                 for (int q = 0; q < 8; ++q) { const float x0 = bflo(xw[q]), x1 = bfhi(xw[q]); ssq[q] += x0 * x0 + x1 * x1;
; #pragma unroll
;                     for (int e = 0; e < 8; ++e) acc[q][e] += x0 * rv[e].x + x1 * rv[e].y; } }
	v_pk_fma_f32 v[32:33], v[232:233], v[136:137], v[32:33] op_sel:[1,0,0] op_sel_hi:[1,1,1]
	v_pk_fma_f32 v[34:35], v[232:233], v[138:139], v[34:35] op_sel:[1,0,0] op_sel_hi:[1,1,1]
	v_pk_fma_f32 v[36:37], v[232:233], v[140:141], v[36:37] op_sel:[1,0,0] op_sel_hi:[1,1,1]
	v_pk_fma_f32 v[38:39], v[232:233], v[142:143], v[38:39] op_sel:[1,0,0] op_sel_hi:[1,1,1]
	v_pk_fma_f32 v[32:33], v[234:235], v[144:145], v[32:33] op_sel_hi:[0,1,1]
	v_pk_fma_f32 v[34:35], v[234:235], v[146:147], v[34:35] op_sel_hi:[0,1,1]
	v_pk_fma_f32 v[36:37], v[234:235], v[148:149], v[36:37] op_sel_hi:[0,1,1]
	v_pk_fma_f32 v[38:39], v[234:235], v[150:151], v[38:39] op_sel_hi:[0,1,1]
	v_pk_fma_f32 v[32:33], v[234:235], v[152:153], v[32:33] op_sel:[1,0,0] op_sel_hi:[1,1,1]
	v_pk_fma_f32 v[34:35], v[234:235], v[154:155], v[34:35] op_sel:[1,0,0] op_sel_hi:[1,1,1]
	v_pk_fma_f32 v[36:37], v[234:235], v[156:157], v[36:37] op_sel:[1,0,0] op_sel_hi:[1,1,1]
	v_pk_fma_f32 v[38:39], v[234:235], v[158:159], v[38:39] op_sel:[1,0,0] op_sel_hi:[1,1,1]
	v_pk_fma_f32 v[32:33], v[236:237], v[160:161], v[32:33] op_sel_hi:[0,1,1]
	v_pk_fma_f32 v[34:35], v[236:237], v[162:163], v[34:35] op_sel_hi:[0,1,1]
	v_pk_fma_f32 v[36:37], v[236:237], v[164:165], v[36:37] op_sel_hi:[0,1,1]
	v_pk_fma_f32 v[38:39], v[236:237], v[166:167], v[38:39] op_sel_hi:[0,1,1]
	v_pk_fma_f32 v[32:33], v[236:237], v[168:169], v[32:33] op_sel:[1,0,0] op_sel_hi:[1,1,1]
	v_pk_fma_f32 v[34:35], v[236:237], v[170:171], v[34:35] op_sel:[1,0,0] op_sel_hi:[1,1,1]
	v_pk_fma_f32 v[36:37], v[236:237], v[172:173], v[36:37] op_sel:[1,0,0] op_sel_hi:[1,1,1]
	v_pk_fma_f32 v[38:39], v[236:237], v[174:175], v[38:39] op_sel:[1,0,0] op_sel_hi:[1,1,1]
	v_pk_fma_f32 v[32:33], v[238:239], v[176:177], v[32:33] op_sel_hi:[0,1,1]
	v_pk_fma_f32 v[34:35], v[238:239], v[178:179], v[34:35] op_sel_hi:[0,1,1]
	v_pk_fma_f32 v[36:37], v[238:239], v[180:181], v[36:37] op_sel_hi:[0,1,1]
	v_pk_fma_f32 v[38:39], v[238:239], v[182:183], v[38:39] op_sel_hi:[0,1,1]
	v_pk_fma_f32 v[32:33], v[238:239], v[184:185], v[32:33] op_sel:[1,0,0] op_sel_hi:[1,1,1]
	v_pk_fma_f32 v[34:35], v[238:239], v[186:187], v[34:35] op_sel:[1,0,0] op_sel_hi:[1,1,1]
	v_pk_fma_f32 v[36:37], v[238:239], v[188:189], v[36:37] op_sel:[1,0,0] op_sel_hi:[1,1,1]
	v_pk_fma_f32 v[38:39], v[238:239], v[190:191], v[38:39] op_sel:[1,0,0] op_sel_hi:[1,1,1]
	v_lshlrev_b32_e32 v232, 16, v84
	v_and_b32_e32 v233, s15, v84
	v_lshlrev_b32_e32 v234, 16, v85
	v_and_b32_e32 v235, s15, v85
	v_lshlrev_b32_e32 v236, 16, v86
	v_and_b32_e32 v237, s15, v86
	v_lshlrev_b32_e32 v238, 16, v87
	v_and_b32_e32 v239, s15, v87
	v_pk_fma_f32 v[202:203], v[232:233], v[232:233], v[202:203]
	v_pk_fma_f32 v[202:203], v[234:235], v[234:235], v[202:203]
	v_pk_fma_f32 v[202:203], v[236:237], v[236:237], v[202:203]
	v_pk_fma_f32 v[202:203], v[238:239], v[238:239], v[202:203]
	v_pk_fma_f32 v[40:41], v[232:233], v[128:129], v[40:41] op_sel_hi:[0,1,1]
	v_pk_fma_f32 v[42:43], v[232:233], v[130:131], v[42:43] op_sel_hi:[0,1,1]
	v_pk_fma_f32 v[44:45], v[232:233], v[132:133], v[44:45] op_sel_hi:[0,1,1]
	v_pk_fma_f32 v[46:47], v[232:233], v[134:135], v[46:47] op_sel_hi:[0,1,1]
	v_pk_fma_f32 v[40:41], v[232:233], v[136:137], v[40:41] op_sel:[1,0,0] op_sel_hi:[1,1,1]
	v_pk_fma_f32 v[42:43], v[232:233], v[138:139], v[42:43] op_sel:[1,0,0] op_sel_hi:[1,1,1]
	v_pk_fma_f32 v[44:45], v[232:233], v[140:141], v[44:45] op_sel:[1,0,0] op_sel_hi:[1,1,1]
	v_pk_fma_f32 v[46:47], v[232:233], v[142:143], v[46:47] op_sel:[1,0,0] op_sel_hi:[1,1,1]
	v_pk_fma_f32 v[40:41], v[234:235], v[144:145], v[40:41] op_sel_hi:[0,1,1]
	v_pk_fma_f32 v[42:43], v[234:235], v[146:147], v[42:43] op_sel_hi:[0,1,1]
	v_pk_fma_f32 v[44:45], v[234:235], v[148:149], v[44:45] op_sel_hi:[0,1,1]
	v_pk_fma_f32 v[46:47], v[234:235], v[150:151], v[46:47] op_sel_hi:[0,1,1]
	v_pk_fma_f32 v[40:41], v[234:235], v[152:153], v[40:41] op_sel:[1,0,0] op_sel_hi:[1,1,1]
	v_pk_fma_f32 v[42:43], v[234:235], v[154:155], v[42:43] op_sel:[1,0,0] op_sel_hi:[1,1,1]
	v_pk_fma_f32 v[44:45], v[234:235], v[156:157], v[44:45] op_sel:[1,0,0] op_sel_hi:[1,1,1]
	v_pk_fma_f32 v[46:47], v[234:235], v[158:159], v[46:47] op_sel:[1,0,0] op_sel_hi:[1,1,1]
	v_pk_fma_f32 v[40:41], v[236:237], v[160:161], v[40:41] op_sel_hi:[0,1,1]
	v_pk_fma_f32 v[42:43], v[236:237], v[162:163], v[42:43] op_sel_hi:[0,1,1]
	v_pk_fma_f32 v[44:45], v[236:237], v[164:165], v[44:45] op_sel_hi:[0,1,1]
	v_pk_fma_f32 v[46:47], v[236:237], v[166:167], v[46:47] op_sel_hi:[0,1,1]
	v_pk_fma_f32 v[40:41], v[236:237], v[168:169], v[40:41] op_sel:[1,0,0] op_sel_hi:[1,1,1]
	v_pk_fma_f32 v[42:43], v[236:237], v[170:171], v[42:43] op_sel:[1,0,0] op_sel_hi:[1,1,1]
	v_pk_fma_f32 v[44:45], v[236:237], v[172:173], v[44:45] op_sel:[1,0,0] op_sel_hi:[1,1,1]
	v_pk_fma_f32 v[46:47], v[236:237], v[174:175], v[46:47] op_sel:[1,0,0] op_sel_hi:[1,1,1]
	v_pk_fma_f32 v[40:41], v[238:239], v[176:177], v[40:41] op_sel_hi:[0,1,1]
	v_pk_fma_f32 v[42:43], v[238:239], v[178:179], v[42:43] op_sel_hi:[0,1,1]
	v_pk_fma_f32 v[44:45], v[238:239], v[180:181], v[44:45] op_sel_hi:[0,1,1]
	v_pk_fma_f32 v[46:47], v[238:239], v[182:183], v[46:47] op_sel_hi:[0,1,1]
	v_pk_fma_f32 v[40:41], v[238:239], v[184:185], v[40:41] op_sel:[1,0,0] op_sel_hi:[1,1,1]
	v_pk_fma_f32 v[42:43], v[238:239], v[186:187], v[42:43] op_sel:[1,0,0] op_sel_hi:[1,1,1]
	v_pk_fma_f32 v[44:45], v[238:239], v[188:189], v[44:45] op_sel:[1,0,0] op_sel_hi:[1,1,1]
	v_pk_fma_f32 v[46:47], v[238:239], v[190:191], v[46:47] op_sel:[1,0,0] op_sel_hi:[1,1,1]
	v_lshlrev_b32_e32 v232, 16, v88
	v_and_b32_e32 v233, s15, v88
	v_lshlrev_b32_e32 v234, 16, v89
	v_and_b32_e32 v235, s15, v89
	v_lshlrev_b32_e32 v236, 16, v90
; #define LAS __attribute__((address_space(3)))
; __global__ void __launch_bounds__(NTHR, 2) fwd_kernel(Args args) {
;     ...
;             for (int i = 0; i < 16; ++i) { const int k = 2 * lane + 128 * i; f32x2 rv[8]; unsigned xw[8];
; #pragma unroll
;                 for (int e = 0; e < 8; ++e) rv[e] = *(const LAS f32x2*)(Rg + e * DM + k);
; #pragma unroll
;                 for (int q = 0; q < 8; ++q) xw[q] = *(const unsigned*)(XB + (size_t)(t0 + q) * DM + k);
; #pragma unroll
;                 for (int q = 0; q < 8; ++q) { const float x0 = bflo(xw[q]), x1 = bfhi(xw[q]); ssq[q] += x0 * x0 + x1 * x1;
; #pragma unroll
;                     for (int e = 0; e < 8; ++e) acc[q][e] += x0 * rv[e].x + x1 * rv[e].y; } }
	v_and_b32_e32 v237, s15, v90
	v_lshlrev_b32_e32 v238, 16, v91
	v_and_b32_e32 v239, s15, v91
	v_pk_fma_f32 v[204:205], v[232:233], v[232:233], v[204:205]
	v_pk_fma_f32 v[204:205], v[234:235], v[234:235], v[204:205]
	v_pk_fma_f32 v[204:205], v[236:237], v[236:237], v[204:205]
	v_pk_fma_f32 v[204:205], v[238:239], v[238:239], v[204:205]
	v_pk_fma_f32 v[48:49], v[232:233], v[128:129], v[48:49] op_sel_hi:[0,1,1]
	v_pk_fma_f32 v[50:51], v[232:233], v[130:131], v[50:51] op_sel_hi:[0,1,1]
	v_pk_fma_f32 v[52:53], v[232:233], v[132:133], v[52:53] op_sel_hi:[0,1,1]
	v_pk_fma_f32 v[54:55], v[232:233], v[134:135], v[54:55] op_sel_hi:[0,1,1]
	v_pk_fma_f32 v[48:49], v[232:233], v[136:137], v[48:49] op_sel:[1,0,0] op_sel_hi:[1,1,1]
	v_pk_fma_f32 v[50:51], v[232:233], v[138:139], v[50:51] op_sel:[1,0,0] op_sel_hi:[1,1,1]
	v_pk_fma_f32 v[52:53], v[232:233], v[140:141], v[52:53] op_sel:[1,0,0] op_sel_hi:[1,1,1]
	v_pk_fma_f32 v[54:55], v[232:233], v[142:143], v[54:55] op_sel:[1,0,0] op_sel_hi:[1,1,1]
	v_pk_fma_f32 v[48:49], v[234:235], v[144:145], v[48:49] op_sel_hi:[0,1,1]
	v_pk_fma_f32 v[50:51], v[234:235], v[146:147], v[50:51] op_sel_hi:[0,1,1]
	v_pk_fma_f32 v[52:53], v[234:235], v[148:149], v[52:53] op_sel_hi:[0,1,1]
	v_pk_fma_f32 v[54:55], v[234:235], v[150:151], v[54:55] op_sel_hi:[0,1,1]
	v_pk_fma_f32 v[48:49], v[234:235], v[152:153], v[48:49] op_sel:[1,0,0] op_sel_hi:[1,1,1]
	v_pk_fma_f32 v[50:51], v[234:235], v[154:155], v[50:51] op_sel:[1,0,0] op_sel_hi:[1,1,1]
	v_pk_fma_f32 v[52:53], v[234:235], v[156:157], v[52:53] op_sel:[1,0,0] op_sel_hi:[1,1,1]
	v_pk_fma_f32 v[54:55], v[234:235], v[158:159], v[54:55] op_sel:[1,0,0] op_sel_hi:[1,1,1]
	v_pk_fma_f32 v[48:49], v[236:237], v[160:161], v[48:49] op_sel_hi:[0,1,1]
	v_pk_fma_f32 v[50:51], v[236:237], v[162:163], v[50:51] op_sel_hi:[0,1,1]
	v_pk_fma_f32 v[52:53], v[236:237], v[164:165], v[52:53] op_sel_hi:[0,1,1]
	v_pk_fma_f32 v[54:55], v[236:237], v[166:167], v[54:55] op_sel_hi:[0,1,1]
	v_pk_fma_f32 v[48:49], v[236:237], v[168:169], v[48:49] op_sel:[1,0,0] op_sel_hi:[1,1,1]
	v_pk_fma_f32 v[50:51], v[236:237], v[170:171], v[50:51] op_sel:[1,0,0] op_sel_hi:[1,1,1]
	v_pk_fma_f32 v[52:53], v[236:237], v[172:173], v[52:53] op_sel:[1,0,0] op_sel_hi:[1,1,1]
	v_pk_fma_f32 v[54:55], v[236:237], v[174:175], v[54:55] op_sel:[1,0,0] op_sel_hi:[1,1,1]
	v_pk_fma_f32 v[48:49], v[238:239], v[176:177], v[48:49] op_sel_hi:[0,1,1]
	v_pk_fma_f32 v[50:51], v[238:239], v[178:179], v[50:51] op_sel_hi:[0,1,1]
	v_pk_fma_f32 v[52:53], v[238:239], v[180:181], v[52:53] op_sel_hi:[0,1,1]
	v_pk_fma_f32 v[54:55], v[238:239], v[182:183], v[54:55] op_sel_hi:[0,1,1]
	v_pk_fma_f32 v[48:49], v[238:239], v[184:185], v[48:49] op_sel:[1,0,0] op_sel_hi:[1,1,1]
	v_pk_fma_f32 v[50:51], v[238:239], v[186:187], v[50:51] op_sel:[1,0,0] op_sel_hi:[1,1,1]
	v_pk_fma_f32 v[52:53], v[238:239], v[188:189], v[52:53] op_sel:[1,0,0] op_sel_hi:[1,1,1]
	v_pk_fma_f32 v[54:55], v[238:239], v[190:191], v[54:55] op_sel:[1,0,0] op_sel_hi:[1,1,1]
	v_lshlrev_b32_e32 v232, 16, v92
	v_and_b32_e32 v233, s15, v92
	v_lshlrev_b32_e32 v234, 16, v93
	v_and_b32_e32 v235, s15, v93
	v_lshlrev_b32_e32 v236, 16, v94
	v_and_b32_e32 v237, s15, v94
	v_lshlrev_b32_e32 v238, 16, v95
	v_and_b32_e32 v239, s15, v95
	v_pk_fma_f32 v[206:207], v[232:233], v[232:233], v[206:207]
	v_pk_fma_f32 v[206:207], v[234:235], v[234:235], v[206:207]
	v_pk_fma_f32 v[206:207], v[236:237], v[236:237], v[206:207]
	v_pk_fma_f32 v[206:207], v[238:239], v[238:239], v[206:207]
	v_pk_fma_f32 v[56:57], v[232:233], v[128:129], v[56:57] op_sel_hi:[0,1,1]
	v_pk_fma_f32 v[58:59], v[232:233], v[130:131], v[58:59] op_sel_hi:[0,1,1]
	v_pk_fma_f32 v[60:61], v[232:233], v[132:133], v[60:61] op_sel_hi:[0,1,1]
	v_pk_fma_f32 v[62:63], v[232:233], v[134:135], v[62:63] op_sel_hi:[0,1,1]
	v_pk_fma_f32 v[56:57], v[232:233], v[136:137], v[56:57] op_sel:[1,0,0] op_sel_hi:[1,1,1]
	v_pk_fma_f32 v[58:59], v[232:233], v[138:139], v[58:59] op_sel:[1,0,0] op_sel_hi:[1,1,1]
	v_pk_fma_f32 v[60:61], v[232:233], v[140:141], v[60:61] op_sel:[1,0,0] op_sel_hi:[1,1,1]
	v_pk_fma_f32 v[62:63], v[232:233], v[142:143], v[62:63] op_sel:[1,0,0] op_sel_hi:[1,1,1]
	v_pk_fma_f32 v[56:57], v[234:235], v[144:145], v[56:57] op_sel_hi:[0,1,1]
	v_pk_fma_f32 v[58:59], v[234:235], v[146:147], v[58:59] op_sel_hi:[0,1,1]
	v_pk_fma_f32 v[60:61], v[234:235], v[148:149], v[60:61] op_sel_hi:[0,1,1]
	v_pk_fma_f32 v[62:63], v[234:235], v[150:151], v[62:63] op_sel_hi:[0,1,1]
	v_pk_fma_f32 v[56:57], v[234:235], v[152:153], v[56:57] op_sel:[1,0,0] op_sel_hi:[1,1,1]
	v_pk_fma_f32 v[58:59], v[234:235], v[154:155], v[58:59] op_sel:[1,0,0] op_sel_hi:[1,1,1]
	v_pk_fma_f32 v[60:61], v[234:235], v[156:157], v[60:61] op_sel:[1,0,0] op_sel_hi:[1,1,1]
	v_pk_fma_f32 v[62:63], v[234:235], v[158:159], v[62:63] op_sel:[1,0,0] op_sel_hi:[1,1,1]
	v_pk_fma_f32 v[56:57], v[236:237], v[160:161], v[56:57] op_sel_hi:[0,1,1]
	v_pk_fma_f32 v[58:59], v[236:237], v[162:163], v[58:59] op_sel_hi:[0,1,1]
	v_pk_fma_f32 v[60:61], v[236:237], v[164:165], v[60:61] op_sel_hi:[0,1,1]
	v_pk_fma_f32 v[62:63], v[236:237], v[166:167], v[62:63] op_sel_hi:[0,1,1]
	v_pk_fma_f32 v[56:57], v[236:237], v[168:169], v[56:57] op_sel:[1,0,0] op_sel_hi:[1,1,1]
	v_pk_fma_f32 v[58:59], v[236:237], v[170:171], v[58:59] op_sel:[1,0,0] op_sel_hi:[1,1,1]
	v_pk_fma_f32 v[60:61], v[236:237], v[172:173], v[60:61] op_sel:[1,0,0] op_sel_hi:[1,1,1]
	v_pk_fma_f32 v[62:63], v[236:237], v[174:175], v[62:63] op_sel:[1,0,0] op_sel_hi:[1,1,1]
	v_pk_fma_f32 v[56:57], v[238:239], v[176:177], v[56:57] op_sel_hi:[0,1,1]
	v_pk_fma_f32 v[58:59], v[238:239], v[178:179], v[58:59] op_sel_hi:[0,1,1]
	v_pk_fma_f32 v[60:61], v[238:239], v[180:181], v[60:61] op_sel_hi:[0,1,1]
	v_pk_fma_f32 v[62:63], v[238:239], v[182:183], v[62:63] op_sel_hi:[0,1,1]
	v_pk_fma_f32 v[56:57], v[238:239], v[184:185], v[56:57] op_sel:[1,0,0] op_sel_hi:[1,1,1]
	v_pk_fma_f32 v[58:59], v[238:239], v[186:187], v[58:59] op_sel:[1,0,0] op_sel_hi:[1,1,1]
	v_pk_fma_f32 v[60:61], v[238:239], v[188:189], v[60:61] op_sel:[1,0,0] op_sel_hi:[1,1,1]
	v_pk_fma_f32 v[62:63], v[238:239], v[190:191], v[62:63] op_sel:[1,0,0] op_sel_hi:[1,1,1]
	ds_read_b128 v[128:131], v208 offset:49152
	ds_read_b128 v[132:135], v208 offset:50176
	ds_read_b128 v[136:139], v208 offset:51200
	ds_read_b128 v[140:143], v208 offset:52224
	ds_read_b128 v[144:147], v208 offset:53248
	ds_read_b128 v[148:151], v208 offset:54272
	ds_read_b128 v[152:155], v208 offset:55296
	ds_read_b128 v[156:159], v208 offset:56320
	ds_read_b128 v[160:163], v208 offset:57344
	ds_read_b128 v[164:167], v208 offset:58368
	ds_read_b128 v[168:171], v208 offset:59392
	ds_read_b128 v[172:175], v208 offset:60416
	ds_read_b128 v[176:179], v208 offset:61440
	ds_read_b128 v[180:183], v208 offset:62464
	ds_read_b128 v[184:187], v208 offset:63488
	ds_read_b128 v[188:191], v208 offset:64512
	s_waitcnt vmcnt(0)
; #define LAS __attribute__((address_space(3)))
; __global__ void __launch_bounds__(NTHR, 2) fwd_kernel(Args args) {
;     ...
;             for (int i = 0; i < 16; ++i) { const int k = 2 * lane + 128 * i; f32x2 rv[8]; unsigned xw[8];
; #pragma unroll
;                 for (int e = 0; e < 8; ++e) rv[e] = *(const LAS f32x2*)(Rg + e * DM + k);
; #pragma unroll
;                 for (int q = 0; q < 8; ++q) xw[q] = *(const unsigned*)(XB + (size_t)(t0 + q) * DM + k);
; #pragma unroll
;                 for (int q = 0; q < 8; ++q) { const float x0 = bflo(xw[q]), x1 = bfhi(xw[q]); ssq[q] += x0 * x0 + x1 * x1;
; #pragma unroll
;                     for (int e = 0; e < 8; ++e) acc[q][e] += x0 * rv[e].x + x1 * rv[e].y; } }
	s_waitcnt lgkmcnt(0)
	v_lshlrev_b32_e32 v232, 16, v96
	v_and_b32_e32 v233, s15, v96
	v_lshlrev_b32_e32 v234, 16, v97
	v_and_b32_e32 v235, s15, v97
	v_lshlrev_b32_e32 v236, 16, v98
	v_and_b32_e32 v237, s15, v98
	v_lshlrev_b32_e32 v238, 16, v99
	v_and_b32_e32 v239, s15, v99
	v_pk_fma_f32 v[192:193], v[232:233], v[232:233], v[192:193]
	v_pk_fma_f32 v[192:193], v[234:235], v[234:235], v[192:193]
	v_pk_fma_f32 v[192:193], v[236:237], v[236:237], v[192:193]
	v_pk_fma_f32 v[192:193], v[238:239], v[238:239], v[192:193]
	v_pk_fma_f32 v[0:1], v[232:233], v[128:129], v[0:1] op_sel_hi:[0,1,1]
	v_pk_fma_f32 v[2:3], v[232:233], v[130:131], v[2:3] op_sel_hi:[0,1,1]
	v_pk_fma_f32 v[4:5], v[232:233], v[132:133], v[4:5] op_sel_hi:[0,1,1]
	v_pk_fma_f32 v[6:7], v[232:233], v[134:135], v[6:7] op_sel_hi:[0,1,1]
	v_pk_fma_f32 v[0:1], v[232:233], v[136:137], v[0:1] op_sel:[1,0,0] op_sel_hi:[1,1,1]
	v_pk_fma_f32 v[2:3], v[232:233], v[138:139], v[2:3] op_sel:[1,0,0] op_sel_hi:[1,1,1]
	v_pk_fma_f32 v[4:5], v[232:233], v[140:141], v[4:5] op_sel:[1,0,0] op_sel_hi:[1,1,1]
	v_pk_fma_f32 v[6:7], v[232:233], v[142:143], v[6:7] op_sel:[1,0,0] op_sel_hi:[1,1,1]
	v_pk_fma_f32 v[0:1], v[234:235], v[144:145], v[0:1] op_sel_hi:[0,1,1]
	v_pk_fma_f32 v[2:3], v[234:235], v[146:147], v[2:3] op_sel_hi:[0,1,1]
	v_pk_fma_f32 v[4:5], v[234:235], v[148:149], v[4:5] op_sel_hi:[0,1,1]
	v_pk_fma_f32 v[6:7], v[234:235], v[150:151], v[6:7] op_sel_hi:[0,1,1]
	v_pk_fma_f32 v[0:1], v[234:235], v[152:153], v[0:1] op_sel:[1,0,0] op_sel_hi:[1,1,1]
	v_pk_fma_f32 v[2:3], v[234:235], v[154:155], v[2:3] op_sel:[1,0,0] op_sel_hi:[1,1,1]
	v_pk_fma_f32 v[4:5], v[234:235], v[156:157], v[4:5] op_sel:[1,0,0] op_sel_hi:[1,1,1]
	v_pk_fma_f32 v[6:7], v[234:235], v[158:159], v[6:7] op_sel:[1,0,0] op_sel_hi:[1,1,1]
	v_pk_fma_f32 v[0:1], v[236:237], v[160:161], v[0:1] op_sel_hi:[0,1,1]
	v_pk_fma_f32 v[2:3], v[236:237], v[162:163], v[2:3] op_sel_hi:[0,1,1]
	v_pk_fma_f32 v[4:5], v[236:237], v[164:165], v[4:5] op_sel_hi:[0,1,1]
	v_pk_fma_f32 v[6:7], v[236:237], v[166:167], v[6:7] op_sel_hi:[0,1,1]
	v_pk_fma_f32 v[0:1], v[236:237], v[168:169], v[0:1] op_sel:[1,0,0] op_sel_hi:[1,1,1]
	v_pk_fma_f32 v[2:3], v[236:237], v[170:171], v[2:3] op_sel:[1,0,0] op_sel_hi:[1,1,1]
	v_pk_fma_f32 v[4:5], v[236:237], v[172:173], v[4:5] op_sel:[1,0,0] op_sel_hi:[1,1,1]
	v_pk_fma_f32 v[6:7], v[236:237], v[174:175], v[6:7] op_sel:[1,0,0] op_sel_hi:[1,1,1]
	v_pk_fma_f32 v[0:1], v[238:239], v[176:177], v[0:1] op_sel_hi:[0,1,1]
	v_pk_fma_f32 v[2:3], v[238:239], v[178:179], v[2:3] op_sel_hi:[0,1,1]
	v_pk_fma_f32 v[4:5], v[238:239], v[180:181], v[4:5] op_sel_hi:[0,1,1]
	v_pk_fma_f32 v[6:7], v[238:239], v[182:183], v[6:7] op_sel_hi:[0,1,1]
	v_pk_fma_f32 v[0:1], v[238:239], v[184:185], v[0:1] op_sel:[1,0,0] op_sel_hi:[1,1,1]
	v_pk_fma_f32 v[2:3], v[238:239], v[186:187], v[2:3] op_sel:[1,0,0] op_sel_hi:[1,1,1]
	v_pk_fma_f32 v[4:5], v[238:239], v[188:189], v[4:5] op_sel:[1,0,0] op_sel_hi:[1,1,1]
	v_pk_fma_f32 v[6:7], v[238:239], v[190:191], v[6:7] op_sel:[1,0,0] op_sel_hi:[1,1,1]
	v_lshlrev_b32_e32 v232, 16, v100
	v_and_b32_e32 v233, s15, v100
	v_lshlrev_b32_e32 v234, 16, v101
	v_and_b32_e32 v235, s15, v101
	v_lshlrev_b32_e32 v236, 16, v102
	v_and_b32_e32 v237, s15, v102
	v_lshlrev_b32_e32 v238, 16, v103
	v_and_b32_e32 v239, s15, v103
	v_pk_fma_f32 v[194:195], v[232:233], v[232:233], v[194:195]
	v_pk_fma_f32 v[194:195], v[234:235], v[234:235], v[194:195]
	v_pk_fma_f32 v[194:195], v[236:237], v[236:237], v[194:195]
	v_pk_fma_f32 v[194:195], v[238:239], v[238:239], v[194:195]
	v_pk_fma_f32 v[8:9], v[232:233], v[128:129], v[8:9] op_sel_hi:[0,1,1]
	v_pk_fma_f32 v[10:11], v[232:233], v[130:131], v[10:11] op_sel_hi:[0,1,1]
	v_pk_fma_f32 v[12:13], v[232:233], v[132:133], v[12:13] op_sel_hi:[0,1,1]
	v_pk_fma_f32 v[14:15], v[232:233], v[134:135], v[14:15] op_sel_hi:[0,1,1]
	v_pk_fma_f32 v[8:9], v[232:233], v[136:137], v[8:9] op_sel:[1,0,0] op_sel_hi:[1,1,1]
	v_pk_fma_f32 v[10:11], v[232:233], v[138:139], v[10:11] op_sel:[1,0,0] op_sel_hi:[1,1,1]
	v_pk_fma_f32 v[12:13], v[232:233], v[140:141], v[12:13] op_sel:[1,0,0] op_sel_hi:[1,1,1]
	v_pk_fma_f32 v[14:15], v[232:233], v[142:143], v[14:15] op_sel:[1,0,0] op_sel_hi:[1,1,1]
	v_pk_fma_f32 v[8:9], v[234:235], v[144:145], v[8:9] op_sel_hi:[0,1,1]
	v_pk_fma_f32 v[10:11], v[234:235], v[146:147], v[10:11] op_sel_hi:[0,1,1]
	v_pk_fma_f32 v[12:13], v[234:235], v[148:149], v[12:13] op_sel_hi:[0,1,1]
	v_pk_fma_f32 v[14:15], v[234:235], v[150:151], v[14:15] op_sel_hi:[0,1,1]
	v_pk_fma_f32 v[8:9], v[234:235], v[152:153], v[8:9] op_sel:[1,0,0] op_sel_hi:[1,1,1]
	v_pk_fma_f32 v[10:11], v[234:235], v[154:155], v[10:11] op_sel:[1,0,0] op_sel_hi:[1,1,1]
	v_pk_fma_f32 v[12:13], v[234:235], v[156:157], v[12:13] op_sel:[1,0,0] op_sel_hi:[1,1,1]
	v_pk_fma_f32 v[14:15], v[234:235], v[158:159], v[14:15] op_sel:[1,0,0] op_sel_hi:[1,1,1]
	v_pk_fma_f32 v[8:9], v[236:237], v[160:161], v[8:9] op_sel_hi:[0,1,1]
	v_pk_fma_f32 v[10:11], v[236:237], v[162:163], v[10:11] op_sel_hi:[0,1,1]
	v_pk_fma_f32 v[12:13], v[236:237], v[164:165], v[12:13] op_sel_hi:[0,1,1]
	v_pk_fma_f32 v[14:15], v[236:237], v[166:167], v[14:15] op_sel_hi:[0,1,1]
	v_pk_fma_f32 v[8:9], v[236:237], v[168:169], v[8:9] op_sel:[1,0,0] op_sel_hi:[1,1,1]
	v_pk_fma_f32 v[10:11], v[236:237], v[170:171], v[10:11] op_sel:[1,0,0] op_sel_hi:[1,1,1]
	v_pk_fma_f32 v[12:13], v[236:237], v[172:173], v[12:13] op_sel:[1,0,0] op_sel_hi:[1,1,1]
	v_pk_fma_f32 v[14:15], v[236:237], v[174:175], v[14:15] op_sel:[1,0,0] op_sel_hi:[1,1,1]
	v_pk_fma_f32 v[8:9], v[238:239], v[176:177], v[8:9] op_sel_hi:[0,1,1]
	v_pk_fma_f32 v[10:11], v[238:239], v[178:179], v[10:11] op_sel_hi:[0,1,1]
; #define LAS __attribute__((address_space(3)))
; __global__ void __launch_bounds__(NTHR, 2) fwd_kernel(Args args) {
;     ...
;             for (int i = 0; i < 16; ++i) { const int k = 2 * lane + 128 * i; f32x2 rv[8]; unsigned xw[8];
; #pragma unroll
;                 for (int e = 0; e < 8; ++e) rv[e] = *(const LAS f32x2*)(Rg + e * DM + k);
; #pragma unroll
;                 for (int q = 0; q < 8; ++q) xw[q] = *(const unsigned*)(XB + (size_t)(t0 + q) * DM + k);
; #pragma unroll
;                 for (int q = 0; q < 8; ++q) { const float x0 = bflo(xw[q]), x1 = bfhi(xw[q]); ssq[q] += x0 * x0 + x1 * x1;
; #pragma unroll
;                     for (int e = 0; e < 8; ++e) acc[q][e] += x0 * rv[e].x + x1 * rv[e].y; } }
	v_pk_fma_f32 v[12:13], v[238:239], v[180:181], v[12:13] op_sel_hi:[0,1,1]
	v_pk_fma_f32 v[14:15], v[238:239], v[182:183], v[14:15] op_sel_hi:[0,1,1]
	v_pk_fma_f32 v[8:9], v[238:239], v[184:185], v[8:9] op_sel:[1,0,0] op_sel_hi:[1,1,1]
	v_pk_fma_f32 v[10:11], v[238:239], v[186:187], v[10:11] op_sel:[1,0,0] op_sel_hi:[1,1,1]
	v_pk_fma_f32 v[12:13], v[238:239], v[188:189], v[12:13] op_sel:[1,0,0] op_sel_hi:[1,1,1]
	v_pk_fma_f32 v[14:15], v[238:239], v[190:191], v[14:15] op_sel:[1,0,0] op_sel_hi:[1,1,1]
	v_lshlrev_b32_e32 v232, 16, v104
	v_and_b32_e32 v233, s15, v104
	v_lshlrev_b32_e32 v234, 16, v105
	v_and_b32_e32 v235, s15, v105
	v_lshlrev_b32_e32 v236, 16, v106
	v_and_b32_e32 v237, s15, v106
	v_lshlrev_b32_e32 v238, 16, v107
	v_and_b32_e32 v239, s15, v107
	v_pk_fma_f32 v[196:197], v[232:233], v[232:233], v[196:197]
	v_pk_fma_f32 v[196:197], v[234:235], v[234:235], v[196:197]
	v_pk_fma_f32 v[196:197], v[236:237], v[236:237], v[196:197]
	v_pk_fma_f32 v[196:197], v[238:239], v[238:239], v[196:197]
	v_pk_fma_f32 v[16:17], v[232:233], v[128:129], v[16:17] op_sel_hi:[0,1,1]
	v_pk_fma_f32 v[18:19], v[232:233], v[130:131], v[18:19] op_sel_hi:[0,1,1]
	v_pk_fma_f32 v[20:21], v[232:233], v[132:133], v[20:21] op_sel_hi:[0,1,1]
	v_pk_fma_f32 v[22:23], v[232:233], v[134:135], v[22:23] op_sel_hi:[0,1,1]
	v_pk_fma_f32 v[16:17], v[232:233], v[136:137], v[16:17] op_sel:[1,0,0] op_sel_hi:[1,1,1]
	v_pk_fma_f32 v[18:19], v[232:233], v[138:139], v[18:19] op_sel:[1,0,0] op_sel_hi:[1,1,1]
	v_pk_fma_f32 v[20:21], v[232:233], v[140:141], v[20:21] op_sel:[1,0,0] op_sel_hi:[1,1,1]
	v_pk_fma_f32 v[22:23], v[232:233], v[142:143], v[22:23] op_sel:[1,0,0] op_sel_hi:[1,1,1]
	v_pk_fma_f32 v[16:17], v[234:235], v[144:145], v[16:17] op_sel_hi:[0,1,1]
	v_pk_fma_f32 v[18:19], v[234:235], v[146:147], v[18:19] op_sel_hi:[0,1,1]
	v_pk_fma_f32 v[20:21], v[234:235], v[148:149], v[20:21] op_sel_hi:[0,1,1]
	v_pk_fma_f32 v[22:23], v[234:235], v[150:151], v[22:23] op_sel_hi:[0,1,1]
	v_pk_fma_f32 v[16:17], v[234:235], v[152:153], v[16:17] op_sel:[1,0,0] op_sel_hi:[1,1,1]
	v_pk_fma_f32 v[18:19], v[234:235], v[154:155], v[18:19] op_sel:[1,0,0] op_sel_hi:[1,1,1]
	v_pk_fma_f32 v[20:21], v[234:235], v[156:157], v[20:21] op_sel:[1,0,0] op_sel_hi:[1,1,1]
	v_pk_fma_f32 v[22:23], v[234:235], v[158:159], v[22:23] op_sel:[1,0,0] op_sel_hi:[1,1,1]
	v_pk_fma_f32 v[16:17], v[236:237], v[160:161], v[16:17] op_sel_hi:[0,1,1]
	v_pk_fma_f32 v[18:19], v[236:237], v[162:163], v[18:19] op_sel_hi:[0,1,1]
	v_pk_fma_f32 v[20:21], v[236:237], v[164:165], v[20:21] op_sel_hi:[0,1,1]
	v_pk_fma_f32 v[22:23], v[236:237], v[166:167], v[22:23] op_sel_hi:[0,1,1]
	v_pk_fma_f32 v[16:17], v[236:237], v[168:169], v[16:17] op_sel:[1,0,0] op_sel_hi:[1,1,1]
	v_pk_fma_f32 v[18:19], v[236:237], v[170:171], v[18:19] op_sel:[1,0,0] op_sel_hi:[1,1,1]
	v_pk_fma_f32 v[20:21], v[236:237], v[172:173], v[20:21] op_sel:[1,0,0] op_sel_hi:[1,1,1]
	v_pk_fma_f32 v[22:23], v[236:237], v[174:175], v[22:23] op_sel:[1,0,0] op_sel_hi:[1,1,1]
	v_pk_fma_f32 v[16:17], v[238:239], v[176:177], v[16:17] op_sel_hi:[0,1,1]
	v_pk_fma_f32 v[18:19], v[238:239], v[178:179], v[18:19] op_sel_hi:[0,1,1]
	v_pk_fma_f32 v[20:21], v[238:239], v[180:181], v[20:21] op_sel_hi:[0,1,1]
	v_pk_fma_f32 v[22:23], v[238:239], v[182:183], v[22:23] op_sel_hi:[0,1,1]
	v_pk_fma_f32 v[16:17], v[238:239], v[184:185], v[16:17] op_sel:[1,0,0] op_sel_hi:[1,1,1]
	v_pk_fma_f32 v[18:19], v[238:239], v[186:187], v[18:19] op_sel:[1,0,0] op_sel_hi:[1,1,1]
	v_pk_fma_f32 v[20:21], v[238:239], v[188:189], v[20:21] op_sel:[1,0,0] op_sel_hi:[1,1,1]
	v_pk_fma_f32 v[22:23], v[238:239], v[190:191], v[22:23] op_sel:[1,0,0] op_sel_hi:[1,1,1]
	v_lshlrev_b32_e32 v232, 16, v108
	v_and_b32_e32 v233, s15, v108
	v_lshlrev_b32_e32 v234, 16, v109
	v_and_b32_e32 v235, s15, v109
	v_lshlrev_b32_e32 v236, 16, v110
	v_and_b32_e32 v237, s15, v110
	v_lshlrev_b32_e32 v238, 16, v111
	v_and_b32_e32 v239, s15, v111
	v_pk_fma_f32 v[198:199], v[232:233], v[232:233], v[198:199]
	v_pk_fma_f32 v[198:199], v[234:235], v[234:235], v[198:199]
	v_pk_fma_f32 v[198:199], v[236:237], v[236:237], v[198:199]
	v_pk_fma_f32 v[198:199], v[238:239], v[238:239], v[198:199]
	v_pk_fma_f32 v[24:25], v[232:233], v[128:129], v[24:25] op_sel_hi:[0,1,1]
	v_pk_fma_f32 v[26:27], v[232:233], v[130:131], v[26:27] op_sel_hi:[0,1,1]
	v_pk_fma_f32 v[28:29], v[232:233], v[132:133], v[28:29] op_sel_hi:[0,1,1]
	v_pk_fma_f32 v[30:31], v[232:233], v[134:135], v[30:31] op_sel_hi:[0,1,1]
	v_pk_fma_f32 v[24:25], v[232:233], v[136:137], v[24:25] op_sel:[1,0,0] op_sel_hi:[1,1,1]
	v_pk_fma_f32 v[26:27], v[232:233], v[138:139], v[26:27] op_sel:[1,0,0] op_sel_hi:[1,1,1]
	v_pk_fma_f32 v[28:29], v[232:233], v[140:141], v[28:29] op_sel:[1,0,0] op_sel_hi:[1,1,1]
	v_pk_fma_f32 v[30:31], v[232:233], v[142:143], v[30:31] op_sel:[1,0,0] op_sel_hi:[1,1,1]
	v_pk_fma_f32 v[24:25], v[234:235], v[144:145], v[24:25] op_sel_hi:[0,1,1]
	v_pk_fma_f32 v[26:27], v[234:235], v[146:147], v[26:27] op_sel_hi:[0,1,1]
	v_pk_fma_f32 v[28:29], v[234:235], v[148:149], v[28:29] op_sel_hi:[0,1,1]
	v_pk_fma_f32 v[30:31], v[234:235], v[150:151], v[30:31] op_sel_hi:[0,1,1]
	v_pk_fma_f32 v[24:25], v[234:235], v[152:153], v[24:25] op_sel:[1,0,0] op_sel_hi:[1,1,1]
	v_pk_fma_f32 v[26:27], v[234:235], v[154:155], v[26:27] op_sel:[1,0,0] op_sel_hi:[1,1,1]
	v_pk_fma_f32 v[28:29], v[234:235], v[156:157], v[28:29] op_sel:[1,0,0] op_sel_hi:[1,1,1]
	v_pk_fma_f32 v[30:31], v[234:235], v[158:159], v[30:31] op_sel:[1,0,0] op_sel_hi:[1,1,1]
	v_pk_fma_f32 v[24:25], v[236:237], v[160:161], v[24:25] op_sel_hi:[0,1,1]
	v_pk_fma_f32 v[26:27], v[236:237], v[162:163], v[26:27] op_sel_hi:[0,1,1]
; #define LAS __attribute__((address_space(3)))
; __global__ void __launch_bounds__(NTHR, 2) fwd_kernel(Args args) {
;     ...
;             for (int i = 0; i < 16; ++i) { const int k = 2 * lane + 128 * i; f32x2 rv[8]; unsigned xw[8];
; #pragma unroll
;                 for (int e = 0; e < 8; ++e) rv[e] = *(const LAS f32x2*)(Rg + e * DM + k);
; #pragma unroll
;                 for (int q = 0; q < 8; ++q) xw[q] = *(const unsigned*)(XB + (size_t)(t0 + q) * DM + k);
; #pragma unroll
;                 for (int q = 0; q < 8; ++q) { const float x0 = bflo(xw[q]), x1 = bfhi(xw[q]); ssq[q] += x0 * x0 + x1 * x1;
; #pragma unroll
;                     for (int e = 0; e < 8; ++e) acc[q][e] += x0 * rv[e].x + x1 * rv[e].y; } }
	v_pk_fma_f32 v[28:29], v[236:237], v[164:165], v[28:29] op_sel_hi:[0,1,1]
	v_pk_fma_f32 v[30:31], v[236:237], v[166:167], v[30:31] op_sel_hi:[0,1,1]
	v_pk_fma_f32 v[24:25], v[236:237], v[168:169], v[24:25] op_sel:[1,0,0] op_sel_hi:[1,1,1]
	v_pk_fma_f32 v[26:27], v[236:237], v[170:171], v[26:27] op_sel:[1,0,0] op_sel_hi:[1,1,1]
	v_pk_fma_f32 v[28:29], v[236:237], v[172:173], v[28:29] op_sel:[1,0,0] op_sel_hi:[1,1,1]
	v_pk_fma_f32 v[30:31], v[236:237], v[174:175], v[30:31] op_sel:[1,0,0] op_sel_hi:[1,1,1]
	v_pk_fma_f32 v[24:25], v[238:239], v[176:177], v[24:25] op_sel_hi:[0,1,1]
	v_pk_fma_f32 v[26:27], v[238:239], v[178:179], v[26:27] op_sel_hi:[0,1,1]
	v_pk_fma_f32 v[28:29], v[238:239], v[180:181], v[28:29] op_sel_hi:[0,1,1]
	v_pk_fma_f32 v[30:31], v[238:239], v[182:183], v[30:31] op_sel_hi:[0,1,1]
	v_pk_fma_f32 v[24:25], v[238:239], v[184:185], v[24:25] op_sel:[1,0,0] op_sel_hi:[1,1,1]
	v_pk_fma_f32 v[26:27], v[238:239], v[186:187], v[26:27] op_sel:[1,0,0] op_sel_hi:[1,1,1]
	v_pk_fma_f32 v[28:29], v[238:239], v[188:189], v[28:29] op_sel:[1,0,0] op_sel_hi:[1,1,1]
	v_pk_fma_f32 v[30:31], v[238:239], v[190:191], v[30:31] op_sel:[1,0,0] op_sel_hi:[1,1,1]
	v_lshlrev_b32_e32 v232, 16, v112
	v_and_b32_e32 v233, s15, v112
	v_lshlrev_b32_e32 v234, 16, v113
	v_and_b32_e32 v235, s15, v113
	v_lshlrev_b32_e32 v236, 16, v114
	v_and_b32_e32 v237, s15, v114
	v_lshlrev_b32_e32 v238, 16, v115
	v_and_b32_e32 v239, s15, v115
	v_pk_fma_f32 v[200:201], v[232:233], v[232:233], v[200:201]
	v_pk_fma_f32 v[200:201], v[234:235], v[234:235], v[200:201]
	v_pk_fma_f32 v[200:201], v[236:237], v[236:237], v[200:201]
	v_pk_fma_f32 v[200:201], v[238:239], v[238:239], v[200:201]
	v_pk_fma_f32 v[32:33], v[232:233], v[128:129], v[32:33] op_sel_hi:[0,1,1]
	v_pk_fma_f32 v[34:35], v[232:233], v[130:131], v[34:35] op_sel_hi:[0,1,1]
	v_pk_fma_f32 v[36:37], v[232:233], v[132:133], v[36:37] op_sel_hi:[0,1,1]
	v_pk_fma_f32 v[38:39], v[232:233], v[134:135], v[38:39] op_sel_hi:[0,1,1]
	v_pk_fma_f32 v[32:33], v[232:233], v[136:137], v[32:33] op_sel:[1,0,0] op_sel_hi:[1,1,1]
	v_pk_fma_f32 v[34:35], v[232:233], v[138:139], v[34:35] op_sel:[1,0,0] op_sel_hi:[1,1,1]
	v_pk_fma_f32 v[36:37], v[232:233], v[140:141], v[36:37] op_sel:[1,0,0] op_sel_hi:[1,1,1]
	v_pk_fma_f32 v[38:39], v[232:233], v[142:143], v[38:39] op_sel:[1,0,0] op_sel_hi:[1,1,1]
	v_pk_fma_f32 v[32:33], v[234:235], v[144:145], v[32:33] op_sel_hi:[0,1,1]
	v_pk_fma_f32 v[34:35], v[234:235], v[146:147], v[34:35] op_sel_hi:[0,1,1]
	v_pk_fma_f32 v[36:37], v[234:235], v[148:149], v[36:37] op_sel_hi:[0,1,1]
	v_pk_fma_f32 v[38:39], v[234:235], v[150:151], v[38:39] op_sel_hi:[0,1,1]
	v_pk_fma_f32 v[32:33], v[234:235], v[152:153], v[32:33] op_sel:[1,0,0] op_sel_hi:[1,1,1]
	v_pk_fma_f32 v[34:35], v[234:235], v[154:155], v[34:35] op_sel:[1,0,0] op_sel_hi:[1,1,1]
	v_pk_fma_f32 v[36:37], v[234:235], v[156:157], v[36:37] op_sel:[1,0,0] op_sel_hi:[1,1,1]
	v_pk_fma_f32 v[38:39], v[234:235], v[158:159], v[38:39] op_sel:[1,0,0] op_sel_hi:[1,1,1]
	v_pk_fma_f32 v[32:33], v[236:237], v[160:161], v[32:33] op_sel_hi:[0,1,1]
	v_pk_fma_f32 v[34:35], v[236:237], v[162:163], v[34:35] op_sel_hi:[0,1,1]
	v_pk_fma_f32 v[36:37], v[236:237], v[164:165], v[36:37] op_sel_hi:[0,1,1]
	v_pk_fma_f32 v[38:39], v[236:237], v[166:167], v[38:39] op_sel_hi:[0,1,1]
	v_pk_fma_f32 v[32:33], v[236:237], v[168:169], v[32:33] op_sel:[1,0,0] op_sel_hi:[1,1,1]
	v_pk_fma_f32 v[34:35], v[236:237], v[170:171], v[34:35] op_sel:[1,0,0] op_sel_hi:[1,1,1]
	v_pk_fma_f32 v[36:37], v[236:237], v[172:173], v[36:37] op_sel:[1,0,0] op_sel_hi:[1,1,1]
	v_pk_fma_f32 v[38:39], v[236:237], v[174:175], v[38:39] op_sel:[1,0,0] op_sel_hi:[1,1,1]
	v_pk_fma_f32 v[32:33], v[238:239], v[176:177], v[32:33] op_sel_hi:[0,1,1]
	v_pk_fma_f32 v[34:35], v[238:239], v[178:179], v[34:35] op_sel_hi:[0,1,1]
	v_pk_fma_f32 v[36:37], v[238:239], v[180:181], v[36:37] op_sel_hi:[0,1,1]
	v_pk_fma_f32 v[38:39], v[238:239], v[182:183], v[38:39] op_sel_hi:[0,1,1]
	v_pk_fma_f32 v[32:33], v[238:239], v[184:185], v[32:33] op_sel:[1,0,0] op_sel_hi:[1,1,1]
	v_pk_fma_f32 v[34:35], v[238:239], v[186:187], v[34:35] op_sel:[1,0,0] op_sel_hi:[1,1,1]
	v_pk_fma_f32 v[36:37], v[238:239], v[188:189], v[36:37] op_sel:[1,0,0] op_sel_hi:[1,1,1]
	v_pk_fma_f32 v[38:39], v[238:239], v[190:191], v[38:39] op_sel:[1,0,0] op_sel_hi:[1,1,1]
	v_lshlrev_b32_e32 v232, 16, v116
	v_and_b32_e32 v233, s15, v116
	v_lshlrev_b32_e32 v234, 16, v117
	v_and_b32_e32 v235, s15, v117
	v_lshlrev_b32_e32 v236, 16, v118
	v_and_b32_e32 v237, s15, v118
	v_lshlrev_b32_e32 v238, 16, v119
	v_and_b32_e32 v239, s15, v119
	v_pk_fma_f32 v[202:203], v[232:233], v[232:233], v[202:203]
	v_pk_fma_f32 v[202:203], v[234:235], v[234:235], v[202:203]
	v_pk_fma_f32 v[202:203], v[236:237], v[236:237], v[202:203]
	v_pk_fma_f32 v[202:203], v[238:239], v[238:239], v[202:203]
	v_pk_fma_f32 v[40:41], v[232:233], v[128:129], v[40:41] op_sel_hi:[0,1,1]
	v_pk_fma_f32 v[42:43], v[232:233], v[130:131], v[42:43] op_sel_hi:[0,1,1]
	v_pk_fma_f32 v[44:45], v[232:233], v[132:133], v[44:45] op_sel_hi:[0,1,1]
	v_pk_fma_f32 v[46:47], v[232:233], v[134:135], v[46:47] op_sel_hi:[0,1,1]
	v_pk_fma_f32 v[40:41], v[232:233], v[136:137], v[40:41] op_sel:[1,0,0] op_sel_hi:[1,1,1]
	v_pk_fma_f32 v[42:43], v[232:233], v[138:139], v[42:43] op_sel:[1,0,0] op_sel_hi:[1,1,1]
	v_pk_fma_f32 v[44:45], v[232:233], v[140:141], v[44:45] op_sel:[1,0,0] op_sel_hi:[1,1,1]
	v_pk_fma_f32 v[46:47], v[232:233], v[142:143], v[46:47] op_sel:[1,0,0] op_sel_hi:[1,1,1]
	v_pk_fma_f32 v[40:41], v[234:235], v[144:145], v[40:41] op_sel_hi:[0,1,1]
	v_pk_fma_f32 v[42:43], v[234:235], v[146:147], v[42:43] op_sel_hi:[0,1,1]
; #define LAS __attribute__((address_space(3)))
; __global__ void __launch_bounds__(NTHR, 2) fwd_kernel(Args args) {
;     ...
;             for (int i = 0; i < 16; ++i) { const int k = 2 * lane + 128 * i; f32x2 rv[8]; unsigned xw[8];
; #pragma unroll
;                 for (int e = 0; e < 8; ++e) rv[e] = *(const LAS f32x2*)(Rg + e * DM + k);
; #pragma unroll
;                 for (int q = 0; q < 8; ++q) xw[q] = *(const unsigned*)(XB + (size_t)(t0 + q) * DM + k);
; #pragma unroll
;                 for (int q = 0; q < 8; ++q) { const float x0 = bflo(xw[q]), x1 = bfhi(xw[q]); ssq[q] += x0 * x0 + x1 * x1;
; #pragma unroll
;                     for (int e = 0; e < 8; ++e) acc[q][e] += x0 * rv[e].x + x1 * rv[e].y; } }
	v_pk_fma_f32 v[44:45], v[234:235], v[148:149], v[44:45] op_sel_hi:[0,1,1]
	v_pk_fma_f32 v[46:47], v[234:235], v[150:151], v[46:47] op_sel_hi:[0,1,1]
	v_pk_fma_f32 v[40:41], v[234:235], v[152:153], v[40:41] op_sel:[1,0,0] op_sel_hi:[1,1,1]
	v_pk_fma_f32 v[42:43], v[234:235], v[154:155], v[42:43] op_sel:[1,0,0] op_sel_hi:[1,1,1]
	v_pk_fma_f32 v[44:45], v[234:235], v[156:157], v[44:45] op_sel:[1,0,0] op_sel_hi:[1,1,1]
	v_pk_fma_f32 v[46:47], v[234:235], v[158:159], v[46:47] op_sel:[1,0,0] op_sel_hi:[1,1,1]
	v_pk_fma_f32 v[40:41], v[236:237], v[160:161], v[40:41] op_sel_hi:[0,1,1]
	v_pk_fma_f32 v[42:43], v[236:237], v[162:163], v[42:43] op_sel_hi:[0,1,1]
	v_pk_fma_f32 v[44:45], v[236:237], v[164:165], v[44:45] op_sel_hi:[0,1,1]
	v_pk_fma_f32 v[46:47], v[236:237], v[166:167], v[46:47] op_sel_hi:[0,1,1]
	v_pk_fma_f32 v[40:41], v[236:237], v[168:169], v[40:41] op_sel:[1,0,0] op_sel_hi:[1,1,1]
	v_pk_fma_f32 v[42:43], v[236:237], v[170:171], v[42:43] op_sel:[1,0,0] op_sel_hi:[1,1,1]
	v_pk_fma_f32 v[44:45], v[236:237], v[172:173], v[44:45] op_sel:[1,0,0] op_sel_hi:[1,1,1]
	v_pk_fma_f32 v[46:47], v[236:237], v[174:175], v[46:47] op_sel:[1,0,0] op_sel_hi:[1,1,1]
	v_pk_fma_f32 v[40:41], v[238:239], v[176:177], v[40:41] op_sel_hi:[0,1,1]
	v_pk_fma_f32 v[42:43], v[238:239], v[178:179], v[42:43] op_sel_hi:[0,1,1]
	v_pk_fma_f32 v[44:45], v[238:239], v[180:181], v[44:45] op_sel_hi:[0,1,1]
	v_pk_fma_f32 v[46:47], v[238:239], v[182:183], v[46:47] op_sel_hi:[0,1,1]
	v_pk_fma_f32 v[40:41], v[238:239], v[184:185], v[40:41] op_sel:[1,0,0] op_sel_hi:[1,1,1]
	v_pk_fma_f32 v[42:43], v[238:239], v[186:187], v[42:43] op_sel:[1,0,0] op_sel_hi:[1,1,1]
	v_pk_fma_f32 v[44:45], v[238:239], v[188:189], v[44:45] op_sel:[1,0,0] op_sel_hi:[1,1,1]
	v_pk_fma_f32 v[46:47], v[238:239], v[190:191], v[46:47] op_sel:[1,0,0] op_sel_hi:[1,1,1]
	v_lshlrev_b32_e32 v232, 16, v120
	v_and_b32_e32 v233, s15, v120
	v_lshlrev_b32_e32 v234, 16, v121
	v_and_b32_e32 v235, s15, v121
	v_lshlrev_b32_e32 v236, 16, v122
	v_and_b32_e32 v237, s15, v122
	v_lshlrev_b32_e32 v238, 16, v123
	v_and_b32_e32 v239, s15, v123
	v_pk_fma_f32 v[204:205], v[232:233], v[232:233], v[204:205]
	v_pk_fma_f32 v[204:205], v[234:235], v[234:235], v[204:205]
	v_pk_fma_f32 v[204:205], v[236:237], v[236:237], v[204:205]
	v_pk_fma_f32 v[204:205], v[238:239], v[238:239], v[204:205]
	v_pk_fma_f32 v[48:49], v[232:233], v[128:129], v[48:49] op_sel_hi:[0,1,1]
	v_pk_fma_f32 v[50:51], v[232:233], v[130:131], v[50:51] op_sel_hi:[0,1,1]
	v_pk_fma_f32 v[52:53], v[232:233], v[132:133], v[52:53] op_sel_hi:[0,1,1]
	v_pk_fma_f32 v[54:55], v[232:233], v[134:135], v[54:55] op_sel_hi:[0,1,1]
	v_pk_fma_f32 v[48:49], v[232:233], v[136:137], v[48:49] op_sel:[1,0,0] op_sel_hi:[1,1,1]
	v_pk_fma_f32 v[50:51], v[232:233], v[138:139], v[50:51] op_sel:[1,0,0] op_sel_hi:[1,1,1]
	v_pk_fma_f32 v[52:53], v[232:233], v[140:141], v[52:53] op_sel:[1,0,0] op_sel_hi:[1,1,1]
	v_pk_fma_f32 v[54:55], v[232:233], v[142:143], v[54:55] op_sel:[1,0,0] op_sel_hi:[1,1,1]
	v_pk_fma_f32 v[48:49], v[234:235], v[144:145], v[48:49] op_sel_hi:[0,1,1]
	v_pk_fma_f32 v[50:51], v[234:235], v[146:147], v[50:51] op_sel_hi:[0,1,1]
	v_pk_fma_f32 v[52:53], v[234:235], v[148:149], v[52:53] op_sel_hi:[0,1,1]
	v_pk_fma_f32 v[54:55], v[234:235], v[150:151], v[54:55] op_sel_hi:[0,1,1]
	v_pk_fma_f32 v[48:49], v[234:235], v[152:153], v[48:49] op_sel:[1,0,0] op_sel_hi:[1,1,1]
	v_pk_fma_f32 v[50:51], v[234:235], v[154:155], v[50:51] op_sel:[1,0,0] op_sel_hi:[1,1,1]
	v_pk_fma_f32 v[52:53], v[234:235], v[156:157], v[52:53] op_sel:[1,0,0] op_sel_hi:[1,1,1]
	v_pk_fma_f32 v[54:55], v[234:235], v[158:159], v[54:55] op_sel:[1,0,0] op_sel_hi:[1,1,1]
	v_pk_fma_f32 v[48:49], v[236:237], v[160:161], v[48:49] op_sel_hi:[0,1,1]
	v_pk_fma_f32 v[50:51], v[236:237], v[162:163], v[50:51] op_sel_hi:[0,1,1]
	v_pk_fma_f32 v[52:53], v[236:237], v[164:165], v[52:53] op_sel_hi:[0,1,1]
	v_pk_fma_f32 v[54:55], v[236:237], v[166:167], v[54:55] op_sel_hi:[0,1,1]
	v_pk_fma_f32 v[48:49], v[236:237], v[168:169], v[48:49] op_sel:[1,0,0] op_sel_hi:[1,1,1]
	v_pk_fma_f32 v[50:51], v[236:237], v[170:171], v[50:51] op_sel:[1,0,0] op_sel_hi:[1,1,1]
	v_pk_fma_f32 v[52:53], v[236:237], v[172:173], v[52:53] op_sel:[1,0,0] op_sel_hi:[1,1,1]
	v_pk_fma_f32 v[54:55], v[236:237], v[174:175], v[54:55] op_sel:[1,0,0] op_sel_hi:[1,1,1]
	v_pk_fma_f32 v[48:49], v[238:239], v[176:177], v[48:49] op_sel_hi:[0,1,1]
	v_pk_fma_f32 v[50:51], v[238:239], v[178:179], v[50:51] op_sel_hi:[0,1,1]
	v_pk_fma_f32 v[52:53], v[238:239], v[180:181], v[52:53] op_sel_hi:[0,1,1]
	v_pk_fma_f32 v[54:55], v[238:239], v[182:183], v[54:55] op_sel_hi:[0,1,1]
	v_pk_fma_f32 v[48:49], v[238:239], v[184:185], v[48:49] op_sel:[1,0,0] op_sel_hi:[1,1,1]
	v_pk_fma_f32 v[50:51], v[238:239], v[186:187], v[50:51] op_sel:[1,0,0] op_sel_hi:[1,1,1]
	v_pk_fma_f32 v[52:53], v[238:239], v[188:189], v[52:53] op_sel:[1,0,0] op_sel_hi:[1,1,1]
	v_pk_fma_f32 v[54:55], v[238:239], v[190:191], v[54:55] op_sel:[1,0,0] op_sel_hi:[1,1,1]
	v_lshlrev_b32_e32 v232, 16, v124
	v_and_b32_e32 v233, s15, v124
	v_lshlrev_b32_e32 v234, 16, v125
	v_and_b32_e32 v235, s15, v125
	v_lshlrev_b32_e32 v236, 16, v126
	v_and_b32_e32 v237, s15, v126
	v_lshlrev_b32_e32 v238, 16, v127
	v_and_b32_e32 v239, s15, v127
	v_pk_fma_f32 v[206:207], v[232:233], v[232:233], v[206:207]
	v_pk_fma_f32 v[206:207], v[234:235], v[234:235], v[206:207]
	v_pk_fma_f32 v[206:207], v[236:237], v[236:237], v[206:207]
	v_pk_fma_f32 v[206:207], v[238:239], v[238:239], v[206:207]
	v_pk_fma_f32 v[56:57], v[232:233], v[128:129], v[56:57] op_sel_hi:[0,1,1]
	v_pk_fma_f32 v[58:59], v[232:233], v[130:131], v[58:59] op_sel_hi:[0,1,1]
; #define LAS __attribute__((address_space(3)))
; __device__ __forceinline__ float wave_sum(float v) {
; #pragma unroll
;     for (int o = 1; o < 64; o <<= 1) v += __shfl_xor(v, o);
;     return v;
; __global__ void __launch_bounds__(NTHR, 2) fwd_kernel(Args args) {
;     ...
;             for (int i = 0; i < 16; ++i) { const int k = 2 * lane + 128 * i; f32x2 rv[8]; unsigned xw[8];
; #pragma unroll
;                 for (int e = 0; e < 8; ++e) rv[e] = *(const LAS f32x2*)(Rg + e * DM + k);
; #pragma unroll
;                 for (int q = 0; q < 8; ++q) xw[q] = *(const unsigned*)(XB + (size_t)(t0 + q) * DM + k);
; #pragma unroll
;                 for (int q = 0; q < 8; ++q) { const float x0 = bflo(xw[q]), x1 = bfhi(xw[q]); ssq[q] += x0 * x0 + x1 * x1;
; #pragma unroll
;                     for (int e = 0; e < 8; ++e) acc[q][e] += x0 * rv[e].x + x1 * rv[e].y; } }
	v_pk_fma_f32 v[60:61], v[232:233], v[132:133], v[60:61] op_sel_hi:[0,1,1]
	v_pk_fma_f32 v[62:63], v[232:233], v[134:135], v[62:63] op_sel_hi:[0,1,1]
	v_pk_fma_f32 v[56:57], v[232:233], v[136:137], v[56:57] op_sel:[1,0,0] op_sel_hi:[1,1,1]
	v_pk_fma_f32 v[58:59], v[232:233], v[138:139], v[58:59] op_sel:[1,0,0] op_sel_hi:[1,1,1]
	v_pk_fma_f32 v[60:61], v[232:233], v[140:141], v[60:61] op_sel:[1,0,0] op_sel_hi:[1,1,1]
	v_pk_fma_f32 v[62:63], v[232:233], v[142:143], v[62:63] op_sel:[1,0,0] op_sel_hi:[1,1,1]
	v_pk_fma_f32 v[56:57], v[234:235], v[144:145], v[56:57] op_sel_hi:[0,1,1]
	v_pk_fma_f32 v[58:59], v[234:235], v[146:147], v[58:59] op_sel_hi:[0,1,1]
	v_pk_fma_f32 v[60:61], v[234:235], v[148:149], v[60:61] op_sel_hi:[0,1,1]
	v_pk_fma_f32 v[62:63], v[234:235], v[150:151], v[62:63] op_sel_hi:[0,1,1]
	v_pk_fma_f32 v[56:57], v[234:235], v[152:153], v[56:57] op_sel:[1,0,0] op_sel_hi:[1,1,1]
	v_pk_fma_f32 v[58:59], v[234:235], v[154:155], v[58:59] op_sel:[1,0,0] op_sel_hi:[1,1,1]
	v_pk_fma_f32 v[60:61], v[234:235], v[156:157], v[60:61] op_sel:[1,0,0] op_sel_hi:[1,1,1]
	v_pk_fma_f32 v[62:63], v[234:235], v[158:159], v[62:63] op_sel:[1,0,0] op_sel_hi:[1,1,1]
	v_pk_fma_f32 v[56:57], v[236:237], v[160:161], v[56:57] op_sel_hi:[0,1,1]
	v_pk_fma_f32 v[58:59], v[236:237], v[162:163], v[58:59] op_sel_hi:[0,1,1]
	v_pk_fma_f32 v[60:61], v[236:237], v[164:165], v[60:61] op_sel_hi:[0,1,1]
	v_pk_fma_f32 v[62:63], v[236:237], v[166:167], v[62:63] op_sel_hi:[0,1,1]
	v_pk_fma_f32 v[56:57], v[236:237], v[168:169], v[56:57] op_sel:[1,0,0] op_sel_hi:[1,1,1]
	v_pk_fma_f32 v[58:59], v[236:237], v[170:171], v[58:59] op_sel:[1,0,0] op_sel_hi:[1,1,1]
	v_pk_fma_f32 v[60:61], v[236:237], v[172:173], v[60:61] op_sel:[1,0,0] op_sel_hi:[1,1,1]
	v_pk_fma_f32 v[62:63], v[236:237], v[174:175], v[62:63] op_sel:[1,0,0] op_sel_hi:[1,1,1]
	v_pk_fma_f32 v[56:57], v[238:239], v[176:177], v[56:57] op_sel_hi:[0,1,1]
	v_pk_fma_f32 v[58:59], v[238:239], v[178:179], v[58:59] op_sel_hi:[0,1,1]
	v_pk_fma_f32 v[60:61], v[238:239], v[180:181], v[60:61] op_sel_hi:[0,1,1]
	v_pk_fma_f32 v[62:63], v[238:239], v[182:183], v[62:63] op_sel_hi:[0,1,1]
	v_pk_fma_f32 v[56:57], v[238:239], v[184:185], v[56:57] op_sel:[1,0,0] op_sel_hi:[1,1,1]
	v_pk_fma_f32 v[58:59], v[238:239], v[186:187], v[58:59] op_sel:[1,0,0] op_sel_hi:[1,1,1]
	v_pk_fma_f32 v[60:61], v[238:239], v[188:189], v[60:61] op_sel:[1,0,0] op_sel_hi:[1,1,1]
	v_pk_fma_f32 v[62:63], v[238:239], v[190:191], v[62:63] op_sel:[1,0,0] op_sel_hi:[1,1,1]
	v_add_f32_e32 v192, v192, v193
	v_add_f32_e32 v194, v194, v195
	v_add_f32_e32 v196, v196, v197
	v_add_f32_e32 v198, v198, v199
	v_add_f32_e32 v200, v200, v201
	v_add_f32_e32 v202, v202, v203
	v_add_f32_e32 v204, v204, v205
	v_add_f32_e32 v206, v206, v207
	v_add_f32_dpp v0, v0, v0 quad_perm:[1,0,3,2] row_mask:0xf bank_mask:0xf
	v_add_f32_dpp v1, v1, v1 quad_perm:[1,0,3,2] row_mask:0xf bank_mask:0xf
	v_add_f32_dpp v2, v2, v2 quad_perm:[1,0,3,2] row_mask:0xf bank_mask:0xf
	v_add_f32_dpp v3, v3, v3 quad_perm:[1,0,3,2] row_mask:0xf bank_mask:0xf
	v_add_f32_dpp v4, v4, v4 quad_perm:[1,0,3,2] row_mask:0xf bank_mask:0xf
	v_add_f32_dpp v5, v5, v5 quad_perm:[1,0,3,2] row_mask:0xf bank_mask:0xf
	v_add_f32_dpp v6, v6, v6 quad_perm:[1,0,3,2] row_mask:0xf bank_mask:0xf
	v_add_f32_dpp v7, v7, v7 quad_perm:[1,0,3,2] row_mask:0xf bank_mask:0xf
	v_add_f32_dpp v8, v8, v8 quad_perm:[1,0,3,2] row_mask:0xf bank_mask:0xf
	v_add_f32_dpp v9, v9, v9 quad_perm:[1,0,3,2] row_mask:0xf bank_mask:0xf
	v_add_f32_dpp v10, v10, v10 quad_perm:[1,0,3,2] row_mask:0xf bank_mask:0xf
	v_add_f32_dpp v11, v11, v11 quad_perm:[1,0,3,2] row_mask:0xf bank_mask:0xf
	v_add_f32_dpp v12, v12, v12 quad_perm:[1,0,3,2] row_mask:0xf bank_mask:0xf
	v_add_f32_dpp v13, v13, v13 quad_perm:[1,0,3,2] row_mask:0xf bank_mask:0xf
	v_add_f32_dpp v14, v14, v14 quad_perm:[1,0,3,2] row_mask:0xf bank_mask:0xf
	v_add_f32_dpp v15, v15, v15 quad_perm:[1,0,3,2] row_mask:0xf bank_mask:0xf
	v_add_f32_dpp v16, v16, v16 quad_perm:[1,0,3,2] row_mask:0xf bank_mask:0xf
	v_add_f32_dpp v17, v17, v17 quad_perm:[1,0,3,2] row_mask:0xf bank_mask:0xf
	v_add_f32_dpp v18, v18, v18 quad_perm:[1,0,3,2] row_mask:0xf bank_mask:0xf
	v_add_f32_dpp v19, v19, v19 quad_perm:[1,0,3,2] row_mask:0xf bank_mask:0xf
	v_add_f32_dpp v20, v20, v20 quad_perm:[1,0,3,2] row_mask:0xf bank_mask:0xf
	v_add_f32_dpp v21, v21, v21 quad_perm:[1,0,3,2] row_mask:0xf bank_mask:0xf
	v_add_f32_dpp v22, v22, v22 quad_perm:[1,0,3,2] row_mask:0xf bank_mask:0xf
	v_add_f32_dpp v23, v23, v23 quad_perm:[1,0,3,2] row_mask:0xf bank_mask:0xf
	v_add_f32_dpp v24, v24, v24 quad_perm:[1,0,3,2] row_mask:0xf bank_mask:0xf
	v_add_f32_dpp v25, v25, v25 quad_perm:[1,0,3,2] row_mask:0xf bank_mask:0xf
	v_add_f32_dpp v26, v26, v26 quad_perm:[1,0,3,2] row_mask:0xf bank_mask:0xf
	v_add_f32_dpp v27, v27, v27 quad_perm:[1,0,3,2] row_mask:0xf bank_mask:0xf
	v_add_f32_dpp v28, v28, v28 quad_perm:[1,0,3,2] row_mask:0xf bank_mask:0xf
	v_add_f32_dpp v29, v29, v29 quad_perm:[1,0,3,2] row_mask:0xf bank_mask:0xf
	v_add_f32_dpp v30, v30, v30 quad_perm:[1,0,3,2] row_mask:0xf bank_mask:0xf
	v_add_f32_dpp v31, v31, v31 quad_perm:[1,0,3,2] row_mask:0xf bank_mask:0xf
	v_add_f32_dpp v32, v32, v32 quad_perm:[1,0,3,2] row_mask:0xf bank_mask:0xf
	v_add_f32_dpp v33, v33, v33 quad_perm:[1,0,3,2] row_mask:0xf bank_mask:0xf
	v_add_f32_dpp v34, v34, v34 quad_perm:[1,0,3,2] row_mask:0xf bank_mask:0xf
	v_add_f32_dpp v35, v35, v35 quad_perm:[1,0,3,2] row_mask:0xf bank_mask:0xf
	v_add_f32_dpp v36, v36, v36 quad_perm:[1,0,3,2] row_mask:0xf bank_mask:0xf
	v_add_f32_dpp v37, v37, v37 quad_perm:[1,0,3,2] row_mask:0xf bank_mask:0xf
; __device__ __forceinline__ float wave_sum(float v) {
; #pragma unroll
;     for (int o = 1; o < 64; o <<= 1) v += __shfl_xor(v, o);
;     return v;
; __global__ void __launch_bounds__(NTHR, 2) fwd_kernel(Args args) {
;     ...
;             for (int q = 0; q < 8; ++q) { const float sq = wave_sum(ssq[q]); const float rs = 1.0f / sqrtf(sq * (1.0f / DM) + EPS);
;                 float lg[8];
; #pragma unroll
;                 for (int e = 0; e < 8; ++e) lg[e] = wave_sum(acc[q][e]) * rs;
	v_add_f32_dpp v38, v38, v38 quad_perm:[1,0,3,2] row_mask:0xf bank_mask:0xf
	v_add_f32_dpp v39, v39, v39 quad_perm:[1,0,3,2] row_mask:0xf bank_mask:0xf
	v_add_f32_dpp v40, v40, v40 quad_perm:[1,0,3,2] row_mask:0xf bank_mask:0xf
	v_add_f32_dpp v41, v41, v41 quad_perm:[1,0,3,2] row_mask:0xf bank_mask:0xf
	v_add_f32_dpp v42, v42, v42 quad_perm:[1,0,3,2] row_mask:0xf bank_mask:0xf
	v_add_f32_dpp v43, v43, v43 quad_perm:[1,0,3,2] row_mask:0xf bank_mask:0xf
	v_add_f32_dpp v44, v44, v44 quad_perm:[1,0,3,2] row_mask:0xf bank_mask:0xf
	v_add_f32_dpp v45, v45, v45 quad_perm:[1,0,3,2] row_mask:0xf bank_mask:0xf
	v_add_f32_dpp v46, v46, v46 quad_perm:[1,0,3,2] row_mask:0xf bank_mask:0xf
	v_add_f32_dpp v47, v47, v47 quad_perm:[1,0,3,2] row_mask:0xf bank_mask:0xf
	v_add_f32_dpp v48, v48, v48 quad_perm:[1,0,3,2] row_mask:0xf bank_mask:0xf
	v_add_f32_dpp v49, v49, v49 quad_perm:[1,0,3,2] row_mask:0xf bank_mask:0xf
	v_add_f32_dpp v50, v50, v50 quad_perm:[1,0,3,2] row_mask:0xf bank_mask:0xf
	v_add_f32_dpp v51, v51, v51 quad_perm:[1,0,3,2] row_mask:0xf bank_mask:0xf
	v_add_f32_dpp v52, v52, v52 quad_perm:[1,0,3,2] row_mask:0xf bank_mask:0xf
	v_add_f32_dpp v53, v53, v53 quad_perm:[1,0,3,2] row_mask:0xf bank_mask:0xf
	v_add_f32_dpp v54, v54, v54 quad_perm:[1,0,3,2] row_mask:0xf bank_mask:0xf
	v_add_f32_dpp v55, v55, v55 quad_perm:[1,0,3,2] row_mask:0xf bank_mask:0xf
	v_add_f32_dpp v56, v56, v56 quad_perm:[1,0,3,2] row_mask:0xf bank_mask:0xf
	v_add_f32_dpp v57, v57, v57 quad_perm:[1,0,3,2] row_mask:0xf bank_mask:0xf
	v_add_f32_dpp v58, v58, v58 quad_perm:[1,0,3,2] row_mask:0xf bank_mask:0xf
	v_add_f32_dpp v59, v59, v59 quad_perm:[1,0,3,2] row_mask:0xf bank_mask:0xf
	v_add_f32_dpp v60, v60, v60 quad_perm:[1,0,3,2] row_mask:0xf bank_mask:0xf
	v_add_f32_dpp v61, v61, v61 quad_perm:[1,0,3,2] row_mask:0xf bank_mask:0xf
	v_add_f32_dpp v62, v62, v62 quad_perm:[1,0,3,2] row_mask:0xf bank_mask:0xf
	v_add_f32_dpp v63, v63, v63 quad_perm:[1,0,3,2] row_mask:0xf bank_mask:0xf
	v_add_f32_dpp v192, v192, v192 quad_perm:[1,0,3,2] row_mask:0xf bank_mask:0xf
	v_add_f32_dpp v194, v194, v194 quad_perm:[1,0,3,2] row_mask:0xf bank_mask:0xf
	v_add_f32_dpp v196, v196, v196 quad_perm:[1,0,3,2] row_mask:0xf bank_mask:0xf
	v_add_f32_dpp v198, v198, v198 quad_perm:[1,0,3,2] row_mask:0xf bank_mask:0xf
	v_add_f32_dpp v200, v200, v200 quad_perm:[1,0,3,2] row_mask:0xf bank_mask:0xf
	v_add_f32_dpp v202, v202, v202 quad_perm:[1,0,3,2] row_mask:0xf bank_mask:0xf
	v_add_f32_dpp v204, v204, v204 quad_perm:[1,0,3,2] row_mask:0xf bank_mask:0xf
	v_add_f32_dpp v206, v206, v206 quad_perm:[1,0,3,2] row_mask:0xf bank_mask:0xf
	v_add_f32_dpp v0, v0, v0 quad_perm:[2,3,0,1] row_mask:0xf bank_mask:0xf
	v_add_f32_dpp v1, v1, v1 quad_perm:[2,3,0,1] row_mask:0xf bank_mask:0xf
	v_add_f32_dpp v2, v2, v2 quad_perm:[2,3,0,1] row_mask:0xf bank_mask:0xf
	v_add_f32_dpp v3, v3, v3 quad_perm:[2,3,0,1] row_mask:0xf bank_mask:0xf
	v_add_f32_dpp v4, v4, v4 quad_perm:[2,3,0,1] row_mask:0xf bank_mask:0xf
	v_add_f32_dpp v5, v5, v5 quad_perm:[2,3,0,1] row_mask:0xf bank_mask:0xf
	v_add_f32_dpp v6, v6, v6 quad_perm:[2,3,0,1] row_mask:0xf bank_mask:0xf
	v_add_f32_dpp v7, v7, v7 quad_perm:[2,3,0,1] row_mask:0xf bank_mask:0xf
	v_add_f32_dpp v8, v8, v8 quad_perm:[2,3,0,1] row_mask:0xf bank_mask:0xf
	v_add_f32_dpp v9, v9, v9 quad_perm:[2,3,0,1] row_mask:0xf bank_mask:0xf
	v_add_f32_dpp v10, v10, v10 quad_perm:[2,3,0,1] row_mask:0xf bank_mask:0xf
	v_add_f32_dpp v11, v11, v11 quad_perm:[2,3,0,1] row_mask:0xf bank_mask:0xf
	v_add_f32_dpp v12, v12, v12 quad_perm:[2,3,0,1] row_mask:0xf bank_mask:0xf
	v_add_f32_dpp v13, v13, v13 quad_perm:[2,3,0,1] row_mask:0xf bank_mask:0xf
	v_add_f32_dpp v14, v14, v14 quad_perm:[2,3,0,1] row_mask:0xf bank_mask:0xf
	v_add_f32_dpp v15, v15, v15 quad_perm:[2,3,0,1] row_mask:0xf bank_mask:0xf
	v_add_f32_dpp v16, v16, v16 quad_perm:[2,3,0,1] row_mask:0xf bank_mask:0xf
	v_add_f32_dpp v17, v17, v17 quad_perm:[2,3,0,1] row_mask:0xf bank_mask:0xf
	v_add_f32_dpp v18, v18, v18 quad_perm:[2,3,0,1] row_mask:0xf bank_mask:0xf
	v_add_f32_dpp v19, v19, v19 quad_perm:[2,3,0,1] row_mask:0xf bank_mask:0xf
	v_add_f32_dpp v20, v20, v20 quad_perm:[2,3,0,1] row_mask:0xf bank_mask:0xf
	v_add_f32_dpp v21, v21, v21 quad_perm:[2,3,0,1] row_mask:0xf bank_mask:0xf
	v_add_f32_dpp v22, v22, v22 quad_perm:[2,3,0,1] row_mask:0xf bank_mask:0xf
	v_add_f32_dpp v23, v23, v23 quad_perm:[2,3,0,1] row_mask:0xf bank_mask:0xf
	v_add_f32_dpp v24, v24, v24 quad_perm:[2,3,0,1] row_mask:0xf bank_mask:0xf
	v_add_f32_dpp v25, v25, v25 quad_perm:[2,3,0,1] row_mask:0xf bank_mask:0xf
	v_add_f32_dpp v26, v26, v26 quad_perm:[2,3,0,1] row_mask:0xf bank_mask:0xf
	v_add_f32_dpp v27, v27, v27 quad_perm:[2,3,0,1] row_mask:0xf bank_mask:0xf
	v_add_f32_dpp v28, v28, v28 quad_perm:[2,3,0,1] row_mask:0xf bank_mask:0xf
	v_add_f32_dpp v29, v29, v29 quad_perm:[2,3,0,1] row_mask:0xf bank_mask:0xf
	v_add_f32_dpp v30, v30, v30 quad_perm:[2,3,0,1] row_mask:0xf bank_mask:0xf
	v_add_f32_dpp v31, v31, v31 quad_perm:[2,3,0,1] row_mask:0xf bank_mask:0xf
	v_add_f32_dpp v32, v32, v32 quad_perm:[2,3,0,1] row_mask:0xf bank_mask:0xf
	v_add_f32_dpp v33, v33, v33 quad_perm:[2,3,0,1] row_mask:0xf bank_mask:0xf
	v_add_f32_dpp v34, v34, v34 quad_perm:[2,3,0,1] row_mask:0xf bank_mask:0xf
	v_add_f32_dpp v35, v35, v35 quad_perm:[2,3,0,1] row_mask:0xf bank_mask:0xf
	v_add_f32_dpp v36, v36, v36 quad_perm:[2,3,0,1] row_mask:0xf bank_mask:0xf
	v_add_f32_dpp v37, v37, v37 quad_perm:[2,3,0,1] row_mask:0xf bank_mask:0xf
	v_add_f32_dpp v38, v38, v38 quad_perm:[2,3,0,1] row_mask:0xf bank_mask:0xf
	v_add_f32_dpp v39, v39, v39 quad_perm:[2,3,0,1] row_mask:0xf bank_mask:0xf
; __device__ __forceinline__ float wave_sum(float v) {
; #pragma unroll
;     for (int o = 1; o < 64; o <<= 1) v += __shfl_xor(v, o);
;     return v;
; __global__ void __launch_bounds__(NTHR, 2) fwd_kernel(Args args) {
;     ...
;             for (int q = 0; q < 8; ++q) { const float sq = wave_sum(ssq[q]); const float rs = 1.0f / sqrtf(sq * (1.0f / DM) + EPS);
;                 float lg[8];
; #pragma unroll
;                 for (int e = 0; e < 8; ++e) lg[e] = wave_sum(acc[q][e]) * rs;
	v_add_f32_dpp v40, v40, v40 quad_perm:[2,3,0,1] row_mask:0xf bank_mask:0xf
	v_add_f32_dpp v41, v41, v41 quad_perm:[2,3,0,1] row_mask:0xf bank_mask:0xf
	v_add_f32_dpp v42, v42, v42 quad_perm:[2,3,0,1] row_mask:0xf bank_mask:0xf
	v_add_f32_dpp v43, v43, v43 quad_perm:[2,3,0,1] row_mask:0xf bank_mask:0xf
	v_add_f32_dpp v44, v44, v44 quad_perm:[2,3,0,1] row_mask:0xf bank_mask:0xf
	v_add_f32_dpp v45, v45, v45 quad_perm:[2,3,0,1] row_mask:0xf bank_mask:0xf
	v_add_f32_dpp v46, v46, v46 quad_perm:[2,3,0,1] row_mask:0xf bank_mask:0xf
	v_add_f32_dpp v47, v47, v47 quad_perm:[2,3,0,1] row_mask:0xf bank_mask:0xf
	v_add_f32_dpp v48, v48, v48 quad_perm:[2,3,0,1] row_mask:0xf bank_mask:0xf
	v_add_f32_dpp v49, v49, v49 quad_perm:[2,3,0,1] row_mask:0xf bank_mask:0xf
	v_add_f32_dpp v50, v50, v50 quad_perm:[2,3,0,1] row_mask:0xf bank_mask:0xf
	v_add_f32_dpp v51, v51, v51 quad_perm:[2,3,0,1] row_mask:0xf bank_mask:0xf
	v_add_f32_dpp v52, v52, v52 quad_perm:[2,3,0,1] row_mask:0xf bank_mask:0xf
	v_add_f32_dpp v53, v53, v53 quad_perm:[2,3,0,1] row_mask:0xf bank_mask:0xf
	v_add_f32_dpp v54, v54, v54 quad_perm:[2,3,0,1] row_mask:0xf bank_mask:0xf
	v_add_f32_dpp v55, v55, v55 quad_perm:[2,3,0,1] row_mask:0xf bank_mask:0xf
	v_add_f32_dpp v56, v56, v56 quad_perm:[2,3,0,1] row_mask:0xf bank_mask:0xf
	v_add_f32_dpp v57, v57, v57 quad_perm:[2,3,0,1] row_mask:0xf bank_mask:0xf
	v_add_f32_dpp v58, v58, v58 quad_perm:[2,3,0,1] row_mask:0xf bank_mask:0xf
	v_add_f32_dpp v59, v59, v59 quad_perm:[2,3,0,1] row_mask:0xf bank_mask:0xf
	v_add_f32_dpp v60, v60, v60 quad_perm:[2,3,0,1] row_mask:0xf bank_mask:0xf
	v_add_f32_dpp v61, v61, v61 quad_perm:[2,3,0,1] row_mask:0xf bank_mask:0xf
	v_add_f32_dpp v62, v62, v62 quad_perm:[2,3,0,1] row_mask:0xf bank_mask:0xf
	v_add_f32_dpp v63, v63, v63 quad_perm:[2,3,0,1] row_mask:0xf bank_mask:0xf
	v_add_f32_dpp v192, v192, v192 quad_perm:[2,3,0,1] row_mask:0xf bank_mask:0xf
	v_add_f32_dpp v194, v194, v194 quad_perm:[2,3,0,1] row_mask:0xf bank_mask:0xf
	v_add_f32_dpp v196, v196, v196 quad_perm:[2,3,0,1] row_mask:0xf bank_mask:0xf
	v_add_f32_dpp v198, v198, v198 quad_perm:[2,3,0,1] row_mask:0xf bank_mask:0xf
	v_add_f32_dpp v200, v200, v200 quad_perm:[2,3,0,1] row_mask:0xf bank_mask:0xf
	v_add_f32_dpp v202, v202, v202 quad_perm:[2,3,0,1] row_mask:0xf bank_mask:0xf
	v_add_f32_dpp v204, v204, v204 quad_perm:[2,3,0,1] row_mask:0xf bank_mask:0xf
	v_add_f32_dpp v206, v206, v206 quad_perm:[2,3,0,1] row_mask:0xf bank_mask:0xf
	v_add_f32_dpp v0, v0, v0 row_half_mirror row_mask:0xf bank_mask:0xf
	v_add_f32_dpp v1, v1, v1 row_half_mirror row_mask:0xf bank_mask:0xf
	v_add_f32_dpp v2, v2, v2 row_half_mirror row_mask:0xf bank_mask:0xf
	v_add_f32_dpp v3, v3, v3 row_half_mirror row_mask:0xf bank_mask:0xf
	v_add_f32_dpp v4, v4, v4 row_half_mirror row_mask:0xf bank_mask:0xf
	v_add_f32_dpp v5, v5, v5 row_half_mirror row_mask:0xf bank_mask:0xf
	v_add_f32_dpp v6, v6, v6 row_half_mirror row_mask:0xf bank_mask:0xf
	v_add_f32_dpp v7, v7, v7 row_half_mirror row_mask:0xf bank_mask:0xf
	v_add_f32_dpp v8, v8, v8 row_half_mirror row_mask:0xf bank_mask:0xf
	v_add_f32_dpp v9, v9, v9 row_half_mirror row_mask:0xf bank_mask:0xf
	v_add_f32_dpp v10, v10, v10 row_half_mirror row_mask:0xf bank_mask:0xf
	v_add_f32_dpp v11, v11, v11 row_half_mirror row_mask:0xf bank_mask:0xf
	v_add_f32_dpp v12, v12, v12 row_half_mirror row_mask:0xf bank_mask:0xf
	v_add_f32_dpp v13, v13, v13 row_half_mirror row_mask:0xf bank_mask:0xf
	v_add_f32_dpp v14, v14, v14 row_half_mirror row_mask:0xf bank_mask:0xf
	v_add_f32_dpp v15, v15, v15 row_half_mirror row_mask:0xf bank_mask:0xf
	v_add_f32_dpp v16, v16, v16 row_half_mirror row_mask:0xf bank_mask:0xf
	v_add_f32_dpp v17, v17, v17 row_half_mirror row_mask:0xf bank_mask:0xf
	v_add_f32_dpp v18, v18, v18 row_half_mirror row_mask:0xf bank_mask:0xf
	v_add_f32_dpp v19, v19, v19 row_half_mirror row_mask:0xf bank_mask:0xf
	v_add_f32_dpp v20, v20, v20 row_half_mirror row_mask:0xf bank_mask:0xf
	v_add_f32_dpp v21, v21, v21 row_half_mirror row_mask:0xf bank_mask:0xf
	v_add_f32_dpp v22, v22, v22 row_half_mirror row_mask:0xf bank_mask:0xf
	v_add_f32_dpp v23, v23, v23 row_half_mirror row_mask:0xf bank_mask:0xf
	v_add_f32_dpp v24, v24, v24 row_half_mirror row_mask:0xf bank_mask:0xf
	v_add_f32_dpp v25, v25, v25 row_half_mirror row_mask:0xf bank_mask:0xf
	v_add_f32_dpp v26, v26, v26 row_half_mirror row_mask:0xf bank_mask:0xf
	v_add_f32_dpp v27, v27, v27 row_half_mirror row_mask:0xf bank_mask:0xf
	v_add_f32_dpp v28, v28, v28 row_half_mirror row_mask:0xf bank_mask:0xf
	v_add_f32_dpp v29, v29, v29 row_half_mirror row_mask:0xf bank_mask:0xf
	v_add_f32_dpp v30, v30, v30 row_half_mirror row_mask:0xf bank_mask:0xf
	v_add_f32_dpp v31, v31, v31 row_half_mirror row_mask:0xf bank_mask:0xf
	v_add_f32_dpp v32, v32, v32 row_half_mirror row_mask:0xf bank_mask:0xf
	v_add_f32_dpp v33, v33, v33 row_half_mirror row_mask:0xf bank_mask:0xf
	v_add_f32_dpp v34, v34, v34 row_half_mirror row_mask:0xf bank_mask:0xf
	v_add_f32_dpp v35, v35, v35 row_half_mirror row_mask:0xf bank_mask:0xf
	v_add_f32_dpp v36, v36, v36 row_half_mirror row_mask:0xf bank_mask:0xf
	v_add_f32_dpp v37, v37, v37 row_half_mirror row_mask:0xf bank_mask:0xf
	v_add_f32_dpp v38, v38, v38 row_half_mirror row_mask:0xf bank_mask:0xf
	v_add_f32_dpp v39, v39, v39 row_half_mirror row_mask:0xf bank_mask:0xf
	v_add_f32_dpp v40, v40, v40 row_half_mirror row_mask:0xf bank_mask:0xf
	v_add_f32_dpp v41, v41, v41 row_half_mirror row_mask:0xf bank_mask:0xf
	v_add_f32_dpp v42, v42, v42 row_half_mirror row_mask:0xf bank_mask:0xf
	v_add_f32_dpp v43, v43, v43 row_half_mirror row_mask:0xf bank_mask:0xf
	v_add_f32_dpp v44, v44, v44 row_half_mirror row_mask:0xf bank_mask:0xf
; __device__ __forceinline__ float wave_sum(float v) {
; #pragma unroll
;     for (int o = 1; o < 64; o <<= 1) v += __shfl_xor(v, o);
;     return v;
; __global__ void __launch_bounds__(NTHR, 2) fwd_kernel(Args args) {
;     ...
;             for (int q = 0; q < 8; ++q) { const float sq = wave_sum(ssq[q]); const float rs = 1.0f / sqrtf(sq * (1.0f / DM) + EPS);
;                 float lg[8];
; #pragma unroll
;                 for (int e = 0; e < 8; ++e) lg[e] = wave_sum(acc[q][e]) * rs;
	v_add_f32_dpp v45, v45, v45 row_half_mirror row_mask:0xf bank_mask:0xf
	v_add_f32_dpp v46, v46, v46 row_half_mirror row_mask:0xf bank_mask:0xf
	v_add_f32_dpp v47, v47, v47 row_half_mirror row_mask:0xf bank_mask:0xf
	v_add_f32_dpp v48, v48, v48 row_half_mirror row_mask:0xf bank_mask:0xf
	v_add_f32_dpp v49, v49, v49 row_half_mirror row_mask:0xf bank_mask:0xf
	v_add_f32_dpp v50, v50, v50 row_half_mirror row_mask:0xf bank_mask:0xf
	v_add_f32_dpp v51, v51, v51 row_half_mirror row_mask:0xf bank_mask:0xf
	v_add_f32_dpp v52, v52, v52 row_half_mirror row_mask:0xf bank_mask:0xf
	v_add_f32_dpp v53, v53, v53 row_half_mirror row_mask:0xf bank_mask:0xf
	v_add_f32_dpp v54, v54, v54 row_half_mirror row_mask:0xf bank_mask:0xf
	v_add_f32_dpp v55, v55, v55 row_half_mirror row_mask:0xf bank_mask:0xf
	v_add_f32_dpp v56, v56, v56 row_half_mirror row_mask:0xf bank_mask:0xf
	v_add_f32_dpp v57, v57, v57 row_half_mirror row_mask:0xf bank_mask:0xf
	v_add_f32_dpp v58, v58, v58 row_half_mirror row_mask:0xf bank_mask:0xf
	v_add_f32_dpp v59, v59, v59 row_half_mirror row_mask:0xf bank_mask:0xf
	v_add_f32_dpp v60, v60, v60 row_half_mirror row_mask:0xf bank_mask:0xf
	v_add_f32_dpp v61, v61, v61 row_half_mirror row_mask:0xf bank_mask:0xf
	v_add_f32_dpp v62, v62, v62 row_half_mirror row_mask:0xf bank_mask:0xf
	v_add_f32_dpp v63, v63, v63 row_half_mirror row_mask:0xf bank_mask:0xf
	v_add_f32_dpp v192, v192, v192 row_half_mirror row_mask:0xf bank_mask:0xf
	v_add_f32_dpp v194, v194, v194 row_half_mirror row_mask:0xf bank_mask:0xf
	v_add_f32_dpp v196, v196, v196 row_half_mirror row_mask:0xf bank_mask:0xf
	v_add_f32_dpp v198, v198, v198 row_half_mirror row_mask:0xf bank_mask:0xf
	v_add_f32_dpp v200, v200, v200 row_half_mirror row_mask:0xf bank_mask:0xf
	v_add_f32_dpp v202, v202, v202 row_half_mirror row_mask:0xf bank_mask:0xf
	v_add_f32_dpp v204, v204, v204 row_half_mirror row_mask:0xf bank_mask:0xf
	v_add_f32_dpp v206, v206, v206 row_half_mirror row_mask:0xf bank_mask:0xf
	v_add_f32_dpp v0, v0, v0 row_mirror row_mask:0xf bank_mask:0xf
	v_add_f32_dpp v1, v1, v1 row_mirror row_mask:0xf bank_mask:0xf
	v_add_f32_dpp v2, v2, v2 row_mirror row_mask:0xf bank_mask:0xf
	v_add_f32_dpp v3, v3, v3 row_mirror row_mask:0xf bank_mask:0xf
	v_add_f32_dpp v4, v4, v4 row_mirror row_mask:0xf bank_mask:0xf
	v_add_f32_dpp v5, v5, v5 row_mirror row_mask:0xf bank_mask:0xf
	v_add_f32_dpp v6, v6, v6 row_mirror row_mask:0xf bank_mask:0xf
	v_add_f32_dpp v7, v7, v7 row_mirror row_mask:0xf bank_mask:0xf
	v_add_f32_dpp v8, v8, v8 row_mirror row_mask:0xf bank_mask:0xf
	v_add_f32_dpp v9, v9, v9 row_mirror row_mask:0xf bank_mask:0xf
	v_add_f32_dpp v10, v10, v10 row_mirror row_mask:0xf bank_mask:0xf
	v_add_f32_dpp v11, v11, v11 row_mirror row_mask:0xf bank_mask:0xf
	v_add_f32_dpp v12, v12, v12 row_mirror row_mask:0xf bank_mask:0xf
	v_add_f32_dpp v13, v13, v13 row_mirror row_mask:0xf bank_mask:0xf
	v_add_f32_dpp v14, v14, v14 row_mirror row_mask:0xf bank_mask:0xf
	v_add_f32_dpp v15, v15, v15 row_mirror row_mask:0xf bank_mask:0xf
	v_add_f32_dpp v16, v16, v16 row_mirror row_mask:0xf bank_mask:0xf
	v_add_f32_dpp v17, v17, v17 row_mirror row_mask:0xf bank_mask:0xf
	v_add_f32_dpp v18, v18, v18 row_mirror row_mask:0xf bank_mask:0xf
	v_add_f32_dpp v19, v19, v19 row_mirror row_mask:0xf bank_mask:0xf
	v_add_f32_dpp v20, v20, v20 row_mirror row_mask:0xf bank_mask:0xf
	v_add_f32_dpp v21, v21, v21 row_mirror row_mask:0xf bank_mask:0xf
	v_add_f32_dpp v22, v22, v22 row_mirror row_mask:0xf bank_mask:0xf
	v_add_f32_dpp v23, v23, v23 row_mirror row_mask:0xf bank_mask:0xf
	v_add_f32_dpp v24, v24, v24 row_mirror row_mask:0xf bank_mask:0xf
	v_add_f32_dpp v25, v25, v25 row_mirror row_mask:0xf bank_mask:0xf
	v_add_f32_dpp v26, v26, v26 row_mirror row_mask:0xf bank_mask:0xf
	v_add_f32_dpp v27, v27, v27 row_mirror row_mask:0xf bank_mask:0xf
	v_add_f32_dpp v28, v28, v28 row_mirror row_mask:0xf bank_mask:0xf
	v_add_f32_dpp v29, v29, v29 row_mirror row_mask:0xf bank_mask:0xf
	v_add_f32_dpp v30, v30, v30 row_mirror row_mask:0xf bank_mask:0xf
	v_add_f32_dpp v31, v31, v31 row_mirror row_mask:0xf bank_mask:0xf
	v_add_f32_dpp v32, v32, v32 row_mirror row_mask:0xf bank_mask:0xf
	v_add_f32_dpp v33, v33, v33 row_mirror row_mask:0xf bank_mask:0xf
	v_add_f32_dpp v34, v34, v34 row_mirror row_mask:0xf bank_mask:0xf
	v_add_f32_dpp v35, v35, v35 row_mirror row_mask:0xf bank_mask:0xf
	v_add_f32_dpp v36, v36, v36 row_mirror row_mask:0xf bank_mask:0xf
	v_add_f32_dpp v37, v37, v37 row_mirror row_mask:0xf bank_mask:0xf
	v_add_f32_dpp v38, v38, v38 row_mirror row_mask:0xf bank_mask:0xf
	v_add_f32_dpp v39, v39, v39 row_mirror row_mask:0xf bank_mask:0xf
	v_add_f32_dpp v40, v40, v40 row_mirror row_mask:0xf bank_mask:0xf
	v_add_f32_dpp v41, v41, v41 row_mirror row_mask:0xf bank_mask:0xf
	v_add_f32_dpp v42, v42, v42 row_mirror row_mask:0xf bank_mask:0xf
	v_add_f32_dpp v43, v43, v43 row_mirror row_mask:0xf bank_mask:0xf
	v_add_f32_dpp v44, v44, v44 row_mirror row_mask:0xf bank_mask:0xf
	v_add_f32_dpp v45, v45, v45 row_mirror row_mask:0xf bank_mask:0xf
	v_add_f32_dpp v46, v46, v46 row_mirror row_mask:0xf bank_mask:0xf
	v_add_f32_dpp v47, v47, v47 row_mirror row_mask:0xf bank_mask:0xf
	v_add_f32_dpp v48, v48, v48 row_mirror row_mask:0xf bank_mask:0xf
	v_add_f32_dpp v49, v49, v49 row_mirror row_mask:0xf bank_mask:0xf
	v_add_f32_dpp v50, v50, v50 row_mirror row_mask:0xf bank_mask:0xf
	v_add_f32_dpp v51, v51, v51 row_mirror row_mask:0xf bank_mask:0xf
	v_add_f32_dpp v52, v52, v52 row_mirror row_mask:0xf bank_mask:0xf
	v_add_f32_dpp v53, v53, v53 row_mirror row_mask:0xf bank_mask:0xf
	v_add_f32_dpp v54, v54, v54 row_mirror row_mask:0xf bank_mask:0xf
; __device__ __forceinline__ float wave_sum(float v) {
; #pragma unroll
;     for (int o = 1; o < 64; o <<= 1) v += __shfl_xor(v, o);
;     return v;
; __global__ void __launch_bounds__(NTHR, 2) fwd_kernel(Args args) {
;     ...
;             for (int q = 0; q < 8; ++q) { const float sq = wave_sum(ssq[q]); const float rs = 1.0f / sqrtf(sq * (1.0f / DM) + EPS);
;                 float lg[8];
; #pragma unroll
;                 for (int e = 0; e < 8; ++e) lg[e] = wave_sum(acc[q][e]) * rs;
	v_add_f32_dpp v55, v55, v55 row_mirror row_mask:0xf bank_mask:0xf
	v_add_f32_dpp v56, v56, v56 row_mirror row_mask:0xf bank_mask:0xf
	v_add_f32_dpp v57, v57, v57 row_mirror row_mask:0xf bank_mask:0xf
	v_add_f32_dpp v58, v58, v58 row_mirror row_mask:0xf bank_mask:0xf
	v_add_f32_dpp v59, v59, v59 row_mirror row_mask:0xf bank_mask:0xf
	v_add_f32_dpp v60, v60, v60 row_mirror row_mask:0xf bank_mask:0xf
	v_add_f32_dpp v61, v61, v61 row_mirror row_mask:0xf bank_mask:0xf
	v_add_f32_dpp v62, v62, v62 row_mirror row_mask:0xf bank_mask:0xf
	v_add_f32_dpp v63, v63, v63 row_mirror row_mask:0xf bank_mask:0xf
	v_add_f32_dpp v192, v192, v192 row_mirror row_mask:0xf bank_mask:0xf
	v_add_f32_dpp v194, v194, v194 row_mirror row_mask:0xf bank_mask:0xf
	v_add_f32_dpp v196, v196, v196 row_mirror row_mask:0xf bank_mask:0xf
	v_add_f32_dpp v198, v198, v198 row_mirror row_mask:0xf bank_mask:0xf
	v_add_f32_dpp v200, v200, v200 row_mirror row_mask:0xf bank_mask:0xf
	v_add_f32_dpp v202, v202, v202 row_mirror row_mask:0xf bank_mask:0xf
	v_add_f32_dpp v204, v204, v204 row_mirror row_mask:0xf bank_mask:0xf
	v_add_f32_dpp v206, v206, v206 row_mirror row_mask:0xf bank_mask:0xf
	v_add_f32_dpp v0, v0, v0 row_bcast:15 row_mask:0xa bank_mask:0xf
	v_add_f32_dpp v1, v1, v1 row_bcast:15 row_mask:0xa bank_mask:0xf
	v_add_f32_dpp v2, v2, v2 row_bcast:15 row_mask:0xa bank_mask:0xf
	v_add_f32_dpp v3, v3, v3 row_bcast:15 row_mask:0xa bank_mask:0xf
	v_add_f32_dpp v4, v4, v4 row_bcast:15 row_mask:0xa bank_mask:0xf
	v_add_f32_dpp v5, v5, v5 row_bcast:15 row_mask:0xa bank_mask:0xf
	v_add_f32_dpp v6, v6, v6 row_bcast:15 row_mask:0xa bank_mask:0xf
	v_add_f32_dpp v7, v7, v7 row_bcast:15 row_mask:0xa bank_mask:0xf
	v_add_f32_dpp v8, v8, v8 row_bcast:15 row_mask:0xa bank_mask:0xf
	v_add_f32_dpp v9, v9, v9 row_bcast:15 row_mask:0xa bank_mask:0xf
	v_add_f32_dpp v10, v10, v10 row_bcast:15 row_mask:0xa bank_mask:0xf
	v_add_f32_dpp v11, v11, v11 row_bcast:15 row_mask:0xa bank_mask:0xf
	v_add_f32_dpp v12, v12, v12 row_bcast:15 row_mask:0xa bank_mask:0xf
	v_add_f32_dpp v13, v13, v13 row_bcast:15 row_mask:0xa bank_mask:0xf
	v_add_f32_dpp v14, v14, v14 row_bcast:15 row_mask:0xa bank_mask:0xf
	v_add_f32_dpp v15, v15, v15 row_bcast:15 row_mask:0xa bank_mask:0xf
	v_add_f32_dpp v16, v16, v16 row_bcast:15 row_mask:0xa bank_mask:0xf
	v_add_f32_dpp v17, v17, v17 row_bcast:15 row_mask:0xa bank_mask:0xf
	v_add_f32_dpp v18, v18, v18 row_bcast:15 row_mask:0xa bank_mask:0xf
	v_add_f32_dpp v19, v19, v19 row_bcast:15 row_mask:0xa bank_mask:0xf
	v_add_f32_dpp v20, v20, v20 row_bcast:15 row_mask:0xa bank_mask:0xf
	v_add_f32_dpp v21, v21, v21 row_bcast:15 row_mask:0xa bank_mask:0xf
	v_add_f32_dpp v22, v22, v22 row_bcast:15 row_mask:0xa bank_mask:0xf
	v_add_f32_dpp v23, v23, v23 row_bcast:15 row_mask:0xa bank_mask:0xf
	v_add_f32_dpp v24, v24, v24 row_bcast:15 row_mask:0xa bank_mask:0xf
	v_add_f32_dpp v25, v25, v25 row_bcast:15 row_mask:0xa bank_mask:0xf
	v_add_f32_dpp v26, v26, v26 row_bcast:15 row_mask:0xa bank_mask:0xf
	v_add_f32_dpp v27, v27, v27 row_bcast:15 row_mask:0xa bank_mask:0xf
	v_add_f32_dpp v28, v28, v28 row_bcast:15 row_mask:0xa bank_mask:0xf
	v_add_f32_dpp v29, v29, v29 row_bcast:15 row_mask:0xa bank_mask:0xf
	v_add_f32_dpp v30, v30, v30 row_bcast:15 row_mask:0xa bank_mask:0xf
	v_add_f32_dpp v31, v31, v31 row_bcast:15 row_mask:0xa bank_mask:0xf
	v_add_f32_dpp v32, v32, v32 row_bcast:15 row_mask:0xa bank_mask:0xf
	v_add_f32_dpp v33, v33, v33 row_bcast:15 row_mask:0xa bank_mask:0xf
	v_add_f32_dpp v34, v34, v34 row_bcast:15 row_mask:0xa bank_mask:0xf
	v_add_f32_dpp v35, v35, v35 row_bcast:15 row_mask:0xa bank_mask:0xf
	v_add_f32_dpp v36, v36, v36 row_bcast:15 row_mask:0xa bank_mask:0xf
	v_add_f32_dpp v37, v37, v37 row_bcast:15 row_mask:0xa bank_mask:0xf
	v_add_f32_dpp v38, v38, v38 row_bcast:15 row_mask:0xa bank_mask:0xf
	v_add_f32_dpp v39, v39, v39 row_bcast:15 row_mask:0xa bank_mask:0xf
	v_add_f32_dpp v40, v40, v40 row_bcast:15 row_mask:0xa bank_mask:0xf
	v_add_f32_dpp v41, v41, v41 row_bcast:15 row_mask:0xa bank_mask:0xf
	v_add_f32_dpp v42, v42, v42 row_bcast:15 row_mask:0xa bank_mask:0xf
	v_add_f32_dpp v43, v43, v43 row_bcast:15 row_mask:0xa bank_mask:0xf
	v_add_f32_dpp v44, v44, v44 row_bcast:15 row_mask:0xa bank_mask:0xf
	v_add_f32_dpp v45, v45, v45 row_bcast:15 row_mask:0xa bank_mask:0xf
	v_add_f32_dpp v46, v46, v46 row_bcast:15 row_mask:0xa bank_mask:0xf
	v_add_f32_dpp v47, v47, v47 row_bcast:15 row_mask:0xa bank_mask:0xf
	v_add_f32_dpp v48, v48, v48 row_bcast:15 row_mask:0xa bank_mask:0xf
	v_add_f32_dpp v49, v49, v49 row_bcast:15 row_mask:0xa bank_mask:0xf
	v_add_f32_dpp v50, v50, v50 row_bcast:15 row_mask:0xa bank_mask:0xf
	v_add_f32_dpp v51, v51, v51 row_bcast:15 row_mask:0xa bank_mask:0xf
	v_add_f32_dpp v52, v52, v52 row_bcast:15 row_mask:0xa bank_mask:0xf
	v_add_f32_dpp v53, v53, v53 row_bcast:15 row_mask:0xa bank_mask:0xf
	v_add_f32_dpp v54, v54, v54 row_bcast:15 row_mask:0xa bank_mask:0xf
	v_add_f32_dpp v55, v55, v55 row_bcast:15 row_mask:0xa bank_mask:0xf
	v_add_f32_dpp v56, v56, v56 row_bcast:15 row_mask:0xa bank_mask:0xf
	v_add_f32_dpp v57, v57, v57 row_bcast:15 row_mask:0xa bank_mask:0xf
	v_add_f32_dpp v58, v58, v58 row_bcast:15 row_mask:0xa bank_mask:0xf
	v_add_f32_dpp v59, v59, v59 row_bcast:15 row_mask:0xa bank_mask:0xf
	v_add_f32_dpp v60, v60, v60 row_bcast:15 row_mask:0xa bank_mask:0xf
	v_add_f32_dpp v61, v61, v61 row_bcast:15 row_mask:0xa bank_mask:0xf
	v_add_f32_dpp v62, v62, v62 row_bcast:15 row_mask:0xa bank_mask:0xf
	v_add_f32_dpp v63, v63, v63 row_bcast:15 row_mask:0xa bank_mask:0xf
	v_add_f32_dpp v192, v192, v192 row_bcast:15 row_mask:0xa bank_mask:0xf
; __device__ __forceinline__ float wave_sum(float v) {
; #pragma unroll
;     for (int o = 1; o < 64; o <<= 1) v += __shfl_xor(v, o);
;     return v;
; __global__ void __launch_bounds__(NTHR, 2) fwd_kernel(Args args) {
;     ...
;             for (int q = 0; q < 8; ++q) { const float sq = wave_sum(ssq[q]); const float rs = 1.0f / sqrtf(sq * (1.0f / DM) + EPS);
;                 float lg[8];
; #pragma unroll
;                 for (int e = 0; e < 8; ++e) lg[e] = wave_sum(acc[q][e]) * rs;
	v_add_f32_dpp v194, v194, v194 row_bcast:15 row_mask:0xa bank_mask:0xf
	v_add_f32_dpp v196, v196, v196 row_bcast:15 row_mask:0xa bank_mask:0xf
	v_add_f32_dpp v198, v198, v198 row_bcast:15 row_mask:0xa bank_mask:0xf
	v_add_f32_dpp v200, v200, v200 row_bcast:15 row_mask:0xa bank_mask:0xf
	v_add_f32_dpp v202, v202, v202 row_bcast:15 row_mask:0xa bank_mask:0xf
	v_add_f32_dpp v204, v204, v204 row_bcast:15 row_mask:0xa bank_mask:0xf
	v_add_f32_dpp v206, v206, v206 row_bcast:15 row_mask:0xa bank_mask:0xf
	v_add_f32_dpp v0, v0, v0 row_bcast:31 row_mask:0xc bank_mask:0xf
	v_add_f32_dpp v1, v1, v1 row_bcast:31 row_mask:0xc bank_mask:0xf
	v_add_f32_dpp v2, v2, v2 row_bcast:31 row_mask:0xc bank_mask:0xf
	v_add_f32_dpp v3, v3, v3 row_bcast:31 row_mask:0xc bank_mask:0xf
	v_add_f32_dpp v4, v4, v4 row_bcast:31 row_mask:0xc bank_mask:0xf
	v_add_f32_dpp v5, v5, v5 row_bcast:31 row_mask:0xc bank_mask:0xf
	v_add_f32_dpp v6, v6, v6 row_bcast:31 row_mask:0xc bank_mask:0xf
	v_add_f32_dpp v7, v7, v7 row_bcast:31 row_mask:0xc bank_mask:0xf
	v_add_f32_dpp v8, v8, v8 row_bcast:31 row_mask:0xc bank_mask:0xf
	v_add_f32_dpp v9, v9, v9 row_bcast:31 row_mask:0xc bank_mask:0xf
	v_add_f32_dpp v10, v10, v10 row_bcast:31 row_mask:0xc bank_mask:0xf
	v_add_f32_dpp v11, v11, v11 row_bcast:31 row_mask:0xc bank_mask:0xf
	v_add_f32_dpp v12, v12, v12 row_bcast:31 row_mask:0xc bank_mask:0xf
	v_add_f32_dpp v13, v13, v13 row_bcast:31 row_mask:0xc bank_mask:0xf
	v_add_f32_dpp v14, v14, v14 row_bcast:31 row_mask:0xc bank_mask:0xf
	v_add_f32_dpp v15, v15, v15 row_bcast:31 row_mask:0xc bank_mask:0xf
	v_add_f32_dpp v16, v16, v16 row_bcast:31 row_mask:0xc bank_mask:0xf
	v_add_f32_dpp v17, v17, v17 row_bcast:31 row_mask:0xc bank_mask:0xf
	v_add_f32_dpp v18, v18, v18 row_bcast:31 row_mask:0xc bank_mask:0xf
	v_add_f32_dpp v19, v19, v19 row_bcast:31 row_mask:0xc bank_mask:0xf
	v_add_f32_dpp v20, v20, v20 row_bcast:31 row_mask:0xc bank_mask:0xf
	v_add_f32_dpp v21, v21, v21 row_bcast:31 row_mask:0xc bank_mask:0xf
	v_add_f32_dpp v22, v22, v22 row_bcast:31 row_mask:0xc bank_mask:0xf
	v_add_f32_dpp v23, v23, v23 row_bcast:31 row_mask:0xc bank_mask:0xf
	v_add_f32_dpp v24, v24, v24 row_bcast:31 row_mask:0xc bank_mask:0xf
	v_add_f32_dpp v25, v25, v25 row_bcast:31 row_mask:0xc bank_mask:0xf
	v_add_f32_dpp v26, v26, v26 row_bcast:31 row_mask:0xc bank_mask:0xf
	v_add_f32_dpp v27, v27, v27 row_bcast:31 row_mask:0xc bank_mask:0xf
	v_add_f32_dpp v28, v28, v28 row_bcast:31 row_mask:0xc bank_mask:0xf
	v_add_f32_dpp v29, v29, v29 row_bcast:31 row_mask:0xc bank_mask:0xf
	v_add_f32_dpp v30, v30, v30 row_bcast:31 row_mask:0xc bank_mask:0xf
	v_add_f32_dpp v31, v31, v31 row_bcast:31 row_mask:0xc bank_mask:0xf
	v_add_f32_dpp v32, v32, v32 row_bcast:31 row_mask:0xc bank_mask:0xf
	v_add_f32_dpp v33, v33, v33 row_bcast:31 row_mask:0xc bank_mask:0xf
	v_add_f32_dpp v34, v34, v34 row_bcast:31 row_mask:0xc bank_mask:0xf
	v_add_f32_dpp v35, v35, v35 row_bcast:31 row_mask:0xc bank_mask:0xf
	v_add_f32_dpp v36, v36, v36 row_bcast:31 row_mask:0xc bank_mask:0xf
	v_add_f32_dpp v37, v37, v37 row_bcast:31 row_mask:0xc bank_mask:0xf
	v_add_f32_dpp v38, v38, v38 row_bcast:31 row_mask:0xc bank_mask:0xf
	v_add_f32_dpp v39, v39, v39 row_bcast:31 row_mask:0xc bank_mask:0xf
	v_add_f32_dpp v40, v40, v40 row_bcast:31 row_mask:0xc bank_mask:0xf
	v_add_f32_dpp v41, v41, v41 row_bcast:31 row_mask:0xc bank_mask:0xf
	v_add_f32_dpp v42, v42, v42 row_bcast:31 row_mask:0xc bank_mask:0xf
	v_add_f32_dpp v43, v43, v43 row_bcast:31 row_mask:0xc bank_mask:0xf
	v_add_f32_dpp v44, v44, v44 row_bcast:31 row_mask:0xc bank_mask:0xf
	v_add_f32_dpp v45, v45, v45 row_bcast:31 row_mask:0xc bank_mask:0xf
	v_add_f32_dpp v46, v46, v46 row_bcast:31 row_mask:0xc bank_mask:0xf
	v_add_f32_dpp v47, v47, v47 row_bcast:31 row_mask:0xc bank_mask:0xf
	v_add_f32_dpp v48, v48, v48 row_bcast:31 row_mask:0xc bank_mask:0xf
	v_add_f32_dpp v49, v49, v49 row_bcast:31 row_mask:0xc bank_mask:0xf
	v_add_f32_dpp v50, v50, v50 row_bcast:31 row_mask:0xc bank_mask:0xf
	v_add_f32_dpp v51, v51, v51 row_bcast:31 row_mask:0xc bank_mask:0xf
	v_add_f32_dpp v52, v52, v52 row_bcast:31 row_mask:0xc bank_mask:0xf
	v_add_f32_dpp v53, v53, v53 row_bcast:31 row_mask:0xc bank_mask:0xf
	v_add_f32_dpp v54, v54, v54 row_bcast:31 row_mask:0xc bank_mask:0xf
	v_add_f32_dpp v55, v55, v55 row_bcast:31 row_mask:0xc bank_mask:0xf
	v_add_f32_dpp v56, v56, v56 row_bcast:31 row_mask:0xc bank_mask:0xf
	v_add_f32_dpp v57, v57, v57 row_bcast:31 row_mask:0xc bank_mask:0xf
	v_add_f32_dpp v58, v58, v58 row_bcast:31 row_mask:0xc bank_mask:0xf
	v_add_f32_dpp v59, v59, v59 row_bcast:31 row_mask:0xc bank_mask:0xf
	v_add_f32_dpp v60, v60, v60 row_bcast:31 row_mask:0xc bank_mask:0xf
	v_add_f32_dpp v61, v61, v61 row_bcast:31 row_mask:0xc bank_mask:0xf
	v_add_f32_dpp v62, v62, v62 row_bcast:31 row_mask:0xc bank_mask:0xf
	v_add_f32_dpp v63, v63, v63 row_bcast:31 row_mask:0xc bank_mask:0xf
	v_add_f32_dpp v192, v192, v192 row_bcast:31 row_mask:0xc bank_mask:0xf
	v_add_f32_dpp v194, v194, v194 row_bcast:31 row_mask:0xc bank_mask:0xf
	v_add_f32_dpp v196, v196, v196 row_bcast:31 row_mask:0xc bank_mask:0xf
	v_add_f32_dpp v198, v198, v198 row_bcast:31 row_mask:0xc bank_mask:0xf
	v_add_f32_dpp v200, v200, v200 row_bcast:31 row_mask:0xc bank_mask:0xf
	v_add_f32_dpp v202, v202, v202 row_bcast:31 row_mask:0xc bank_mask:0xf
	v_add_f32_dpp v204, v204, v204 row_bcast:31 row_mask:0xc bank_mask:0xf
	v_add_f32_dpp v206, v206, v206 row_bcast:31 row_mask:0xc bank_mask:0xf
	s_lshl_b32 s22, s91, 3
	s_add_i32 s22, s22, 0x20100
	v_mov_b32_e32 v240, s22
	v_cmp_eq_u32_e32 vcc, 63, v210
	s_and_saveexec_b64 s[2:3], vcc
	ds_write_b128 v240, v[0:3] offset:0
	ds_write_b128 v240, v[4:7] offset:16
	ds_write_b32 v240, v192 offset:32
	ds_write_b128 v240, v[8:11] offset:48
	ds_write_b128 v240, v[12:15] offset:64
	ds_write_b32 v240, v194 offset:80
	ds_write_b128 v240, v[16:19] offset:96
	ds_write_b128 v240, v[20:23] offset:112
	ds_write_b32 v240, v196 offset:128
	ds_write_b128 v240, v[24:27] offset:144
	ds_write_b128 v240, v[28:31] offset:160
	ds_write_b32 v240, v198 offset:176
	ds_write_b128 v240, v[32:35] offset:192
	ds_write_b128 v240, v[36:39] offset:208
	ds_write_b32 v240, v200 offset:224
	ds_write_b128 v240, v[40:43] offset:240
	ds_write_b128 v240, v[44:47] offset:256
	ds_write_b32 v240, v202 offset:272
	ds_write_b128 v240, v[48:51] offset:288
	ds_write_b128 v240, v[52:55] offset:304
	ds_write_b32 v240, v204 offset:320
	ds_write_b128 v240, v[56:59] offset:336
	ds_write_b128 v240, v[60:63] offset:352
	ds_write_b32 v240, v206 offset:368
	s_mov_b64 exec, s[2:3]
	v_mad_u32_u24 v241, v210, 48, v240
	s_waitcnt lgkmcnt(0)
; __global__ void __launch_bounds__(NTHR, 2) fwd_kernel(Args args) {
;     ...
;             for (int q = 0; q < 8; ++q) { const float sq = wave_sum(ssq[q]); const float rs = 1.0f / sqrtf(sq * (1.0f / DM) + EPS);
;                 float lg[8];
; #pragma unroll
;                 for (int e = 0; e < 8; ++e) lg[e] = wave_sum(acc[q][e]) * rs;
;                 int i0 = 0; float v0 = lg[0];
; #pragma unroll
;                 for (int e = 1; e < 8; ++e) if (lg[e] > v0) { v0 = lg[e]; i0 = e; }
;                 int i1 = -1; float v1 = -__builtin_inff();
; #pragma unroll
;                 for (int e = 0; e < 8; ++e) if (e != i0 && lg[e] > v1) { v1 = lg[e]; i1 = e; }
;                 if (lane == 0) { const int t = t0 + q; const float w0 = 1.0f / (1.0f + expf(v1 - v0));
;                     tok_e[t] = i0 | (i1 << 8); tok_w[2 * t] = w0; tok_w[2 * t + 1] = 1.0f - w0; rstd3[t] = rs;
;                     atomicAdd((int*)&lcnt[i0], 1); atomicAdd((int*)&lcnt[i1], 1); } }
;             __syncthreads();
;             if (tid < 8) cnt_chunk[c * 8 + tid] = lcnt[tid];
	ds_read_b128 v[0:3], v241
	ds_read_b128 v[4:7], v241 offset:16
	ds_read_b32 v192, v241 offset:32
	s_waitcnt lgkmcnt(0)
	v_fmamk_f32 v232, v192, 0x3a000000, v222
	v_mul_f32_e32 v233, 0x4f800000, v232
	v_cmp_gt_f32_e32 vcc, s63, v232
	s_nop 1
	v_cndmask_b32_e32 v232, v232, v233, vcc
	v_sqrt_f32_e32 v233, v232
	s_nop 0
	v_add_u32_e32 v234, -1, v233
	v_add_u32_e32 v235, 1, v233
	v_fma_f32 v236, -v234, v233, v232
	v_fma_f32 v237, -v235, v233, v232
	v_cmp_ge_f32_e64 s[68:69], 0, v236
	s_nop 1
	v_cndmask_b32_e64 v233, v233, v234, s[68:69]
	v_cmp_lt_f32_e64 s[68:69], 0, v237
	s_nop 1
	v_cndmask_b32_e64 v233, v233, v235, s[68:69]
	v_mul_f32_e32 v234, 0x37800000, v233
	v_cndmask_b32_e32 v233, v233, v234, vcc
	v_cmp_class_f32_e32 vcc, v232, v223
	s_nop 1
	v_cndmask_b32_e32 v232, v233, v232, vcc
	v_div_scale_f32 v233, s[68:69], v232, v232, 1.0
	v_rcp_f32_e32 v234, v233
	s_nop 0
	v_fma_f32 v235, -v233, v234, 1.0
	v_fmac_f32_e32 v234, v235, v234
	v_div_scale_f32 v235, vcc, 1.0, v232, 1.0
	v_mul_f32_e32 v236, v235, v234
	v_fma_f32 v237, -v233, v236, v235
	v_fmac_f32_e32 v236, v237, v234
	v_fma_f32 v233, -v233, v236, v235
	s_nop 0
	v_div_fmas_f32 v233, v233, v234, v236
	v_div_fixup_f32 v112, v233, v232, 1.0
	v_mul_f32_e32 v0, v112, v0
	v_mul_f32_e32 v1, v112, v1
	v_mul_f32_e32 v2, v112, v2
	v_mul_f32_e32 v3, v112, v3
	v_mul_f32_e32 v4, v112, v4
	v_mul_f32_e32 v5, v112, v5
	v_mul_f32_e32 v6, v112, v6
	v_mul_f32_e32 v7, v112, v7
	v_mov_b32_e32 v238, v0
	v_mov_b32_e32 v64, 0
	v_cmp_gt_f32_e32 vcc, v1, v238
	s_nop 1
	v_cndmask_b32_e32 v238, v238, v1, vcc
	v_cndmask_b32_e64 v64, v64, 1, vcc
	v_cmp_gt_f32_e32 vcc, v2, v238
	s_nop 1
	v_cndmask_b32_e32 v238, v238, v2, vcc
	v_cndmask_b32_e64 v64, v64, 2, vcc
	v_cmp_gt_f32_e32 vcc, v3, v238
	s_nop 1
	v_cndmask_b32_e32 v238, v238, v3, vcc
	v_cndmask_b32_e64 v64, v64, 3, vcc
	v_cmp_gt_f32_e32 vcc, v4, v238
	s_nop 1
	v_cndmask_b32_e32 v238, v238, v4, vcc
	v_cndmask_b32_e64 v64, v64, 4, vcc
	v_cmp_gt_f32_e32 vcc, v5, v238
	s_nop 1
	v_cndmask_b32_e32 v238, v238, v5, vcc
	v_cndmask_b32_e64 v64, v64, 5, vcc
	v_cmp_gt_f32_e32 vcc, v6, v238
	s_nop 1
	v_cndmask_b32_e32 v238, v238, v6, vcc
	v_cndmask_b32_e64 v64, v64, 6, vcc
	v_cmp_gt_f32_e32 vcc, v7, v238
	s_nop 1
	v_cndmask_b32_e32 v238, v238, v7, vcc
	v_cndmask_b32_e64 v64, v64, 7, vcc
	v_mov_b32_e32 v239, v224
	v_mov_b32_e32 v65, -1
	v_cmp_ne_u32_e64 s[68:69], 0, v64
	v_cmp_gt_f32_e32 vcc, v0, v239
	s_and_b64 vcc, vcc, s[68:69]
	v_cndmask_b32_e32 v239, v239, v0, vcc
	v_cndmask_b32_e64 v65, v65, 0, vcc
	v_cmp_ne_u32_e64 s[68:69], 1, v64
	v_cmp_gt_f32_e32 vcc, v1, v239
	s_and_b64 vcc, vcc, s[68:69]
	v_cndmask_b32_e32 v239, v239, v1, vcc
	v_cndmask_b32_e64 v65, v65, 1, vcc
	v_cmp_ne_u32_e64 s[68:69], 2, v64
	v_cmp_gt_f32_e32 vcc, v2, v239
	s_and_b64 vcc, vcc, s[68:69]
	v_cndmask_b32_e32 v239, v239, v2, vcc
	v_cndmask_b32_e64 v65, v65, 2, vcc
	v_cmp_ne_u32_e64 s[68:69], 3, v64
	v_cmp_gt_f32_e32 vcc, v3, v239
	s_and_b64 vcc, vcc, s[68:69]
	v_cndmask_b32_e32 v239, v239, v3, vcc
	v_cndmask_b32_e64 v65, v65, 3, vcc
	v_cmp_ne_u32_e64 s[68:69], 4, v64
	v_cmp_gt_f32_e32 vcc, v4, v239
	s_and_b64 vcc, vcc, s[68:69]
	v_cndmask_b32_e32 v239, v239, v4, vcc
	v_cndmask_b32_e64 v65, v65, 4, vcc
	v_cmp_ne_u32_e64 s[68:69], 5, v64
	v_cmp_gt_f32_e32 vcc, v5, v239
	s_and_b64 vcc, vcc, s[68:69]
	v_cndmask_b32_e32 v239, v239, v5, vcc
	v_cndmask_b32_e64 v65, v65, 5, vcc
	v_cmp_ne_u32_e64 s[68:69], 6, v64
	v_cmp_gt_f32_e32 vcc, v6, v239
	s_and_b64 vcc, vcc, s[68:69]
	v_cndmask_b32_e32 v239, v239, v6, vcc
	v_cndmask_b32_e64 v65, v65, 6, vcc
	v_cmp_ne_u32_e64 s[68:69], 7, v64
	v_cmp_gt_f32_e32 vcc, v7, v239
	s_and_b64 vcc, vcc, s[68:69]
	v_cndmask_b32_e32 v239, v239, v7, vcc
	v_cndmask_b32_e64 v65, v65, 7, vcc
	v_sub_f32_e32 v232, v239, v238
	v_mul_f32_e32 v233, 0x3fb8aa3b, v232
	v_fma_f32 v234, v232, s65, -v233
	v_rndne_f32_e32 v235, v233
	v_fmac_f32_e32 v234, 0x32a5705f, v232
	v_sub_f32_e32 v233, v233, v235
	v_add_f32_e32 v233, v233, v234
	v_exp_f32_e32 v233, v233
	v_cvt_i32_f32_e32 v234, v235
	v_cmp_ngt_f32_e32 vcc, s66, v232
	v_ldexp_f32 v233, v233, v234
	s_nop 0
	v_cndmask_b32_e32 v233, 0, v233, vcc
	v_cmp_nlt_f32_e32 vcc, s67, v232
	s_nop 1
	v_cndmask_b32_e32 v232, v225, v233, vcc
	v_add_f32_e32 v232, 1.0, v232
	v_div_scale_f32 v233, s[68:69], v232, v232, 1.0
	v_rcp_f32_e32 v234, v233
	s_nop 0
	v_fma_f32 v235, -v233, v234, 1.0
	v_fmac_f32_e32 v234, v235, v234
	v_div_scale_f32 v235, vcc, 1.0, v232, 1.0
	v_mul_f32_e32 v236, v235, v234
	v_fma_f32 v237, -v233, v236, v235
	v_fmac_f32_e32 v236, v237, v234
	v_fma_f32 v233, -v233, v236, v235
	s_nop 0
	v_div_fmas_f32 v233, v233, v234, v236
	v_div_fixup_f32 v66, v233, v232, 1.0
	v_sub_f32_e32 v67, 1.0, v66
	v_lshl_add_u32 v68, v65, 8, v64
	v_add_u32_e32 v242, s13, v210
	v_lshl_add_u32 v243, v242, 2, v226
	v_lshl_add_u32 v244, v242, 3, v227
	v_lshl_add_u32 v245, v242, 2, v228
	v_lshl_add_u32 v232, v64, 2, s20
	v_lshl_add_u32 v233, v65, 2, s20
	v_cmp_gt_u32_e32 vcc, 8, v210
	s_and_saveexec_b64 s[2:3], vcc
	global_store_dword v243, v68, s[8:9]
	global_store_dwordx2 v244, v[66:67], s[8:9]
	global_store_dword v245, v112, s[8:9]
	ds_add_u32 v232, v221
	ds_add_u32 v233, v221
	s_mov_b64 exec, s[2:3]
	s_waitcnt lgkmcnt(0)
	s_barrier
	v_cmp_gt_u32_e32 vcc, 8, v211
	s_and_saveexec_b64 s[2:3], vcc
	ds_read_b32 v232, v229
	s_lshl_b32 s14, s12, 5
	v_lshl_add_u32 v233, v211, 2, s14
	v_add_u32_e32 v233, 0x392000, v233
	s_waitcnt lgkmcnt(0)
	global_store_dword v233, v232, s[8:9]
	s_mov_b64 exec, s[2:3]
	s_add_i32 s12, s12, s92
	s_cmpk_lt_i32 s12, 0x100
	s_barrier
	s_cbranch_scc1 .Lr14_chunk
